# P12 down-weight conversion: slot = (bx&15)>>1 so one column-tile group (16 WGs sharing B tiles) per XCD converts while the XCD's other group keeps running the GEMM; 3-in-flight converter
# baseline (speedup 1.0000x reference)
;     __device__ __forceinline__ void operator()(const f32x4 (&acc)[2][2][4][2], const Unit& u, int wr, int wc, int fr, int fq) const {
;         asm volatile("" : "+v"(fr), "+v"(fq));
;         const int e = blkE[u.z], c0 = u.pn * 128 + wc * 32 + 8 * fq, row0 = wr * 64 + fr;
;         const float* bg = bup + (size_t)e * 2 * FF + c0; const f32x4 g0 = *(const f32x4*)bg, g1 = *(const f32x4*)(bg + 4), l0 = *(const f32x4*)(bg + FF), l1 = *(const f32x4*)(bg + FF + 4);
;         float rsb[8];
; #pragma unroll
;         for (int q = 0; q < 8; ++q) rsb[q] = ssq[tokTab[u.pm * 256 + row0 + (q >> 2) * 128 + (q & 3) * 16]] * W8_INV;
; #pragma unroll
;         for (int ai = 0; ai < 2; ++ai)
; #pragma unroll
;             for (int m = 0; m < 4; ++m) { const int r = row0 + ai * 128 + m * 16; const float rs = rsb[ai * 4 + m];
;                 float a[8];
; #pragma unroll
;                 for (int j = 0; j < 8; ++j) { const float gb = j < 4 ? g0[j & 3] : g1[j & 3], lb = j < 4 ? l0[j & 3] : l1[j & 3];
;                     const float gl = fminf(acc[ai][0][m][j >> 2][j & 3] * rs + gb, 7.0f), ln = fminf(fmaxf(acc[ai][1][m][j >> 2][j & 3] * rs + lb, -7.0f), 7.0f);
;                     a[j] = gl * __builtin_amdgcn_rcpf(1.0f + __builtin_amdgcn_exp2f(-1.702f * 1.4426950408889634f * gl)) * (ln + 1.0f); }
;                 v2u w; w.x = pk4_fp8(a[0], a[1], a[2], a[3]); w.y = pk4_fp8(a[4], a[5], a[6], a[7]);
;                 *(v2u*)(ACT + ((size_t)u.z * 256 + r) * FF + c0) = w; }
;     __device__ __forceinline__ void done(const Unit& u) const { if (u.pm == (c & 7)) convert_share(); }
.LBB0_1534:
	s_lshl_b32 s4, s40, 7
	v_mov_b32_e32 v2, v218
	v_mov_b32_e32 v3, v219
	s_or_b32 s4, s4, s89
	v_mov_b32_e32 v0, s35
	v_lshl_add_u32 v16, v3, 3, s4
	v_readlane_b32 s0, v254, 2
	v_readlane_b32 s4, v254, 6
	s_lshl_b32 s4, s65, 10
	v_add_u32_e32 v18, s88, v2
	s_add_i32 s4, s4, 0
	v_lshl_add_u32 v2, v18, 2, s4
	v_add_u32_e32 v9, 0x20400, v2
	ds_read2_b32 v[4:5], v9 offset1:16
	ds_read_b32 v0, v0
	v_readlane_b32 s1, v254, 3
	v_ashrrev_i32_e32 v17, 31, v16
	ds_read2_b32 v[20:21], v9 offset0:160 offset1:176
	s_waitcnt lgkmcnt(0)
	v_ashrrev_i32_e32 v11, 31, v4
	v_mov_b32_e32 v10, v4
	v_lshl_add_u64 v[10:11], v[10:11], 2, s[14:15]
	global_load_dword v19, v[10:11], off
	ds_read2_b32 v[10:11], v9 offset0:32 offset1:48
	v_ashrrev_i32_e32 v13, 31, v5
	v_mov_b32_e32 v12, v5
	v_lshl_add_u64 v[4:5], v[12:13], 2, s[14:15]
	global_load_dword v24, v[4:5], off
	s_waitcnt lgkmcnt(0)
	v_ashrrev_i32_e32 v5, 31, v10
	v_mov_b32_e32 v4, v10
	v_lshl_add_u64 v[4:5], v[4:5], 2, s[14:15]
	global_load_dword v25, v[4:5], off
	ds_read2_b32 v[4:5], v9 offset0:128 offset1:144
	v_ashrrev_i32_e32 v13, 31, v11
	v_mov_b32_e32 v12, v11
	v_lshl_add_u64 v[10:11], v[12:13], 2, s[14:15]
	v_ashrrev_i32_e32 v1, 31, v0
	global_load_dword v26, v[10:11], off
	s_waitcnt lgkmcnt(0)
	v_ashrrev_i32_e32 v11, 31, v4
	v_mov_b32_e32 v10, v4
	v_lshlrev_b64 v[0:1], 14, v[0:1]
	v_lshl_add_u64 v[10:11], v[10:11], 2, s[14:15]
	v_lshl_add_u64 v[0:1], s[0:1], 0, v[0:1]
	global_load_dword v27, v[10:11], off
	v_ashrrev_i32_e32 v11, 31, v5
	v_mov_b32_e32 v10, v5
	v_lshl_add_u64 v[6:7], v[16:17], 2, v[0:1]
	v_lshl_add_u64 v[4:5], v[10:11], 2, s[14:15]
	global_load_dwordx4 v[0:3], v[6:7], off
	global_load_dword v28, v[4:5], off
	v_ashrrev_i32_e32 v5, 31, v20
	v_mov_b32_e32 v4, v20
	v_add_co_u32_e32 v8, vcc, s56, v6
	v_lshl_add_u64 v[4:5], v[4:5], 2, s[14:15]
	global_load_dword v29, v[4:5], off
	v_addc_co_u32_e32 v9, vcc, 0, v7, vcc
	global_load_dwordx4 v[8:11], v[8:9], off
	s_nop 0
	global_load_dwordx4 v[12:15], v[6:7], off offset:16
	v_readlane_b32 s5, v254, 7
	s_mov_b64 s[4:5], 0x2000
	v_ashrrev_i32_e32 v23, 31, v21
	v_lshl_add_u64 v[4:5], v[6:7], 0, s[4:5]
	global_load_dwordx4 v[4:7], v[4:5], off offset:16
	v_mov_b32_e32 v22, v21
	v_lshl_add_u64 v[20:21], v[22:23], 2, s[14:15]
	global_load_dword v20, v[20:21], off
	s_ashr_i32 s39, s38, 31
	s_lshl_b64 s[4:5], s[38:39], 19
	s_add_u32 s4, s93, s4
	s_addc_u32 s5, s87, s5
	s_bfe_u32 s0, s92, 0x30001
	s_cmp_lg_u32 s65, s0
	v_readlane_b32 s2, v254, 4
	v_readlane_b32 s3, v254, 5
	v_readlane_b32 s6, v254, 8
	v_readlane_b32 s7, v254, 9
	s_waitcnt vmcnt(0)
	v_mul_f32_e32 v19, 0x3b800000, v19
	v_mul_f32_e32 v30, 0x3b800000, v24
	v_mul_f32_e32 v25, 0x3b800000, v25
	v_mul_f32_e32 v24, 0x3b800000, v26
	v_mul_f32_e32 v23, 0x3b800000, v27
	v_fma_f32 v26, v192, v19, v0
	v_mul_f32_e32 v22, 0x3b800000, v28
	v_fma_f32 v28, v193, v19, v1
	v_min_f32_e32 v26, 0x40e00000, v26
	v_min_f32_e32 v28, 0x40e00000, v28
	v_fma_f32 v31, v194, v19, v2
	v_mul_f32_e32 v34, 0xc01d265f, v26
	v_mul_f32_e32 v35, 0xc01d265f, v28
	v_min_f32_e32 v31, 0x40e00000, v31
	v_exp_f32_e32 v34, v34
	v_exp_f32_e32 v35, v35
	v_mul_f32_e32 v36, 0xc01d265f, v31
	v_fma_f32 v33, v195, v19, v3
	v_exp_f32_e32 v36, v36
	v_min_f32_e32 v33, 0x40e00000, v33
	v_mul_f32_e32 v37, 0xc01d265f, v33
	v_add_f32_e32 v34, 1.0, v34
	v_add_f32_e32 v35, 1.0, v35
	v_exp_f32_e32 v37, v37
	v_rcp_f32_e32 v34, v34
	v_rcp_f32_e32 v35, v35
	v_add_f32_e32 v36, 1.0, v36
	v_mul_f32_e32 v21, 0x3b800000, v29
	v_fma_f32 v27, v188, v19, v8
	v_fma_f32 v29, v189, v19, v9
	v_rcp_f32_e32 v36, v36
	v_med3_f32 v27, v27, s23, v236
	v_med3_f32 v29, v29, s23, v236
	v_fma_f32 v32, v190, v19, v10
	v_add_f32_e32 v27, 1.0, v27
	v_add_f32_e32 v29, 1.0, v29
	v_add_f32_e32 v37, 1.0, v37
	v_mul_f32_e32 v26, v26, v34
	v_mul_f32_e32 v28, v28, v35
	v_med3_f32 v32, v32, s23, v236
	v_mul_f32_e32 v26, v27, v26
	v_mul_f32_e32 v27, v29, v28
	v_rcp_f32_e32 v28, v37
	v_add_f32_e32 v32, 1.0, v32
	v_mul_f32_e32 v31, v31, v36
	v_mul_f32_e32 v29, v32, v31
	v_fma_f32 v32, v184, v19, v12
	v_min_f32_e32 v32, 0x40e00000, v32
	v_mul_f32_e32 v28, v33, v28
	v_mul_f32_e32 v33, 0xc01d265f, v32
	v_exp_f32_e32 v33, v33
	v_fma_f32 v34, v185, v19, v13
	v_min_f32_e32 v34, 0x40e00000, v34
	v_mul_f32_e32 v35, 0xc01d265f, v34
	v_add_f32_e32 v33, 1.0, v33
	v_rcp_f32_e32 v33, v33
	v_exp_f32_e32 v35, v35
	v_fma_f32 v31, v191, v19, v11
	v_fma_f32 v36, v187, v19, v15
	v_mul_f32_e32 v32, v32, v33
	v_add_f32_e32 v33, 1.0, v35
	v_rcp_f32_e32 v33, v33
	v_med3_f32 v31, v31, s23, v236
	v_min_f32_e32 v36, 0x40e00000, v36
	v_add_f32_e32 v31, 1.0, v31
	v_mul_f32_e32 v33, v34, v33
	v_fma_f32 v34, v186, v19, v14
	v_min_f32_e32 v34, 0x40e00000, v34
	v_mul_f32_e32 v35, 0xc01d265f, v34
	v_exp_f32_e32 v35, v35
	v_mul_f32_e32 v37, 0xc01d265f, v36
	v_mul_f32_e32 v28, v31, v28
	v_fma_f32 v31, v180, v19, v4
	v_add_f32_e32 v35, 1.0, v35
	v_rcp_f32_e32 v35, v35
	v_exp_f32_e32 v37, v37
	v_med3_f32 v31, v31, s23, v236
	v_add_f32_e32 v31, 1.0, v31
	v_mul_f32_e32 v31, v31, v32
	v_fma_f32 v32, v181, v19, v5
	v_med3_f32 v32, v32, s23, v236
	v_mul_f32_e32 v34, v34, v35
	v_add_f32_e32 v35, 1.0, v37
	v_add_f32_e32 v32, 1.0, v32
	v_rcp_f32_e32 v35, v35
	v_mul_f32_e32 v32, v32, v33
	v_fma_f32 v33, v182, v19, v6
	v_med3_f32 v33, v33, s23, v236
	v_fma_f32 v19, v183, v19, v7
	v_add_f32_e32 v33, 1.0, v33
	v_med3_f32 v19, v19, s23, v236
	v_mul_f32_e32 v33, v33, v34
	v_mul_f32_e32 v34, v36, v35
	v_add_f32_e32 v19, 1.0, v19
	v_mul_f32_e32 v19, v19, v34
	v_med3_f32 v34, v26, s24, v237
	v_med3_f32 v27, v27, s24, v237
	v_mov_b32_e32 v26, v65
	v_cvt_pk_fp8_f32 v26, v34, v27
	v_med3_f32 v31, v31, s24, v237
	v_med3_f32 v32, v32, s24, v237
;     __device__ __forceinline__ void operator()(const f32x4 (&acc)[2][2][4][2], const Unit& u, int wr, int wc, int fr, int fq) const {
;     ...
; #pragma unroll
;         for (int ai = 0; ai < 2; ++ai)
; #pragma unroll
;             for (int m = 0; m < 4; ++m) { const int r = row0 + ai * 128 + m * 16; const float rs = rsb[ai * 4 + m];
;                 float a[8];
; #pragma unroll
;                 for (int j = 0; j < 8; ++j) { const float gb = j < 4 ? g0[j & 3] : g1[j & 3], lb = j < 4 ? l0[j & 3] : l1[j & 3];
;                     const float gl = fminf(acc[ai][0][m][j >> 2][j & 3] * rs + gb, 7.0f), ln = fminf(fmaxf(acc[ai][1][m][j >> 2][j & 3] * rs + lb, -7.0f), 7.0f);
;                     a[j] = gl * __builtin_amdgcn_rcpf(1.0f + __builtin_amdgcn_exp2f(-1.702f * 1.4426950408889634f * gl)) * (ln + 1.0f); }
;                 v2u w; w.x = pk4_fp8(a[0], a[1], a[2], a[3]); w.y = pk4_fp8(a[4], a[5], a[6], a[7]);
;                 *(v2u*)(ACT + ((size_t)u.z * 256 + r) * FF + c0) = w; }
	v_mov_b32_e32 v27, v65
	v_cvt_pk_fp8_f32 v27, v31, v32
	v_med3_f32 v29, v29, s24, v237
	v_med3_f32 v28, v28, s24, v237
	v_cvt_pk_fp8_f32 v26, v29, v28 op_sel:[0,0,1]
	v_med3_f32 v28, v33, s24, v237
	v_med3_f32 v19, v19, s24, v237
	v_cvt_pk_fp8_f32 v27, v28, v19 op_sel:[0,0,1]
	v_ashrrev_i32_e32 v19, 31, v18
	v_lshlrev_b64 v[18:19], 11, v[18:19]
	v_lshl_add_u64 v[18:19], s[4:5], 0, v[18:19]
	v_lshl_add_u64 v[16:17], v[18:19], 0, v[16:17]
	global_store_dwordx2 v[16:17], v[26:27], off
	v_fma_f32 v26, v177, v30, v1
	v_min_f32_e32 v26, 0x40e00000, v26
	v_fma_f32 v28, v176, v30, v0
	v_mul_f32_e32 v27, 0xc01d265f, v26
	v_min_f32_e32 v28, 0x40e00000, v28
	v_exp_f32_e32 v27, v27
	v_mul_f32_e32 v29, 0xc01d265f, v28
	v_exp_f32_e32 v29, v29
	v_fma_f32 v32, v169, v30, v13
	v_add_f32_e32 v27, 1.0, v27
	v_rcp_f32_e32 v27, v27
	v_add_f32_e32 v19, 1.0, v29
	v_rcp_f32_e32 v19, v19
	v_fma_f32 v29, v179, v30, v3
	v_mul_f32_e32 v26, v26, v27
	v_fma_f32 v27, v178, v30, v2
	v_min_f32_e32 v27, 0x40e00000, v27
	v_mul_f32_e32 v19, v28, v19
	v_mul_f32_e32 v28, 0xc01d265f, v27
	v_exp_f32_e32 v28, v28
	v_min_f32_e32 v29, 0x40e00000, v29
	v_mul_f32_e32 v31, 0xc01d265f, v29
	v_exp_f32_e32 v31, v31
	v_add_f32_e32 v28, 1.0, v28
	v_rcp_f32_e32 v28, v28
	v_min_f32_e32 v32, 0x40e00000, v32
	v_mul_f32_e32 v33, 0xc01d265f, v32
	v_exp_f32_e32 v33, v33
	v_mul_f32_e32 v27, v27, v28
	v_add_f32_e32 v28, 1.0, v31
	v_rcp_f32_e32 v28, v28
	v_fma_f32 v18, v172, v30, v8
	v_med3_f32 v18, v18, s23, v236
	v_add_f32_e32 v18, 1.0, v18
	v_mul_f32_e32 v28, v29, v28
	v_fma_f32 v29, v168, v30, v12
	v_min_f32_e32 v29, 0x40e00000, v29
	v_mul_f32_e32 v31, 0xc01d265f, v29
	v_exp_f32_e32 v31, v31
	v_mul_f32_e32 v18, v18, v19
	v_fma_f32 v19, v173, v30, v9
	v_med3_f32 v19, v19, s23, v236
	v_add_f32_e32 v31, 1.0, v31
	v_rcp_f32_e32 v31, v31
	v_add_f32_e32 v19, 1.0, v19
	v_mul_f32_e32 v19, v19, v26
	v_fma_f32 v26, v174, v30, v10
	v_mul_f32_e32 v29, v29, v31
	v_add_f32_e32 v31, 1.0, v33
	v_rcp_f32_e32 v31, v31
	v_med3_f32 v26, v26, s23, v236
	v_add_f32_e32 v26, 1.0, v26
	v_mul_f32_e32 v26, v26, v27
	v_mul_f32_e32 v31, v32, v31
	v_fma_f32 v32, v170, v30, v14
	v_min_f32_e32 v32, 0x40e00000, v32
	v_mul_f32_e32 v33, 0xc01d265f, v32
	v_exp_f32_e32 v33, v33
	v_fma_f32 v27, v175, v30, v11
	v_fma_f32 v34, v171, v30, v15
	v_med3_f32 v27, v27, s23, v236
	v_min_f32_e32 v34, 0x40e00000, v34
	v_add_f32_e32 v27, 1.0, v27
	v_add_f32_e32 v33, 1.0, v33
	v_mul_f32_e32 v35, 0xc01d265f, v34
	v_mul_f32_e32 v27, v27, v28
	v_fma_f32 v28, v164, v30, v4
	v_rcp_f32_e32 v33, v33
	v_exp_f32_e32 v35, v35
	v_med3_f32 v28, v28, s23, v236
	v_add_f32_e32 v28, 1.0, v28
	v_mul_f32_e32 v28, v28, v29
	v_fma_f32 v29, v165, v30, v5
	v_med3_f32 v29, v29, s23, v236
	v_mul_f32_e32 v32, v32, v33
	v_add_f32_e32 v33, 1.0, v35
	v_add_f32_e32 v29, 1.0, v29
	v_rcp_f32_e32 v33, v33
	v_mul_f32_e32 v29, v29, v31
	v_fma_f32 v31, v166, v30, v6
	v_med3_f32 v31, v31, s23, v236
	v_fma_f32 v30, v167, v30, v7
	v_add_f32_e32 v31, 1.0, v31
	v_med3_f32 v30, v30, s23, v236
	v_mul_f32_e32 v31, v31, v32
	v_mul_f32_e32 v32, v34, v33
	v_add_f32_e32 v30, 1.0, v30
	v_mul_f32_e32 v30, v30, v32
	v_med3_f32 v32, v18, s24, v237
	v_med3_f32 v19, v19, s24, v237
	v_mov_b32_e32 v18, v65
	v_cvt_pk_fp8_f32 v18, v32, v19
	v_med3_f32 v28, v28, s24, v237
	v_med3_f32 v29, v29, s24, v237
	v_mov_b32_e32 v19, v65
	v_cvt_pk_fp8_f32 v19, v28, v29
	v_med3_f32 v26, v26, s24, v237
	v_med3_f32 v27, v27, s24, v237
	v_cvt_pk_fp8_f32 v18, v26, v27 op_sel:[0,0,1]
	v_med3_f32 v26, v31, s24, v237
	v_med3_f32 v27, v30, s24, v237
	v_cvt_pk_fp8_f32 v19, v26, v27 op_sel:[0,0,1]
	v_fma_f32 v27, v160, v25, v0
	v_min_f32_e32 v28, 0x40e00000, v27
	v_add_co_u32_e32 v26, vcc, s73, v16
	v_mul_f32_e32 v27, 0xc01d265f, v28
	v_exp_f32_e32 v29, v27
	v_addc_co_u32_e32 v27, vcc, 0, v17, vcc
	global_store_dwordx2 v[26:27], v[18:19], off
	v_fma_f32 v26, v161, v25, v1
	v_min_f32_e32 v26, 0x40e00000, v26
	v_mul_f32_e32 v27, 0xc01d265f, v26
	v_exp_f32_e32 v27, v27
	v_add_f32_e32 v19, 1.0, v29
	v_rcp_f32_e32 v19, v19
	v_fma_f32 v29, v163, v25, v3
	v_add_f32_e32 v27, 1.0, v27
	v_rcp_f32_e32 v27, v27
	v_mul_f32_e32 v19, v28, v19
	v_min_f32_e32 v29, 0x40e00000, v29
	v_mul_f32_e32 v30, 0xc01d265f, v29
	v_mul_f32_e32 v26, v26, v27
	v_fma_f32 v27, v162, v25, v2
	v_min_f32_e32 v27, 0x40e00000, v27
	v_mul_f32_e32 v28, 0xc01d265f, v27
	v_exp_f32_e32 v28, v28
	v_exp_f32_e32 v30, v30
	v_fma_f32 v31, v153, v25, v13
	v_min_f32_e32 v31, 0x40e00000, v31
	v_add_f32_e32 v28, 1.0, v28
	v_rcp_f32_e32 v28, v28
	v_mul_f32_e32 v32, 0xc01d265f, v31
	v_exp_f32_e32 v32, v32
	v_fma_f32 v18, v156, v25, v8
	v_mul_f32_e32 v27, v27, v28
	v_add_f32_e32 v28, 1.0, v30
	v_rcp_f32_e32 v28, v28
	v_med3_f32 v18, v18, s23, v236
	v_add_f32_e32 v18, 1.0, v18
	v_mul_f32_e32 v18, v18, v19
	v_mul_f32_e32 v28, v29, v28
	v_fma_f32 v29, v152, v25, v12
	v_min_f32_e32 v29, 0x40e00000, v29
	v_mul_f32_e32 v30, 0xc01d265f, v29
	v_exp_f32_e32 v30, v30
	v_fma_f32 v19, v157, v25, v9
	v_med3_f32 v19, v19, s23, v236
	v_add_f32_e32 v19, 1.0, v19
	v_add_f32_e32 v30, 1.0, v30
	v_rcp_f32_e32 v30, v30
	v_mul_f32_e32 v19, v19, v26
	v_fma_f32 v26, v158, v25, v10
	v_med3_f32 v26, v26, s23, v236
	v_mul_f32_e32 v29, v29, v30
	v_add_f32_e32 v30, 1.0, v32
	v_rcp_f32_e32 v30, v30
	v_add_f32_e32 v26, 1.0, v26
	v_mul_f32_e32 v26, v26, v27
	v_fma_f32 v27, v159, v25, v11
	v_mul_f32_e32 v30, v31, v30
	v_fma_f32 v31, v154, v25, v14
	v_min_f32_e32 v31, 0x40e00000, v31
	v_mul_f32_e32 v32, 0xc01d265f, v31
	v_exp_f32_e32 v32, v32
	v_fma_f32 v33, v155, v25, v15
	v_med3_f32 v27, v27, s23, v236
	v_min_f32_e32 v33, 0x40e00000, v33
	v_add_f32_e32 v27, 1.0, v27
	v_add_f32_e32 v32, 1.0, v32
;     __device__ __forceinline__ void operator()(const f32x4 (&acc)[2][2][4][2], const Unit& u, int wr, int wc, int fr, int fq) const {
;     ...
; #pragma unroll
;         for (int ai = 0; ai < 2; ++ai)
; #pragma unroll
;             for (int m = 0; m < 4; ++m) { const int r = row0 + ai * 128 + m * 16; const float rs = rsb[ai * 4 + m];
;                 float a[8];
; #pragma unroll
;                 for (int j = 0; j < 8; ++j) { const float gb = j < 4 ? g0[j & 3] : g1[j & 3], lb = j < 4 ? l0[j & 3] : l1[j & 3];
;                     const float gl = fminf(acc[ai][0][m][j >> 2][j & 3] * rs + gb, 7.0f), ln = fminf(fmaxf(acc[ai][1][m][j >> 2][j & 3] * rs + lb, -7.0f), 7.0f);
;                     a[j] = gl * __builtin_amdgcn_rcpf(1.0f + __builtin_amdgcn_exp2f(-1.702f * 1.4426950408889634f * gl)) * (ln + 1.0f); }
;                 v2u w; w.x = pk4_fp8(a[0], a[1], a[2], a[3]); w.y = pk4_fp8(a[4], a[5], a[6], a[7]);
;                 *(v2u*)(ACT + ((size_t)u.z * 256 + r) * FF + c0) = w; }
	v_mul_f32_e32 v34, 0xc01d265f, v33
	v_mul_f32_e32 v27, v27, v28
	v_fma_f32 v28, v148, v25, v4
	v_rcp_f32_e32 v32, v32
	v_exp_f32_e32 v34, v34
	v_med3_f32 v28, v28, s23, v236
	v_add_f32_e32 v28, 1.0, v28
	v_mul_f32_e32 v28, v28, v29
	v_fma_f32 v29, v149, v25, v5
	v_med3_f32 v29, v29, s23, v236
	v_mul_f32_e32 v31, v31, v32
	v_add_f32_e32 v32, 1.0, v34
	v_add_f32_e32 v29, 1.0, v29
	v_rcp_f32_e32 v32, v32
	v_mul_f32_e32 v29, v29, v30
	v_fma_f32 v30, v150, v25, v6
	v_med3_f32 v30, v30, s23, v236
	v_fma_f32 v25, v151, v25, v7
	v_add_f32_e32 v30, 1.0, v30
	v_med3_f32 v25, v25, s23, v236
	v_mul_f32_e32 v30, v30, v31
	v_mul_f32_e32 v31, v33, v32
	v_add_f32_e32 v25, 1.0, v25
	v_mul_f32_e32 v25, v25, v31
	v_med3_f32 v31, v18, s24, v237
	v_med3_f32 v19, v19, s24, v237
	v_mov_b32_e32 v18, v65
	v_cvt_pk_fp8_f32 v18, v31, v19
	v_med3_f32 v28, v28, s24, v237
	v_med3_f32 v29, v29, s24, v237
	v_mov_b32_e32 v19, v65
	v_cvt_pk_fp8_f32 v19, v28, v29
	v_med3_f32 v26, v26, s24, v237
	v_med3_f32 v27, v27, s24, v237
	v_cvt_pk_fp8_f32 v18, v26, v27 op_sel:[0,0,1]
	v_med3_f32 v26, v30, s24, v237
	v_med3_f32 v25, v25, s24, v237
	v_cvt_pk_fp8_f32 v19, v26, v25 op_sel:[0,0,1]
	v_fma_f32 v25, v144, v24, v0
	v_min_f32_e32 v25, 0x40e00000, v25
	v_mul_f32_e32 v27, 0xc01d265f, v25
	v_add_co_u32_e32 v26, vcc, s57, v16
	v_exp_f32_e32 v28, v27
	s_nop 0
	v_addc_co_u32_e32 v27, vcc, 0, v17, vcc
	global_store_dwordx2 v[26:27], v[18:19], off
	v_fma_f32 v26, v145, v24, v1
	v_min_f32_e32 v26, 0x40e00000, v26
	v_add_f32_e32 v19, 1.0, v28
	v_mul_f32_e32 v27, 0xc01d265f, v26
	v_rcp_f32_e32 v19, v19
	v_exp_f32_e32 v27, v27
	v_fma_f32 v28, v147, v24, v3
	v_min_f32_e32 v28, 0x40e00000, v28
	v_mul_f32_e32 v19, v25, v19
	v_add_f32_e32 v25, 1.0, v27
	v_rcp_f32_e32 v25, v25
	v_mul_f32_e32 v29, 0xc01d265f, v28
	v_exp_f32_e32 v29, v29
	v_fma_f32 v30, v137, v24, v13
	v_mul_f32_e32 v25, v26, v25
	v_fma_f32 v26, v146, v24, v2
	v_min_f32_e32 v26, 0x40e00000, v26
	v_mul_f32_e32 v27, 0xc01d265f, v26
	v_exp_f32_e32 v27, v27
	v_min_f32_e32 v30, 0x40e00000, v30
	v_mul_f32_e32 v31, 0xc01d265f, v30
	v_exp_f32_e32 v31, v31
	v_add_f32_e32 v27, 1.0, v27
	v_rcp_f32_e32 v27, v27
	v_fma_f32 v18, v140, v24, v8
	v_med3_f32 v18, v18, s23, v236
	v_add_f32_e32 v18, 1.0, v18
	v_mul_f32_e32 v26, v26, v27
	v_add_f32_e32 v27, 1.0, v29
	v_rcp_f32_e32 v27, v27
	v_mul_f32_e32 v18, v18, v19
	v_fma_f32 v19, v141, v24, v9
	v_med3_f32 v19, v19, s23, v236
	v_mul_f32_e32 v27, v28, v27
	v_fma_f32 v28, v136, v24, v12
	v_min_f32_e32 v28, 0x40e00000, v28
	v_mul_f32_e32 v29, 0xc01d265f, v28
	v_exp_f32_e32 v29, v29
	v_add_f32_e32 v19, 1.0, v19
	v_mul_f32_e32 v19, v19, v25
	v_fma_f32 v25, v142, v24, v10
	v_add_f32_e32 v29, 1.0, v29
	v_rcp_f32_e32 v29, v29
	v_med3_f32 v25, v25, s23, v236
	v_add_f32_e32 v25, 1.0, v25
	v_mul_f32_e32 v25, v25, v26
	v_mul_f32_e32 v28, v28, v29
	v_add_f32_e32 v29, 1.0, v31
	v_rcp_f32_e32 v29, v29
	v_fma_f32 v26, v143, v24, v11
	v_fma_f32 v32, v139, v24, v15
	v_med3_f32 v26, v26, s23, v236
	v_mul_f32_e32 v29, v30, v29
	v_fma_f32 v30, v138, v24, v14
	v_min_f32_e32 v30, 0x40e00000, v30
	v_mul_f32_e32 v31, 0xc01d265f, v30
	v_exp_f32_e32 v31, v31
	v_min_f32_e32 v32, 0x40e00000, v32
	v_add_f32_e32 v26, 1.0, v26
	v_mul_f32_e32 v33, 0xc01d265f, v32
	v_add_f32_e32 v31, 1.0, v31
	v_mul_f32_e32 v26, v26, v27
	v_fma_f32 v27, v132, v24, v4
	v_rcp_f32_e32 v31, v31
	v_exp_f32_e32 v33, v33
	v_med3_f32 v27, v27, s23, v236
	v_add_f32_e32 v27, 1.0, v27
	v_mul_f32_e32 v27, v27, v28
	v_fma_f32 v28, v133, v24, v5
	v_med3_f32 v28, v28, s23, v236
	v_mul_f32_e32 v30, v30, v31
	v_add_f32_e32 v31, 1.0, v33
	v_add_f32_e32 v28, 1.0, v28
	v_rcp_f32_e32 v31, v31
	v_mul_f32_e32 v28, v28, v29
	v_fma_f32 v29, v134, v24, v6
	v_med3_f32 v29, v29, s23, v236
	v_fma_f32 v24, v135, v24, v7
	v_add_f32_e32 v29, 1.0, v29
	v_med3_f32 v24, v24, s23, v236
	v_mul_f32_e32 v29, v29, v30
	v_mul_f32_e32 v30, v32, v31
	v_add_f32_e32 v24, 1.0, v24
	v_mul_f32_e32 v24, v24, v30
	v_med3_f32 v30, v18, s24, v237
	v_med3_f32 v19, v19, s24, v237
	v_mov_b32_e32 v18, v65
	v_cvt_pk_fp8_f32 v18, v30, v19
	v_med3_f32 v27, v27, s24, v237
	v_med3_f32 v28, v28, s24, v237
	v_mov_b32_e32 v19, v65
	v_cvt_pk_fp8_f32 v19, v27, v28
	v_med3_f32 v25, v25, s24, v237
	v_med3_f32 v26, v26, s24, v237
	v_cvt_pk_fp8_f32 v18, v25, v26 op_sel:[0,0,1]
	v_med3_f32 v25, v29, s24, v237
	v_med3_f32 v24, v24, s24, v237
	v_cvt_pk_fp8_f32 v19, v25, v24 op_sel:[0,0,1]
	v_fma_f32 v25, v128, v23, v0
	v_min_f32_e32 v26, 0x40e00000, v25
	v_add_co_u32_e32 v24, vcc, s69, v16
	v_mul_f32_e32 v25, 0xc01d265f, v26
	v_exp_f32_e32 v27, v25
	v_addc_co_u32_e32 v25, vcc, 0, v17, vcc
	global_store_dwordx2 v[24:25], v[18:19], off
	v_fma_f32 v24, v129, v23, v1
	v_min_f32_e32 v24, 0x40e00000, v24
	v_mul_f32_e32 v25, 0xc01d265f, v24
	v_exp_f32_e32 v25, v25
	v_add_f32_e32 v19, 1.0, v27
	v_rcp_f32_e32 v19, v19
	v_fma_f32 v27, v131, v23, v3
	v_add_f32_e32 v25, 1.0, v25
	v_rcp_f32_e32 v25, v25
	v_mul_f32_e32 v19, v26, v19
	v_min_f32_e32 v27, 0x40e00000, v27
	v_mul_f32_e32 v28, 0xc01d265f, v27
	v_mul_f32_e32 v24, v24, v25
	v_fma_f32 v25, v130, v23, v2
	v_min_f32_e32 v25, 0x40e00000, v25
	v_mul_f32_e32 v26, 0xc01d265f, v25
	v_exp_f32_e32 v26, v26
	v_exp_f32_e32 v28, v28
	v_fma_f32 v29, v121, v23, v13
	v_min_f32_e32 v29, 0x40e00000, v29
	v_add_f32_e32 v26, 1.0, v26
	v_rcp_f32_e32 v26, v26
	v_mul_f32_e32 v30, 0xc01d265f, v29
	v_exp_f32_e32 v30, v30
	v_fma_f32 v18, v124, v23, v8
	v_mul_f32_e32 v25, v25, v26
	v_add_f32_e32 v26, 1.0, v28
	v_rcp_f32_e32 v26, v26
	v_med3_f32 v18, v18, s23, v236
	v_add_f32_e32 v18, 1.0, v18
	v_mul_f32_e32 v18, v18, v19
	v_mul_f32_e32 v26, v27, v26
	v_fma_f32 v27, v120, v23, v12
;     __device__ __forceinline__ void operator()(const f32x4 (&acc)[2][2][4][2], const Unit& u, int wr, int wc, int fr, int fq) const {
;     ...
; #pragma unroll
;         for (int ai = 0; ai < 2; ++ai)
; #pragma unroll
;             for (int m = 0; m < 4; ++m) { const int r = row0 + ai * 128 + m * 16; const float rs = rsb[ai * 4 + m];
;                 float a[8];
; #pragma unroll
;                 for (int j = 0; j < 8; ++j) { const float gb = j < 4 ? g0[j & 3] : g1[j & 3], lb = j < 4 ? l0[j & 3] : l1[j & 3];
;                     const float gl = fminf(acc[ai][0][m][j >> 2][j & 3] * rs + gb, 7.0f), ln = fminf(fmaxf(acc[ai][1][m][j >> 2][j & 3] * rs + lb, -7.0f), 7.0f);
;                     a[j] = gl * __builtin_amdgcn_rcpf(1.0f + __builtin_amdgcn_exp2f(-1.702f * 1.4426950408889634f * gl)) * (ln + 1.0f); }
;                 v2u w; w.x = pk4_fp8(a[0], a[1], a[2], a[3]); w.y = pk4_fp8(a[4], a[5], a[6], a[7]);
;                 *(v2u*)(ACT + ((size_t)u.z * 256 + r) * FF + c0) = w; }
	v_min_f32_e32 v27, 0x40e00000, v27
	v_mul_f32_e32 v28, 0xc01d265f, v27
	v_exp_f32_e32 v28, v28
	v_fma_f32 v19, v125, v23, v9
	v_med3_f32 v19, v19, s23, v236
	v_add_f32_e32 v19, 1.0, v19
	v_add_f32_e32 v28, 1.0, v28
	v_rcp_f32_e32 v28, v28
	v_mul_f32_e32 v19, v19, v24
	v_fma_f32 v24, v126, v23, v10
	v_med3_f32 v24, v24, s23, v236
	v_mul_f32_e32 v27, v27, v28
	v_add_f32_e32 v28, 1.0, v30
	v_rcp_f32_e32 v28, v28
	v_add_f32_e32 v24, 1.0, v24
	v_mul_f32_e32 v24, v24, v25
	v_fma_f32 v25, v127, v23, v11
	v_mul_f32_e32 v28, v29, v28
	v_fma_f32 v29, v122, v23, v14
	v_min_f32_e32 v29, 0x40e00000, v29
	v_mul_f32_e32 v30, 0xc01d265f, v29
	v_exp_f32_e32 v30, v30
	v_fma_f32 v31, v123, v23, v15
	v_med3_f32 v25, v25, s23, v236
	v_min_f32_e32 v31, 0x40e00000, v31
	v_add_f32_e32 v25, 1.0, v25
	v_add_f32_e32 v30, 1.0, v30
	v_mul_f32_e32 v32, 0xc01d265f, v31
	v_mul_f32_e32 v25, v25, v26
	v_fma_f32 v26, v116, v23, v4
	v_rcp_f32_e32 v30, v30
	v_exp_f32_e32 v32, v32
	v_med3_f32 v26, v26, s23, v236
	v_add_f32_e32 v26, 1.0, v26
	v_mul_f32_e32 v26, v26, v27
	v_fma_f32 v27, v117, v23, v5
	v_med3_f32 v27, v27, s23, v236
	v_mul_f32_e32 v29, v29, v30
	v_add_f32_e32 v30, 1.0, v32
	v_add_f32_e32 v27, 1.0, v27
	v_rcp_f32_e32 v30, v30
	v_mul_f32_e32 v27, v27, v28
	v_fma_f32 v28, v118, v23, v6
	v_med3_f32 v28, v28, s23, v236
	v_fma_f32 v23, v119, v23, v7
	v_add_f32_e32 v28, 1.0, v28
	v_med3_f32 v23, v23, s23, v236
	v_mul_f32_e32 v28, v28, v29
	v_mul_f32_e32 v29, v31, v30
	v_add_f32_e32 v23, 1.0, v23
	v_mul_f32_e32 v23, v23, v29
	v_med3_f32 v29, v18, s24, v237
	v_med3_f32 v19, v19, s24, v237
	v_mov_b32_e32 v18, v65
	v_cvt_pk_fp8_f32 v18, v29, v19
	v_med3_f32 v26, v26, s24, v237
	v_med3_f32 v27, v27, s24, v237
	v_mov_b32_e32 v19, v65
	v_cvt_pk_fp8_f32 v19, v26, v27
	v_med3_f32 v24, v24, s24, v237
	v_med3_f32 v25, v25, s24, v237
	v_cvt_pk_fp8_f32 v18, v24, v25 op_sel:[0,0,1]
	v_med3_f32 v24, v28, s24, v237
	v_med3_f32 v23, v23, s24, v237
	v_cvt_pk_fp8_f32 v19, v24, v23 op_sel:[0,0,1]
	v_fma_f32 v23, v112, v22, v0
	v_min_f32_e32 v23, 0x40e00000, v23
	s_mov_b32 s4, 0x40000
	v_mul_f32_e32 v25, 0xc01d265f, v23
	v_add_co_u32_e32 v24, vcc, s4, v16
	v_exp_f32_e32 v26, v25
	s_nop 0
	v_addc_co_u32_e32 v25, vcc, 0, v17, vcc
	global_store_dwordx2 v[24:25], v[18:19], off
	v_fma_f32 v24, v113, v22, v1
	v_min_f32_e32 v24, 0x40e00000, v24
	v_add_f32_e32 v19, 1.0, v26
	v_mul_f32_e32 v25, 0xc01d265f, v24
	v_rcp_f32_e32 v19, v19
	v_exp_f32_e32 v25, v25
	v_fma_f32 v26, v115, v22, v3
	v_min_f32_e32 v26, 0x40e00000, v26
	v_mul_f32_e32 v19, v23, v19
	v_add_f32_e32 v23, 1.0, v25
	v_rcp_f32_e32 v23, v23
	v_mul_f32_e32 v27, 0xc01d265f, v26
	v_exp_f32_e32 v27, v27
	v_fma_f32 v28, v105, v22, v13
	v_mul_f32_e32 v23, v24, v23
	v_fma_f32 v24, v114, v22, v2
	v_min_f32_e32 v24, 0x40e00000, v24
	v_mul_f32_e32 v25, 0xc01d265f, v24
	v_exp_f32_e32 v25, v25
	v_min_f32_e32 v28, 0x40e00000, v28
	v_mul_f32_e32 v29, 0xc01d265f, v28
	v_exp_f32_e32 v29, v29
	v_add_f32_e32 v25, 1.0, v25
	v_rcp_f32_e32 v25, v25
	v_fma_f32 v18, v108, v22, v8
	v_med3_f32 v18, v18, s23, v236
	v_add_f32_e32 v18, 1.0, v18
	v_mul_f32_e32 v24, v24, v25
	v_add_f32_e32 v25, 1.0, v27
	v_rcp_f32_e32 v25, v25
	v_mul_f32_e32 v18, v18, v19
	v_fma_f32 v19, v109, v22, v9
	v_med3_f32 v19, v19, s23, v236
	v_mul_f32_e32 v25, v26, v25
	v_fma_f32 v26, v104, v22, v12
	v_min_f32_e32 v26, 0x40e00000, v26
	v_mul_f32_e32 v27, 0xc01d265f, v26
	v_exp_f32_e32 v27, v27
	v_add_f32_e32 v19, 1.0, v19
	v_mul_f32_e32 v19, v19, v23
	v_fma_f32 v23, v110, v22, v10
	v_add_f32_e32 v27, 1.0, v27
	v_rcp_f32_e32 v27, v27
	v_med3_f32 v23, v23, s23, v236
	v_add_f32_e32 v23, 1.0, v23
	v_mul_f32_e32 v23, v23, v24
	v_mul_f32_e32 v26, v26, v27
	v_add_f32_e32 v27, 1.0, v29
	v_rcp_f32_e32 v27, v27
	v_fma_f32 v24, v111, v22, v11
	v_fma_f32 v30, v107, v22, v15
	v_med3_f32 v24, v24, s23, v236
	v_mul_f32_e32 v27, v28, v27
	v_fma_f32 v28, v106, v22, v14
	v_min_f32_e32 v28, 0x40e00000, v28
	v_mul_f32_e32 v29, 0xc01d265f, v28
	v_exp_f32_e32 v29, v29
	v_min_f32_e32 v30, 0x40e00000, v30
	v_add_f32_e32 v24, 1.0, v24
	v_mul_f32_e32 v31, 0xc01d265f, v30
	v_add_f32_e32 v29, 1.0, v29
	v_mul_f32_e32 v24, v24, v25
	v_fma_f32 v25, v100, v22, v4
	v_rcp_f32_e32 v29, v29
	v_exp_f32_e32 v31, v31
	v_med3_f32 v25, v25, s23, v236
	v_add_f32_e32 v25, 1.0, v25
	v_mul_f32_e32 v25, v25, v26
	v_fma_f32 v26, v101, v22, v5
	v_med3_f32 v26, v26, s23, v236
	v_mul_f32_e32 v28, v28, v29
	v_add_f32_e32 v29, 1.0, v31
	v_add_f32_e32 v26, 1.0, v26
	v_rcp_f32_e32 v29, v29
	v_mul_f32_e32 v26, v26, v27
	v_fma_f32 v27, v102, v22, v6
	v_med3_f32 v27, v27, s23, v236
	v_fma_f32 v22, v103, v22, v7
	v_add_f32_e32 v27, 1.0, v27
	v_med3_f32 v22, v22, s23, v236
	v_mul_f32_e32 v27, v27, v28
	v_mul_f32_e32 v28, v30, v29
	v_add_f32_e32 v22, 1.0, v22
	v_mul_f32_e32 v22, v22, v28
	v_med3_f32 v28, v18, s24, v237
	v_med3_f32 v19, v19, s24, v237
	v_mov_b32_e32 v18, v65
	v_cvt_pk_fp8_f32 v18, v28, v19
	v_med3_f32 v25, v25, s24, v237
	v_med3_f32 v26, v26, s24, v237
	v_mov_b32_e32 v19, v65
	v_cvt_pk_fp8_f32 v19, v25, v26
	v_med3_f32 v23, v23, s24, v237
	v_med3_f32 v24, v24, s24, v237
	v_cvt_pk_fp8_f32 v18, v23, v24 op_sel:[0,0,1]
	v_med3_f32 v23, v27, s24, v237
	v_med3_f32 v22, v22, s24, v237
	v_cvt_pk_fp8_f32 v19, v23, v22 op_sel:[0,0,1]
	v_fma_f32 v23, v96, v21, v0
	s_mov_b32 s4, 0x48000
	v_min_f32_e32 v24, 0x40e00000, v23
	v_add_co_u32_e32 v22, vcc, s4, v16
	v_mul_f32_e32 v23, 0xc01d265f, v24
	v_exp_f32_e32 v25, v23
	v_addc_co_u32_e32 v23, vcc, 0, v17, vcc
	global_store_dwordx2 v[22:23], v[18:19], off
	v_fma_f32 v22, v97, v21, v1
	v_min_f32_e32 v22, 0x40e00000, v22
	v_mul_f32_e32 v23, 0xc01d265f, v22
	v_exp_f32_e32 v23, v23
	v_add_f32_e32 v19, 1.0, v25
;     __device__ __forceinline__ void operator()(const f32x4 (&acc)[2][2][4][2], const Unit& u, int wr, int wc, int fr, int fq) const {
;     ...
; #pragma unroll
;         for (int ai = 0; ai < 2; ++ai)
; #pragma unroll
;             for (int m = 0; m < 4; ++m) { const int r = row0 + ai * 128 + m * 16; const float rs = rsb[ai * 4 + m];
;                 float a[8];
; #pragma unroll
;                 for (int j = 0; j < 8; ++j) { const float gb = j < 4 ? g0[j & 3] : g1[j & 3], lb = j < 4 ? l0[j & 3] : l1[j & 3];
;                     const float gl = fminf(acc[ai][0][m][j >> 2][j & 3] * rs + gb, 7.0f), ln = fminf(fmaxf(acc[ai][1][m][j >> 2][j & 3] * rs + lb, -7.0f), 7.0f);
;                     a[j] = gl * __builtin_amdgcn_rcpf(1.0f + __builtin_amdgcn_exp2f(-1.702f * 1.4426950408889634f * gl)) * (ln + 1.0f); }
;                 v2u w; w.x = pk4_fp8(a[0], a[1], a[2], a[3]); w.y = pk4_fp8(a[4], a[5], a[6], a[7]);
;                 *(v2u*)(ACT + ((size_t)u.z * 256 + r) * FF + c0) = w; }
;     __device__ __forceinline__ void done(const Unit& u) const { if (u.pm == (c & 7)) convert_share(); }
	v_rcp_f32_e32 v19, v19
	v_fma_f32 v25, v99, v21, v3
	v_add_f32_e32 v23, 1.0, v23
	v_rcp_f32_e32 v23, v23
	v_mul_f32_e32 v19, v24, v19
	v_min_f32_e32 v25, 0x40e00000, v25
	v_mul_f32_e32 v26, 0xc01d265f, v25
	v_mul_f32_e32 v22, v22, v23
	v_fma_f32 v23, v98, v21, v2
	v_min_f32_e32 v23, 0x40e00000, v23
	v_mul_f32_e32 v24, 0xc01d265f, v23
	v_exp_f32_e32 v24, v24
	v_exp_f32_e32 v26, v26
	v_fma_f32 v27, v89, v21, v13
	v_min_f32_e32 v27, 0x40e00000, v27
	v_add_f32_e32 v24, 1.0, v24
	v_rcp_f32_e32 v24, v24
	v_mul_f32_e32 v28, 0xc01d265f, v27
	v_exp_f32_e32 v28, v28
	v_fma_f32 v18, v92, v21, v8
	v_mul_f32_e32 v23, v23, v24
	v_add_f32_e32 v24, 1.0, v26
	v_rcp_f32_e32 v24, v24
	v_med3_f32 v18, v18, s23, v236
	v_add_f32_e32 v18, 1.0, v18
	v_mul_f32_e32 v18, v18, v19
	v_mul_f32_e32 v24, v25, v24
	v_fma_f32 v25, v88, v21, v12
	v_min_f32_e32 v25, 0x40e00000, v25
	v_mul_f32_e32 v26, 0xc01d265f, v25
	v_exp_f32_e32 v26, v26
	v_fma_f32 v19, v93, v21, v9
	v_med3_f32 v19, v19, s23, v236
	v_add_f32_e32 v19, 1.0, v19
	v_add_f32_e32 v26, 1.0, v26
	v_rcp_f32_e32 v26, v26
	v_mul_f32_e32 v19, v19, v22
	v_fma_f32 v22, v94, v21, v10
	v_med3_f32 v22, v22, s23, v236
	v_mul_f32_e32 v25, v25, v26
	v_add_f32_e32 v26, 1.0, v28
	v_rcp_f32_e32 v26, v26
	v_add_f32_e32 v22, 1.0, v22
	v_mul_f32_e32 v22, v22, v23
	v_fma_f32 v23, v95, v21, v11
	v_mul_f32_e32 v26, v27, v26
	v_fma_f32 v27, v90, v21, v14
	v_min_f32_e32 v27, 0x40e00000, v27
	v_mul_f32_e32 v28, 0xc01d265f, v27
	v_exp_f32_e32 v28, v28
	v_fma_f32 v29, v91, v21, v15
	v_med3_f32 v23, v23, s23, v236
	v_min_f32_e32 v29, 0x40e00000, v29
	v_add_f32_e32 v23, 1.0, v23
	v_add_f32_e32 v28, 1.0, v28
	v_mul_f32_e32 v30, 0xc01d265f, v29
	v_mul_f32_e32 v23, v23, v24
	v_fma_f32 v24, v84, v21, v4
	v_rcp_f32_e32 v28, v28
	v_exp_f32_e32 v30, v30
	v_med3_f32 v24, v24, s23, v236
	v_add_f32_e32 v24, 1.0, v24
	v_mul_f32_e32 v24, v24, v25
	v_fma_f32 v25, v85, v21, v5
	v_med3_f32 v25, v25, s23, v236
	v_mul_f32_e32 v27, v27, v28
	v_add_f32_e32 v28, 1.0, v30
	v_add_f32_e32 v25, 1.0, v25
	v_rcp_f32_e32 v28, v28
	v_mul_f32_e32 v25, v25, v26
	v_fma_f32 v26, v86, v21, v6
	v_med3_f32 v26, v26, s23, v236
	v_fma_f32 v21, v87, v21, v7
	v_add_f32_e32 v26, 1.0, v26
	v_med3_f32 v21, v21, s23, v236
	v_mul_f32_e32 v26, v26, v27
	v_mul_f32_e32 v27, v29, v28
	v_add_f32_e32 v21, 1.0, v21
	v_mul_f32_e32 v21, v21, v27
	v_med3_f32 v27, v18, s24, v237
	v_med3_f32 v19, v19, s24, v237
	v_mov_b32_e32 v18, v65
	v_cvt_pk_fp8_f32 v18, v27, v19
	v_med3_f32 v24, v24, s24, v237
	v_med3_f32 v25, v25, s24, v237
	v_mov_b32_e32 v19, v65
	v_cvt_pk_fp8_f32 v19, v24, v25
	v_mul_f32_e32 v20, 0x3b800000, v20
	v_med3_f32 v22, v22, s24, v237
	v_med3_f32 v23, v23, s24, v237
	v_fma_f32 v14, v74, v20, v14
	v_cvt_pk_fp8_f32 v18, v22, v23 op_sel:[0,0,1]
	v_med3_f32 v22, v26, s24, v237
	v_med3_f32 v21, v21, s24, v237
	v_min_f32_e32 v14, 0x40e00000, v14
	v_cvt_pk_fp8_f32 v19, v22, v21 op_sel:[0,0,1]
	v_mul_f32_e32 v21, 0xc01d265f, v14
	v_exp_f32_e32 v21, v21
	s_mov_b32 s4, 0x50000
	v_add_co_u32_e32 v22, vcc, s4, v16
	v_fma_f32 v13, v73, v20, v13
	s_nop 0
	v_addc_co_u32_e32 v23, vcc, 0, v17, vcc
	global_store_dwordx2 v[22:23], v[18:19], off
	v_add_f32_e32 v18, 1.0, v21
	v_rcp_f32_e32 v18, v18
	v_min_f32_e32 v13, 0x40e00000, v13
	v_fma_f32 v6, v70, v20, v6
	v_med3_f32 v6, v6, s23, v236
	v_mul_f32_e32 v14, v14, v18
	v_mul_f32_e32 v18, 0xc01d265f, v13
	v_exp_f32_e32 v18, v18
	v_add_f32_e32 v6, 1.0, v6
	v_fma_f32 v12, v72, v20, v12
	v_mul_f32_e32 v6, v6, v14
	v_add_f32_e32 v14, 1.0, v18
	v_min_f32_e32 v12, 0x40e00000, v12
	v_rcp_f32_e32 v14, v14
	v_mul_f32_e32 v18, 0xc01d265f, v12
	v_exp_f32_e32 v18, v18
	v_fma_f32 v5, v69, v20, v5
	v_med3_f32 v5, v5, s23, v236
	v_add_f32_e32 v5, 1.0, v5
	v_mul_f32_e32 v13, v13, v14
	v_mul_f32_e32 v5, v5, v13
	v_add_f32_e32 v13, 1.0, v18
	v_rcp_f32_e32 v13, v13
	v_fma_f32 v3, v83, v20, v3
	v_min_f32_e32 v3, 0x40e00000, v3
	v_fma_f32 v4, v68, v20, v4
	v_mul_f32_e32 v12, v12, v13
	v_mul_f32_e32 v13, 0xc01d265f, v3
	v_exp_f32_e32 v13, v13
	v_med3_f32 v4, v4, s23, v236
	v_add_f32_e32 v4, 1.0, v4
	v_fma_f32 v2, v82, v20, v2
	v_mul_f32_e32 v4, v4, v12
	v_add_f32_e32 v12, 1.0, v13
	v_min_f32_e32 v2, 0x40e00000, v2
	v_rcp_f32_e32 v12, v12
	v_mul_f32_e32 v13, 0xc01d265f, v2
	v_exp_f32_e32 v13, v13
	v_fma_f32 v11, v79, v20, v11
	v_med3_f32 v11, v11, s23, v236
	v_add_f32_e32 v11, 1.0, v11
	v_mul_f32_e32 v3, v3, v12
	v_mul_f32_e32 v3, v11, v3
	v_add_f32_e32 v11, 1.0, v13
	v_rcp_f32_e32 v11, v11
	v_fma_f32 v10, v78, v20, v10
	v_med3_f32 v10, v10, s23, v236
	v_fma_f32 v1, v81, v20, v1
	v_add_f32_e32 v10, 1.0, v10
	v_mul_f32_e32 v2, v2, v11
	v_min_f32_e32 v1, 0x40e00000, v1
	v_mul_f32_e32 v2, v10, v2
	v_mul_f32_e32 v10, 0xc01d265f, v1
	v_exp_f32_e32 v10, v10
	v_fmac_f32_e32 v0, v80, v20
	v_min_f32_e32 v0, 0x40e00000, v0
	v_mul_f32_e32 v11, 0xc01d265f, v0
	v_add_f32_e32 v10, 1.0, v10
	v_rcp_f32_e32 v10, v10
	v_exp_f32_e32 v11, v11
	v_fma_f32 v9, v77, v20, v9
	v_med3_f32 v9, v9, s23, v236
	v_fmac_f32_e32 v15, v75, v20
	v_add_f32_e32 v9, 1.0, v9
	v_mul_f32_e32 v1, v1, v10
	v_min_f32_e32 v10, 0x40e00000, v15
	v_mul_f32_e32 v1, v9, v1
	v_add_f32_e32 v9, 1.0, v11
	v_mul_f32_e32 v11, 0xc01d265f, v10
	v_rcp_f32_e32 v9, v9
	v_exp_f32_e32 v11, v11
	v_fmac_f32_e32 v8, v76, v20
	v_med3_f32 v8, v8, s23, v236
	v_mul_f32_e32 v0, v0, v9
	v_add_f32_e32 v9, 1.0, v11
	v_rcp_f32_e32 v9, v9
	v_fmac_f32_e32 v7, v71, v20
	v_add_f32_e32 v8, 1.0, v8
	v_med3_f32 v7, v7, s23, v236
	v_mul_f32_e32 v0, v8, v0
	v_mul_f32_e32 v8, v10, v9
	v_add_f32_e32 v7, 1.0, v7
	v_mul_f32_e32 v7, v7, v8
	v_med3_f32 v8, v0, s24, v237
	v_med3_f32 v1, v1, s24, v237
	v_mov_b32_e32 v0, v65
	v_cvt_pk_fp8_f32 v0, v8, v1
	v_med3_f32 v4, v4, s24, v237
	v_med3_f32 v5, v5, s24, v237
	v_mov_b32_e32 v1, v65
	v_cvt_pk_fp8_f32 v1, v4, v5
	v_med3_f32 v2, v2, s24, v237
	v_med3_f32 v3, v3, s24, v237
	v_cvt_pk_fp8_f32 v0, v2, v3 op_sel:[0,0,1]
	v_med3_f32 v2, v6, s24, v237
	v_med3_f32 v3, v7, s24, v237
	v_cvt_pk_fp8_f32 v1, v2, v3 op_sel:[0,0,1]
	v_add_co_u32_e32 v2, vcc, 0x58000, v16
	s_nop 1
	v_addc_co_u32_e32 v3, vcc, 0, v17, vcc
	global_store_dwordx2 v[2:3], v[0:1], off
	s_cbranch_scc1 .LBB0_1541
; __device__ __forceinline__ int lane_id_now() { unsigned z = 0u; asm volatile("" : "+v"(z)); return (int)__builtin_amdgcn_mbcnt_hi(~0u, __builtin_amdgcn_mbcnt_lo(~0u, z)); }
; #define GAS __attribute__((address_space(1)))
; template <bool GAIN, bool NT = false> __device__ __forceinline__ void titem8_load(const TItem& d, int lane, f32x4 (&r)[16], f32x4 (&g)[4]) {
;     const int q = lane & 7, kg = lane >> 3; const unsigned lo = (unsigned)((16 * kg) * d.N + 4 * q) * 4u;
;     const GAS char* base = (const GAS char*)d.src;
; #pragma unroll
;     for (int j = 0; j < 16; ++j) { const GAS f32x4* p = (const GAS f32x4*)(base + (size_t)j * (size_t)d.N * 4 + lo); r[j] = NT ? __builtin_nontemporal_load(p) : *p; }
;     if constexpr (GAIN) { const GAS char* gb = (const GAS char*)d.gain; const unsigned go = (unsigned)(16 * kg) * 4u;
; #pragma unroll
;         for (int j4 = 0; j4 < 4; ++j4) g[j4] = *(const GAS f32x4*)(gb + 16 * j4 + go); }
;     asm volatile("" ::: "memory"); __builtin_amdgcn_sched_barrier(0);
; }
;     __device__ __forceinline__ void convert_share() const {
;         const int lane = lane_id_now(), gw = c * NWAVES + wave, NGW = G * NWAVES;
;         constexpr int NIT = E * (FF / 128) * (D / 32);
;         TSTREAM(NIT, dec_dn, TI8L_NT, TI8S_NT);
	v_readlane_b32 s0, v254, 26
	v_readlane_b32 s1, v254, 27
	v_mov_b32_e32 v0, v65
	s_andn2_b64 vcc, exec, s[0:1]
	s_cbranch_vccnz .LBB0_1541
	v_mbcnt_lo_u32_b32 v64, -1, 0
	v_mbcnt_hi_u32_b32 v64, -1, v64
	v_and_b32_e32 v194, 7, v64
	v_lshrrev_b32_e32 v195, 3, v64
	v_lshlrev_b32_e32 v246, 17, v195
	v_lshl_or_b32 v246, v194, 4, v246
	v_add_u32_e32 v247, 0x2000, v246
	v_add_u32_e32 v248, 0x4000, v246
	v_add_u32_e32 v249, 0x6000, v246
	v_lshlrev_b32_e32 v250, 13, v194
	v_lshl_or_b32 v250, v195, 4, v250
	v_add_u32_e32 v251, 0x1000, v250
	v_readlane_b32 s0, v254, 60
	v_readlane_b32 s4, v254, 4
	v_readlane_b32 s5, v254, 5
	s_nop 3
	s_lshl_b32 s1, s92, 3
	s_add_i32 s0, s0, s1
	s_lshr_b32 s1, s0, 10
	s_and_b32 s0, s0, 0x3ff
	s_lshr_b32 s2, s0, 6
	s_and_b32 s0, s0, 63
	s_lshl_b32 s35, s1, 24
	s_lshl_b32 s38, s2, 20
	s_add_i32 s35, s35, s38
	s_lshl_b32 s38, s0, 7
	s_add_i32 s35, s35, s38
	s_add_u32 s4, s4, s35
	s_addc_u32 s5, s5, 0
	s_add_u32 s6, s4, 0x8000
	s_addc_u32 s7, s5, 0
	s_add_u32 s8, s4, 0x10000
	s_addc_u32 s9, s5, 0
	s_add_u32 s38, s4, 0x18000
	s_addc_u32 s39, s5, 0
	s_lshl_b32 s35, s1, 22
	s_lshl_b32 s40, s0, 16
	s_add_i32 s35, s35, s40
	s_lshl_b32 s40, s2, 7
	s_add_i32 s35, s35, s40
	s_add_u32 s42, s78, 0x57dc8000
	s_addc_u32 s43, s79, 0
	s_add_u32 s42, s42, s35
	s_addc_u32 s43, s43, 0
	global_load_dwordx4 v[0:3], v246, s[4:5] nt
	global_load_dwordx4 v[4:7], v247, s[4:5] nt
	global_load_dwordx4 v[8:11], v248, s[4:5] nt
	global_load_dwordx4 v[12:15], v249, s[4:5] nt
	global_load_dwordx4 v[16:19], v246, s[6:7] nt
	global_load_dwordx4 v[20:23], v247, s[6:7] nt
	global_load_dwordx4 v[24:27], v248, s[6:7] nt
	global_load_dwordx4 v[28:31], v249, s[6:7] nt
	global_load_dwordx4 v[32:35], v246, s[8:9] nt
	global_load_dwordx4 v[36:39], v247, s[8:9] nt
	global_load_dwordx4 v[40:43], v248, s[8:9] nt
	global_load_dwordx4 v[44:47], v249, s[8:9] nt
	global_load_dwordx4 v[48:51], v246, s[38:39] nt
	global_load_dwordx4 v[52:55], v247, s[38:39] nt
	global_load_dwordx4 v[56:59], v248, s[38:39] nt
	global_load_dwordx4 v[60:63], v249, s[38:39] nt
	s_add_u32 s4, s4, 0x2000000
	s_addc_u32 s5, s5, 0
	s_add_u32 s6, s6, 0x2000000
	s_addc_u32 s7, s7, 0
	s_add_u32 s8, s8, 0x2000000
	s_addc_u32 s9, s9, 0
	s_add_u32 s38, s38, 0x2000000
	s_addc_u32 s39, s39, 0
	global_load_dwordx4 v[66:69], v246, s[4:5] nt
	global_load_dwordx4 v[70:73], v247, s[4:5] nt
	global_load_dwordx4 v[74:77], v248, s[4:5] nt
	global_load_dwordx4 v[78:81], v249, s[4:5] nt
	global_load_dwordx4 v[82:85], v246, s[6:7] nt
	global_load_dwordx4 v[86:89], v247, s[6:7] nt
	global_load_dwordx4 v[90:93], v248, s[6:7] nt
	global_load_dwordx4 v[94:97], v249, s[6:7] nt
	global_load_dwordx4 v[98:101], v246, s[8:9] nt
	global_load_dwordx4 v[102:105], v247, s[8:9] nt
	global_load_dwordx4 v[106:109], v248, s[8:9] nt
	global_load_dwordx4 v[110:113], v249, s[8:9] nt
	global_load_dwordx4 v[114:117], v246, s[38:39] nt
	global_load_dwordx4 v[118:121], v247, s[38:39] nt
	global_load_dwordx4 v[122:125], v248, s[38:39] nt
	global_load_dwordx4 v[126:129], v249, s[38:39] nt
	s_add_u32 s4, s4, 0x2000000
	s_addc_u32 s5, s5, 0
	s_add_u32 s6, s6, 0x2000000
	s_addc_u32 s7, s7, 0
	s_add_u32 s8, s8, 0x2000000
	s_addc_u32 s9, s9, 0
	s_add_u32 s38, s38, 0x2000000
	s_addc_u32 s39, s39, 0
	global_load_dwordx4 v[130:133], v246, s[4:5] nt
	global_load_dwordx4 v[134:137], v247, s[4:5] nt
	global_load_dwordx4 v[138:141], v248, s[4:5] nt
	global_load_dwordx4 v[142:145], v249, s[4:5] nt
	global_load_dwordx4 v[146:149], v246, s[6:7] nt
	global_load_dwordx4 v[150:153], v247, s[6:7] nt
	global_load_dwordx4 v[154:157], v248, s[6:7] nt
	global_load_dwordx4 v[158:161], v249, s[6:7] nt
	global_load_dwordx4 v[162:165], v246, s[8:9] nt
	global_load_dwordx4 v[166:169], v247, s[8:9] nt
	global_load_dwordx4 v[170:173], v248, s[8:9] nt
	global_load_dwordx4 v[174:177], v249, s[8:9] nt
	global_load_dwordx4 v[178:181], v246, s[38:39] nt
	global_load_dwordx4 v[182:185], v247, s[38:39] nt
	global_load_dwordx4 v[186:189], v248, s[38:39] nt
	global_load_dwordx4 v[190:193], v249, s[38:39] nt
	s_add_u32 s4, s4, 0x2000000
	s_addc_u32 s5, s5, 0
	s_add_u32 s6, s6, 0x2000000
	s_addc_u32 s7, s7, 0
	s_add_u32 s8, s8, 0x2000000
	s_addc_u32 s9, s9, 0
	s_add_u32 s38, s38, 0x2000000
	s_addc_u32 s39, s39, 0
	s_waitcnt vmcnt(32)
; #define GAS __attribute__((address_space(1)))
; template <bool GAIN, bool NT = false> __device__ __forceinline__ void titem8_load(const TItem& d, int lane, f32x4 (&r)[16], f32x4 (&g)[4]) {
;     const int q = lane & 7, kg = lane >> 3; const unsigned lo = (unsigned)((16 * kg) * d.N + 4 * q) * 4u;
;     const GAS char* base = (const GAS char*)d.src;
; #pragma unroll
;     for (int j = 0; j < 16; ++j) { const GAS f32x4* p = (const GAS f32x4*)(base + (size_t)j * (size_t)d.N * 4 + lo); r[j] = NT ? __builtin_nontemporal_load(p) : *p; }
;     if constexpr (GAIN) { const GAS char* gb = (const GAS char*)d.gain; const unsigned go = (unsigned)(16 * kg) * 4u;
; #pragma unroll
;         for (int j4 = 0; j4 < 4; ++j4) g[j4] = *(const GAS f32x4*)(gb + 16 * j4 + go); }
;     asm volatile("" ::: "memory"); __builtin_amdgcn_sched_barrier(0);
; }
; template <bool GAIN, bool NT = false> __device__ __forceinline__ void titem8_store(const TItem& d, int lane, const f32x4 (&r)[16], const f32x4 (&g)[4]) {
;     const int q = lane & 7, kg = lane >> 3; const unsigned lo = (unsigned)((4 * q) * d.ldk + 16 * kg);
;     GAS char* base = (GAS char*)d.dst;
;     f32x4 s[16];
; #pragma unroll
;     for (int j = 0; j < 16; ++j) s[j] = r[j] * ((GAIN ? g[j >> 2][j & 3] : 1.0f) * W8_SCALE);
; #pragma unroll
;     for (int i = 0; i < 4; ++i) { v4u w;
;         w.x = pk4_fp8w(s[0][i], s[1][i], s[2][i], s[3][i]); w.y = pk4_fp8w(s[4][i], s[5][i], s[6][i], s[7][i]);
;         w.z = pk4_fp8w(s[8][i], s[9][i], s[10][i], s[11][i]); w.w = pk4_fp8w(s[12][i], s[13][i], s[14][i], s[15][i]);
;         GAS v4u* p = (GAS v4u*)(base + (size_t)i * (size_t)d.ldk + lo);
;         if (NT) __builtin_nontemporal_store(w, p); else *p = w; }
; }
	v_pk_mul_f32 v[0:1], v[0:1], s[30:31] op_sel_hi:[1,0]
	v_pk_mul_f32 v[2:3], v[2:3], s[30:31] op_sel_hi:[1,0]
	v_pk_mul_f32 v[4:5], v[4:5], s[30:31] op_sel_hi:[1,0]
	v_pk_mul_f32 v[6:7], v[6:7], s[30:31] op_sel_hi:[1,0]
	v_pk_mul_f32 v[8:9], v[8:9], s[30:31] op_sel_hi:[1,0]
	v_pk_mul_f32 v[10:11], v[10:11], s[30:31] op_sel_hi:[1,0]
	v_pk_mul_f32 v[12:13], v[12:13], s[30:31] op_sel_hi:[1,0]
	v_pk_mul_f32 v[14:15], v[14:15], s[30:31] op_sel_hi:[1,0]
	v_pk_mul_f32 v[16:17], v[16:17], s[30:31] op_sel_hi:[1,0]
	v_pk_mul_f32 v[18:19], v[18:19], s[30:31] op_sel_hi:[1,0]
	v_pk_mul_f32 v[20:21], v[20:21], s[30:31] op_sel_hi:[1,0]
	v_pk_mul_f32 v[22:23], v[22:23], s[30:31] op_sel_hi:[1,0]
	v_pk_mul_f32 v[24:25], v[24:25], s[30:31] op_sel_hi:[1,0]
	v_pk_mul_f32 v[26:27], v[26:27], s[30:31] op_sel_hi:[1,0]
	v_pk_mul_f32 v[28:29], v[28:29], s[30:31] op_sel_hi:[1,0]
	v_pk_mul_f32 v[30:31], v[30:31], s[30:31] op_sel_hi:[1,0]
	v_pk_mul_f32 v[32:33], v[32:33], s[30:31] op_sel_hi:[1,0]
	v_pk_mul_f32 v[34:35], v[34:35], s[30:31] op_sel_hi:[1,0]
	v_pk_mul_f32 v[36:37], v[36:37], s[30:31] op_sel_hi:[1,0]
	v_pk_mul_f32 v[38:39], v[38:39], s[30:31] op_sel_hi:[1,0]
	v_pk_mul_f32 v[40:41], v[40:41], s[30:31] op_sel_hi:[1,0]
	v_pk_mul_f32 v[42:43], v[42:43], s[30:31] op_sel_hi:[1,0]
	v_pk_mul_f32 v[44:45], v[44:45], s[30:31] op_sel_hi:[1,0]
	v_pk_mul_f32 v[46:47], v[46:47], s[30:31] op_sel_hi:[1,0]
	v_pk_mul_f32 v[48:49], v[48:49], s[30:31] op_sel_hi:[1,0]
	v_pk_mul_f32 v[50:51], v[50:51], s[30:31] op_sel_hi:[1,0]
	v_pk_mul_f32 v[52:53], v[52:53], s[30:31] op_sel_hi:[1,0]
	v_pk_mul_f32 v[54:55], v[54:55], s[30:31] op_sel_hi:[1,0]
	v_pk_mul_f32 v[56:57], v[56:57], s[30:31] op_sel_hi:[1,0]
	v_pk_mul_f32 v[58:59], v[58:59], s[30:31] op_sel_hi:[1,0]
	v_pk_mul_f32 v[60:61], v[60:61], s[30:31] op_sel_hi:[1,0]
	v_pk_mul_f32 v[62:63], v[62:63], s[30:31] op_sel_hi:[1,0]
	v_med3_f32 v0, v0, s24, v237
	v_med3_f32 v1, v1, s24, v237
	v_med3_f32 v2, v2, s24, v237
	v_med3_f32 v3, v3, s24, v237
	v_med3_f32 v4, v4, s24, v237
	v_med3_f32 v5, v5, s24, v237
	v_med3_f32 v6, v6, s24, v237
	v_med3_f32 v7, v7, s24, v237
	v_med3_f32 v8, v8, s24, v237
	v_med3_f32 v9, v9, s24, v237
	v_med3_f32 v10, v10, s24, v237
	v_med3_f32 v11, v11, s24, v237
	v_med3_f32 v12, v12, s24, v237
	v_med3_f32 v13, v13, s24, v237
	v_med3_f32 v14, v14, s24, v237
	v_med3_f32 v15, v15, s24, v237
	v_med3_f32 v16, v16, s24, v237
	v_med3_f32 v17, v17, s24, v237
	v_med3_f32 v18, v18, s24, v237
	v_med3_f32 v19, v19, s24, v237
	v_med3_f32 v20, v20, s24, v237
	v_med3_f32 v21, v21, s24, v237
	v_med3_f32 v22, v22, s24, v237
	v_med3_f32 v23, v23, s24, v237
	v_med3_f32 v24, v24, s24, v237
	v_med3_f32 v25, v25, s24, v237
	v_med3_f32 v26, v26, s24, v237
	v_med3_f32 v27, v27, s24, v237
	v_med3_f32 v28, v28, s24, v237
	v_med3_f32 v29, v29, s24, v237
	v_med3_f32 v30, v30, s24, v237
	v_med3_f32 v31, v31, s24, v237
	v_med3_f32 v32, v32, s24, v237
	v_med3_f32 v33, v33, s24, v237
	v_med3_f32 v34, v34, s24, v237
	v_med3_f32 v35, v35, s24, v237
	v_med3_f32 v36, v36, s24, v237
	v_med3_f32 v37, v37, s24, v237
	v_med3_f32 v38, v38, s24, v237
	v_med3_f32 v39, v39, s24, v237
	v_med3_f32 v40, v40, s24, v237
	v_med3_f32 v41, v41, s24, v237
	v_med3_f32 v42, v42, s24, v237
	v_med3_f32 v43, v43, s24, v237
	v_med3_f32 v44, v44, s24, v237
	v_med3_f32 v45, v45, s24, v237
	v_med3_f32 v46, v46, s24, v237
	v_med3_f32 v47, v47, s24, v237
	v_med3_f32 v48, v48, s24, v237
	v_med3_f32 v49, v49, s24, v237
	v_med3_f32 v50, v50, s24, v237
	v_med3_f32 v51, v51, s24, v237
	v_med3_f32 v52, v52, s24, v237
	v_med3_f32 v53, v53, s24, v237
	v_med3_f32 v54, v54, s24, v237
	v_med3_f32 v55, v55, s24, v237
	v_med3_f32 v56, v56, s24, v237
	v_med3_f32 v57, v57, s24, v237
	v_med3_f32 v58, v58, s24, v237
	v_med3_f32 v59, v59, s24, v237
	v_med3_f32 v60, v60, s24, v237
	v_med3_f32 v61, v61, s24, v237
	v_med3_f32 v62, v62, s24, v237
	v_med3_f32 v63, v63, s24, v237
	v_cvt_pk_fp8_f32 v0, v0, v4
	v_cvt_pk_fp8_f32 v0, v8, v12 op_sel:[0,0,1]
	v_cvt_pk_fp8_f32 v4, v1, v5
	v_cvt_pk_fp8_f32 v4, v9, v13 op_sel:[0,0,1]
	v_cvt_pk_fp8_f32 v8, v2, v6
	v_cvt_pk_fp8_f32 v8, v10, v14 op_sel:[0,0,1]
	v_cvt_pk_fp8_f32 v12, v3, v7
	v_cvt_pk_fp8_f32 v12, v11, v15 op_sel:[0,0,1]
	v_cvt_pk_fp8_f32 v1, v16, v20
	v_cvt_pk_fp8_f32 v1, v24, v28 op_sel:[0,0,1]
	v_cvt_pk_fp8_f32 v5, v17, v21
	v_cvt_pk_fp8_f32 v5, v25, v29 op_sel:[0,0,1]
	v_cvt_pk_fp8_f32 v9, v18, v22
	v_cvt_pk_fp8_f32 v9, v26, v30 op_sel:[0,0,1]
	v_cvt_pk_fp8_f32 v13, v19, v23
	v_cvt_pk_fp8_f32 v13, v27, v31 op_sel:[0,0,1]
	v_cvt_pk_fp8_f32 v2, v32, v36
	v_cvt_pk_fp8_f32 v2, v40, v44 op_sel:[0,0,1]
	v_cvt_pk_fp8_f32 v6, v33, v37
	v_cvt_pk_fp8_f32 v6, v41, v45 op_sel:[0,0,1]
	v_cvt_pk_fp8_f32 v10, v34, v38
	v_cvt_pk_fp8_f32 v10, v42, v46 op_sel:[0,0,1]
	v_cvt_pk_fp8_f32 v14, v35, v39
	v_cvt_pk_fp8_f32 v14, v43, v47 op_sel:[0,0,1]
	v_cvt_pk_fp8_f32 v3, v48, v52
	v_cvt_pk_fp8_f32 v3, v56, v60 op_sel:[0,0,1]
	v_cvt_pk_fp8_f32 v7, v49, v53
	v_cvt_pk_fp8_f32 v7, v57, v61 op_sel:[0,0,1]
	v_cvt_pk_fp8_f32 v11, v50, v54
	v_cvt_pk_fp8_f32 v11, v58, v62 op_sel:[0,0,1]
	v_cvt_pk_fp8_f32 v15, v51, v55
	v_cvt_pk_fp8_f32 v15, v59, v63 op_sel:[0,0,1]
	global_store_dwordx4 v250, v[0:3], s[42:43] nt
	global_store_dwordx4 v250, v[4:7], s[42:43] offset:2048 nt
	global_store_dwordx4 v251, v[8:11], s[42:43] nt
	global_store_dwordx4 v251, v[12:15], s[42:43] offset:2048 nt
	s_add_u32 s42, s42, 0x800000
	s_addc_u32 s43, s43, 0
	global_load_dwordx4 v[0:3], v246, s[4:5] nt
	global_load_dwordx4 v[4:7], v247, s[4:5] nt
	global_load_dwordx4 v[8:11], v248, s[4:5] nt
	global_load_dwordx4 v[12:15], v249, s[4:5] nt
	global_load_dwordx4 v[16:19], v246, s[6:7] nt
	global_load_dwordx4 v[20:23], v247, s[6:7] nt
	global_load_dwordx4 v[24:27], v248, s[6:7] nt
	global_load_dwordx4 v[28:31], v249, s[6:7] nt
	global_load_dwordx4 v[32:35], v246, s[8:9] nt
	global_load_dwordx4 v[36:39], v247, s[8:9] nt
	global_load_dwordx4 v[40:43], v248, s[8:9] nt
	global_load_dwordx4 v[44:47], v249, s[8:9] nt
	global_load_dwordx4 v[48:51], v246, s[38:39] nt
	global_load_dwordx4 v[52:55], v247, s[38:39] nt
	global_load_dwordx4 v[56:59], v248, s[38:39] nt
	global_load_dwordx4 v[60:63], v249, s[38:39] nt
	s_add_u32 s4, s4, 0x2000000
	s_addc_u32 s5, s5, 0
	s_add_u32 s6, s6, 0x2000000
	s_addc_u32 s7, s7, 0
	s_add_u32 s8, s8, 0x2000000
	s_addc_u32 s9, s9, 0
	s_add_u32 s38, s38, 0x2000000
	s_addc_u32 s39, s39, 0
	s_waitcnt vmcnt(36)
; #define GAS __attribute__((address_space(1)))
; template <bool GAIN, bool NT = false> __device__ __forceinline__ void titem8_load(const TItem& d, int lane, f32x4 (&r)[16], f32x4 (&g)[4]) {
;     const int q = lane & 7, kg = lane >> 3; const unsigned lo = (unsigned)((16 * kg) * d.N + 4 * q) * 4u;
;     const GAS char* base = (const GAS char*)d.src;
; #pragma unroll
;     for (int j = 0; j < 16; ++j) { const GAS f32x4* p = (const GAS f32x4*)(base + (size_t)j * (size_t)d.N * 4 + lo); r[j] = NT ? __builtin_nontemporal_load(p) : *p; }
;     if constexpr (GAIN) { const GAS char* gb = (const GAS char*)d.gain; const unsigned go = (unsigned)(16 * kg) * 4u;
; #pragma unroll
;         for (int j4 = 0; j4 < 4; ++j4) g[j4] = *(const GAS f32x4*)(gb + 16 * j4 + go); }
;     asm volatile("" ::: "memory"); __builtin_amdgcn_sched_barrier(0);
; }
; template <bool GAIN, bool NT = false> __device__ __forceinline__ void titem8_store(const TItem& d, int lane, const f32x4 (&r)[16], const f32x4 (&g)[4]) {
;     const int q = lane & 7, kg = lane >> 3; const unsigned lo = (unsigned)((4 * q) * d.ldk + 16 * kg);
;     GAS char* base = (GAS char*)d.dst;
;     f32x4 s[16];
; #pragma unroll
;     for (int j = 0; j < 16; ++j) s[j] = r[j] * ((GAIN ? g[j >> 2][j & 3] : 1.0f) * W8_SCALE);
; #pragma unroll
;     for (int i = 0; i < 4; ++i) { v4u w;
;         w.x = pk4_fp8w(s[0][i], s[1][i], s[2][i], s[3][i]); w.y = pk4_fp8w(s[4][i], s[5][i], s[6][i], s[7][i]);
;         w.z = pk4_fp8w(s[8][i], s[9][i], s[10][i], s[11][i]); w.w = pk4_fp8w(s[12][i], s[13][i], s[14][i], s[15][i]);
;         GAS v4u* p = (GAS v4u*)(base + (size_t)i * (size_t)d.ldk + lo);
;         if (NT) __builtin_nontemporal_store(w, p); else *p = w; }
; }
	v_pk_mul_f32 v[66:67], v[66:67], s[30:31] op_sel_hi:[1,0]
	v_pk_mul_f32 v[68:69], v[68:69], s[30:31] op_sel_hi:[1,0]
	v_pk_mul_f32 v[70:71], v[70:71], s[30:31] op_sel_hi:[1,0]
	v_pk_mul_f32 v[72:73], v[72:73], s[30:31] op_sel_hi:[1,0]
	v_pk_mul_f32 v[74:75], v[74:75], s[30:31] op_sel_hi:[1,0]
	v_pk_mul_f32 v[76:77], v[76:77], s[30:31] op_sel_hi:[1,0]
	v_pk_mul_f32 v[78:79], v[78:79], s[30:31] op_sel_hi:[1,0]
	v_pk_mul_f32 v[80:81], v[80:81], s[30:31] op_sel_hi:[1,0]
	v_pk_mul_f32 v[82:83], v[82:83], s[30:31] op_sel_hi:[1,0]
	v_pk_mul_f32 v[84:85], v[84:85], s[30:31] op_sel_hi:[1,0]
	v_pk_mul_f32 v[86:87], v[86:87], s[30:31] op_sel_hi:[1,0]
	v_pk_mul_f32 v[88:89], v[88:89], s[30:31] op_sel_hi:[1,0]
	v_pk_mul_f32 v[90:91], v[90:91], s[30:31] op_sel_hi:[1,0]
	v_pk_mul_f32 v[92:93], v[92:93], s[30:31] op_sel_hi:[1,0]
	v_pk_mul_f32 v[94:95], v[94:95], s[30:31] op_sel_hi:[1,0]
	v_pk_mul_f32 v[96:97], v[96:97], s[30:31] op_sel_hi:[1,0]
	v_pk_mul_f32 v[98:99], v[98:99], s[30:31] op_sel_hi:[1,0]
	v_pk_mul_f32 v[100:101], v[100:101], s[30:31] op_sel_hi:[1,0]
	v_pk_mul_f32 v[102:103], v[102:103], s[30:31] op_sel_hi:[1,0]
	v_pk_mul_f32 v[104:105], v[104:105], s[30:31] op_sel_hi:[1,0]
	v_pk_mul_f32 v[106:107], v[106:107], s[30:31] op_sel_hi:[1,0]
	v_pk_mul_f32 v[108:109], v[108:109], s[30:31] op_sel_hi:[1,0]
	v_pk_mul_f32 v[110:111], v[110:111], s[30:31] op_sel_hi:[1,0]
	v_pk_mul_f32 v[112:113], v[112:113], s[30:31] op_sel_hi:[1,0]
	v_pk_mul_f32 v[114:115], v[114:115], s[30:31] op_sel_hi:[1,0]
	v_pk_mul_f32 v[116:117], v[116:117], s[30:31] op_sel_hi:[1,0]
	v_pk_mul_f32 v[118:119], v[118:119], s[30:31] op_sel_hi:[1,0]
	v_pk_mul_f32 v[120:121], v[120:121], s[30:31] op_sel_hi:[1,0]
	v_pk_mul_f32 v[122:123], v[122:123], s[30:31] op_sel_hi:[1,0]
	v_pk_mul_f32 v[124:125], v[124:125], s[30:31] op_sel_hi:[1,0]
	v_pk_mul_f32 v[126:127], v[126:127], s[30:31] op_sel_hi:[1,0]
	v_pk_mul_f32 v[128:129], v[128:129], s[30:31] op_sel_hi:[1,0]
	v_med3_f32 v66, v66, s24, v237
	v_med3_f32 v67, v67, s24, v237
	v_med3_f32 v68, v68, s24, v237
	v_med3_f32 v69, v69, s24, v237
	v_med3_f32 v70, v70, s24, v237
	v_med3_f32 v71, v71, s24, v237
	v_med3_f32 v72, v72, s24, v237
	v_med3_f32 v73, v73, s24, v237
	v_med3_f32 v74, v74, s24, v237
	v_med3_f32 v75, v75, s24, v237
	v_med3_f32 v76, v76, s24, v237
	v_med3_f32 v77, v77, s24, v237
	v_med3_f32 v78, v78, s24, v237
	v_med3_f32 v79, v79, s24, v237
	v_med3_f32 v80, v80, s24, v237
	v_med3_f32 v81, v81, s24, v237
	v_med3_f32 v82, v82, s24, v237
	v_med3_f32 v83, v83, s24, v237
	v_med3_f32 v84, v84, s24, v237
	v_med3_f32 v85, v85, s24, v237
	v_med3_f32 v86, v86, s24, v237
	v_med3_f32 v87, v87, s24, v237
	v_med3_f32 v88, v88, s24, v237
	v_med3_f32 v89, v89, s24, v237
	v_med3_f32 v90, v90, s24, v237
	v_med3_f32 v91, v91, s24, v237
	v_med3_f32 v92, v92, s24, v237
	v_med3_f32 v93, v93, s24, v237
	v_med3_f32 v94, v94, s24, v237
	v_med3_f32 v95, v95, s24, v237
	v_med3_f32 v96, v96, s24, v237
	v_med3_f32 v97, v97, s24, v237
	v_med3_f32 v98, v98, s24, v237
	v_med3_f32 v99, v99, s24, v237
	v_med3_f32 v100, v100, s24, v237
	v_med3_f32 v101, v101, s24, v237
	v_med3_f32 v102, v102, s24, v237
	v_med3_f32 v103, v103, s24, v237
	v_med3_f32 v104, v104, s24, v237
	v_med3_f32 v105, v105, s24, v237
	v_med3_f32 v106, v106, s24, v237
	v_med3_f32 v107, v107, s24, v237
	v_med3_f32 v108, v108, s24, v237
	v_med3_f32 v109, v109, s24, v237
	v_med3_f32 v110, v110, s24, v237
	v_med3_f32 v111, v111, s24, v237
	v_med3_f32 v112, v112, s24, v237
	v_med3_f32 v113, v113, s24, v237
	v_med3_f32 v114, v114, s24, v237
	v_med3_f32 v115, v115, s24, v237
	v_med3_f32 v116, v116, s24, v237
	v_med3_f32 v117, v117, s24, v237
	v_med3_f32 v118, v118, s24, v237
	v_med3_f32 v119, v119, s24, v237
	v_med3_f32 v120, v120, s24, v237
	v_med3_f32 v121, v121, s24, v237
	v_med3_f32 v122, v122, s24, v237
	v_med3_f32 v123, v123, s24, v237
	v_med3_f32 v124, v124, s24, v237
	v_med3_f32 v125, v125, s24, v237
	v_med3_f32 v126, v126, s24, v237
	v_med3_f32 v127, v127, s24, v237
	v_med3_f32 v128, v128, s24, v237
	v_med3_f32 v129, v129, s24, v237
	v_cvt_pk_fp8_f32 v66, v66, v70
	v_cvt_pk_fp8_f32 v66, v74, v78 op_sel:[0,0,1]
	v_cvt_pk_fp8_f32 v70, v67, v71
	v_cvt_pk_fp8_f32 v70, v75, v79 op_sel:[0,0,1]
	v_cvt_pk_fp8_f32 v74, v68, v72
	v_cvt_pk_fp8_f32 v74, v76, v80 op_sel:[0,0,1]
	v_cvt_pk_fp8_f32 v78, v69, v73
	v_cvt_pk_fp8_f32 v78, v77, v81 op_sel:[0,0,1]
	v_cvt_pk_fp8_f32 v67, v82, v86
	v_cvt_pk_fp8_f32 v67, v90, v94 op_sel:[0,0,1]
	v_cvt_pk_fp8_f32 v71, v83, v87
	v_cvt_pk_fp8_f32 v71, v91, v95 op_sel:[0,0,1]
	v_cvt_pk_fp8_f32 v75, v84, v88
	v_cvt_pk_fp8_f32 v75, v92, v96 op_sel:[0,0,1]
	v_cvt_pk_fp8_f32 v79, v85, v89
	v_cvt_pk_fp8_f32 v79, v93, v97 op_sel:[0,0,1]
	v_cvt_pk_fp8_f32 v68, v98, v102
	v_cvt_pk_fp8_f32 v68, v106, v110 op_sel:[0,0,1]
	v_cvt_pk_fp8_f32 v72, v99, v103
	v_cvt_pk_fp8_f32 v72, v107, v111 op_sel:[0,0,1]
	v_cvt_pk_fp8_f32 v76, v100, v104
	v_cvt_pk_fp8_f32 v76, v108, v112 op_sel:[0,0,1]
	v_cvt_pk_fp8_f32 v80, v101, v105
	v_cvt_pk_fp8_f32 v80, v109, v113 op_sel:[0,0,1]
	v_cvt_pk_fp8_f32 v69, v114, v118
	v_cvt_pk_fp8_f32 v69, v122, v126 op_sel:[0,0,1]
	v_cvt_pk_fp8_f32 v73, v115, v119
	v_cvt_pk_fp8_f32 v73, v123, v127 op_sel:[0,0,1]
	v_cvt_pk_fp8_f32 v77, v116, v120
	v_cvt_pk_fp8_f32 v77, v124, v128 op_sel:[0,0,1]
	v_cvt_pk_fp8_f32 v81, v117, v121
	v_cvt_pk_fp8_f32 v81, v125, v129 op_sel:[0,0,1]
	global_store_dwordx4 v250, v[66:69], s[42:43] nt
	global_store_dwordx4 v250, v[70:73], s[42:43] offset:2048 nt
	global_store_dwordx4 v251, v[74:77], s[42:43] nt
	global_store_dwordx4 v251, v[78:81], s[42:43] offset:2048 nt
	s_add_u32 s42, s42, 0x800000
	s_addc_u32 s43, s43, 0
	global_load_dwordx4 v[66:69], v246, s[4:5] nt
	global_load_dwordx4 v[70:73], v247, s[4:5] nt
	global_load_dwordx4 v[74:77], v248, s[4:5] nt
	global_load_dwordx4 v[78:81], v249, s[4:5] nt
	global_load_dwordx4 v[82:85], v246, s[6:7] nt
	global_load_dwordx4 v[86:89], v247, s[6:7] nt
	global_load_dwordx4 v[90:93], v248, s[6:7] nt
	global_load_dwordx4 v[94:97], v249, s[6:7] nt
	global_load_dwordx4 v[98:101], v246, s[8:9] nt
	global_load_dwordx4 v[102:105], v247, s[8:9] nt
	global_load_dwordx4 v[106:109], v248, s[8:9] nt
	global_load_dwordx4 v[110:113], v249, s[8:9] nt
	global_load_dwordx4 v[114:117], v246, s[38:39] nt
	global_load_dwordx4 v[118:121], v247, s[38:39] nt
	global_load_dwordx4 v[122:125], v248, s[38:39] nt
	global_load_dwordx4 v[126:129], v249, s[38:39] nt
	s_add_u32 s4, s4, 0x2000000
	s_addc_u32 s5, s5, 0
	s_add_u32 s6, s6, 0x2000000
	s_addc_u32 s7, s7, 0
	s_add_u32 s8, s8, 0x2000000
	s_addc_u32 s9, s9, 0
	s_add_u32 s38, s38, 0x2000000
	s_addc_u32 s39, s39, 0
	s_waitcnt vmcnt(40)
; #define GAS __attribute__((address_space(1)))
; template <bool GAIN, bool NT = false> __device__ __forceinline__ void titem8_load(const TItem& d, int lane, f32x4 (&r)[16], f32x4 (&g)[4]) {
;     const int q = lane & 7, kg = lane >> 3; const unsigned lo = (unsigned)((16 * kg) * d.N + 4 * q) * 4u;
;     const GAS char* base = (const GAS char*)d.src;
; #pragma unroll
;     for (int j = 0; j < 16; ++j) { const GAS f32x4* p = (const GAS f32x4*)(base + (size_t)j * (size_t)d.N * 4 + lo); r[j] = NT ? __builtin_nontemporal_load(p) : *p; }
;     if constexpr (GAIN) { const GAS char* gb = (const GAS char*)d.gain; const unsigned go = (unsigned)(16 * kg) * 4u;
; #pragma unroll
;         for (int j4 = 0; j4 < 4; ++j4) g[j4] = *(const GAS f32x4*)(gb + 16 * j4 + go); }
;     asm volatile("" ::: "memory"); __builtin_amdgcn_sched_barrier(0);
; }
; template <bool GAIN, bool NT = false> __device__ __forceinline__ void titem8_store(const TItem& d, int lane, const f32x4 (&r)[16], const f32x4 (&g)[4]) {
;     const int q = lane & 7, kg = lane >> 3; const unsigned lo = (unsigned)((4 * q) * d.ldk + 16 * kg);
;     GAS char* base = (GAS char*)d.dst;
;     f32x4 s[16];
; #pragma unroll
;     for (int j = 0; j < 16; ++j) s[j] = r[j] * ((GAIN ? g[j >> 2][j & 3] : 1.0f) * W8_SCALE);
; #pragma unroll
;     for (int i = 0; i < 4; ++i) { v4u w;
;         w.x = pk4_fp8w(s[0][i], s[1][i], s[2][i], s[3][i]); w.y = pk4_fp8w(s[4][i], s[5][i], s[6][i], s[7][i]);
;         w.z = pk4_fp8w(s[8][i], s[9][i], s[10][i], s[11][i]); w.w = pk4_fp8w(s[12][i], s[13][i], s[14][i], s[15][i]);
;         GAS v4u* p = (GAS v4u*)(base + (size_t)i * (size_t)d.ldk + lo);
;         if (NT) __builtin_nontemporal_store(w, p); else *p = w; }
; }
	v_pk_mul_f32 v[130:131], v[130:131], s[30:31] op_sel_hi:[1,0]
	v_pk_mul_f32 v[132:133], v[132:133], s[30:31] op_sel_hi:[1,0]
	v_pk_mul_f32 v[134:135], v[134:135], s[30:31] op_sel_hi:[1,0]
	v_pk_mul_f32 v[136:137], v[136:137], s[30:31] op_sel_hi:[1,0]
	v_pk_mul_f32 v[138:139], v[138:139], s[30:31] op_sel_hi:[1,0]
	v_pk_mul_f32 v[140:141], v[140:141], s[30:31] op_sel_hi:[1,0]
	v_pk_mul_f32 v[142:143], v[142:143], s[30:31] op_sel_hi:[1,0]
	v_pk_mul_f32 v[144:145], v[144:145], s[30:31] op_sel_hi:[1,0]
	v_pk_mul_f32 v[146:147], v[146:147], s[30:31] op_sel_hi:[1,0]
	v_pk_mul_f32 v[148:149], v[148:149], s[30:31] op_sel_hi:[1,0]
	v_pk_mul_f32 v[150:151], v[150:151], s[30:31] op_sel_hi:[1,0]
	v_pk_mul_f32 v[152:153], v[152:153], s[30:31] op_sel_hi:[1,0]
	v_pk_mul_f32 v[154:155], v[154:155], s[30:31] op_sel_hi:[1,0]
	v_pk_mul_f32 v[156:157], v[156:157], s[30:31] op_sel_hi:[1,0]
	v_pk_mul_f32 v[158:159], v[158:159], s[30:31] op_sel_hi:[1,0]
	v_pk_mul_f32 v[160:161], v[160:161], s[30:31] op_sel_hi:[1,0]
	v_pk_mul_f32 v[162:163], v[162:163], s[30:31] op_sel_hi:[1,0]
	v_pk_mul_f32 v[164:165], v[164:165], s[30:31] op_sel_hi:[1,0]
	v_pk_mul_f32 v[166:167], v[166:167], s[30:31] op_sel_hi:[1,0]
	v_pk_mul_f32 v[168:169], v[168:169], s[30:31] op_sel_hi:[1,0]
	v_pk_mul_f32 v[170:171], v[170:171], s[30:31] op_sel_hi:[1,0]
	v_pk_mul_f32 v[172:173], v[172:173], s[30:31] op_sel_hi:[1,0]
	v_pk_mul_f32 v[174:175], v[174:175], s[30:31] op_sel_hi:[1,0]
	v_pk_mul_f32 v[176:177], v[176:177], s[30:31] op_sel_hi:[1,0]
	v_pk_mul_f32 v[178:179], v[178:179], s[30:31] op_sel_hi:[1,0]
	v_pk_mul_f32 v[180:181], v[180:181], s[30:31] op_sel_hi:[1,0]
	v_pk_mul_f32 v[182:183], v[182:183], s[30:31] op_sel_hi:[1,0]
	v_pk_mul_f32 v[184:185], v[184:185], s[30:31] op_sel_hi:[1,0]
	v_pk_mul_f32 v[186:187], v[186:187], s[30:31] op_sel_hi:[1,0]
	v_pk_mul_f32 v[188:189], v[188:189], s[30:31] op_sel_hi:[1,0]
	v_pk_mul_f32 v[190:191], v[190:191], s[30:31] op_sel_hi:[1,0]
	v_pk_mul_f32 v[192:193], v[192:193], s[30:31] op_sel_hi:[1,0]
	v_med3_f32 v130, v130, s24, v237
	v_med3_f32 v131, v131, s24, v237
	v_med3_f32 v132, v132, s24, v237
	v_med3_f32 v133, v133, s24, v237
	v_med3_f32 v134, v134, s24, v237
	v_med3_f32 v135, v135, s24, v237
	v_med3_f32 v136, v136, s24, v237
	v_med3_f32 v137, v137, s24, v237
	v_med3_f32 v138, v138, s24, v237
	v_med3_f32 v139, v139, s24, v237
	v_med3_f32 v140, v140, s24, v237
	v_med3_f32 v141, v141, s24, v237
	v_med3_f32 v142, v142, s24, v237
	v_med3_f32 v143, v143, s24, v237
	v_med3_f32 v144, v144, s24, v237
	v_med3_f32 v145, v145, s24, v237
	v_med3_f32 v146, v146, s24, v237
	v_med3_f32 v147, v147, s24, v237
	v_med3_f32 v148, v148, s24, v237
	v_med3_f32 v149, v149, s24, v237
	v_med3_f32 v150, v150, s24, v237
	v_med3_f32 v151, v151, s24, v237
	v_med3_f32 v152, v152, s24, v237
	v_med3_f32 v153, v153, s24, v237
	v_med3_f32 v154, v154, s24, v237
	v_med3_f32 v155, v155, s24, v237
	v_med3_f32 v156, v156, s24, v237
	v_med3_f32 v157, v157, s24, v237
	v_med3_f32 v158, v158, s24, v237
	v_med3_f32 v159, v159, s24, v237
	v_med3_f32 v160, v160, s24, v237
	v_med3_f32 v161, v161, s24, v237
	v_med3_f32 v162, v162, s24, v237
	v_med3_f32 v163, v163, s24, v237
	v_med3_f32 v164, v164, s24, v237
	v_med3_f32 v165, v165, s24, v237
	v_med3_f32 v166, v166, s24, v237
	v_med3_f32 v167, v167, s24, v237
	v_med3_f32 v168, v168, s24, v237
	v_med3_f32 v169, v169, s24, v237
	v_med3_f32 v170, v170, s24, v237
	v_med3_f32 v171, v171, s24, v237
	v_med3_f32 v172, v172, s24, v237
	v_med3_f32 v173, v173, s24, v237
	v_med3_f32 v174, v174, s24, v237
	v_med3_f32 v175, v175, s24, v237
	v_med3_f32 v176, v176, s24, v237
	v_med3_f32 v177, v177, s24, v237
	v_med3_f32 v178, v178, s24, v237
	v_med3_f32 v179, v179, s24, v237
	v_med3_f32 v180, v180, s24, v237
	v_med3_f32 v181, v181, s24, v237
	v_med3_f32 v182, v182, s24, v237
	v_med3_f32 v183, v183, s24, v237
	v_med3_f32 v184, v184, s24, v237
	v_med3_f32 v185, v185, s24, v237
	v_med3_f32 v186, v186, s24, v237
	v_med3_f32 v187, v187, s24, v237
	v_med3_f32 v188, v188, s24, v237
	v_med3_f32 v189, v189, s24, v237
	v_med3_f32 v190, v190, s24, v237
	v_med3_f32 v191, v191, s24, v237
	v_med3_f32 v192, v192, s24, v237
	v_med3_f32 v193, v193, s24, v237
	v_cvt_pk_fp8_f32 v130, v130, v134
	v_cvt_pk_fp8_f32 v130, v138, v142 op_sel:[0,0,1]
	v_cvt_pk_fp8_f32 v134, v131, v135
	v_cvt_pk_fp8_f32 v134, v139, v143 op_sel:[0,0,1]
	v_cvt_pk_fp8_f32 v138, v132, v136
	v_cvt_pk_fp8_f32 v138, v140, v144 op_sel:[0,0,1]
	v_cvt_pk_fp8_f32 v142, v133, v137
	v_cvt_pk_fp8_f32 v142, v141, v145 op_sel:[0,0,1]
	v_cvt_pk_fp8_f32 v131, v146, v150
	v_cvt_pk_fp8_f32 v131, v154, v158 op_sel:[0,0,1]
	v_cvt_pk_fp8_f32 v135, v147, v151
	v_cvt_pk_fp8_f32 v135, v155, v159 op_sel:[0,0,1]
	v_cvt_pk_fp8_f32 v139, v148, v152
	v_cvt_pk_fp8_f32 v139, v156, v160 op_sel:[0,0,1]
	v_cvt_pk_fp8_f32 v143, v149, v153
	v_cvt_pk_fp8_f32 v143, v157, v161 op_sel:[0,0,1]
	v_cvt_pk_fp8_f32 v132, v162, v166
	v_cvt_pk_fp8_f32 v132, v170, v174 op_sel:[0,0,1]
	v_cvt_pk_fp8_f32 v136, v163, v167
	v_cvt_pk_fp8_f32 v136, v171, v175 op_sel:[0,0,1]
	v_cvt_pk_fp8_f32 v140, v164, v168
	v_cvt_pk_fp8_f32 v140, v172, v176 op_sel:[0,0,1]
	v_cvt_pk_fp8_f32 v144, v165, v169
	v_cvt_pk_fp8_f32 v144, v173, v177 op_sel:[0,0,1]
	v_cvt_pk_fp8_f32 v133, v178, v182
	v_cvt_pk_fp8_f32 v133, v186, v190 op_sel:[0,0,1]
	v_cvt_pk_fp8_f32 v137, v179, v183
	v_cvt_pk_fp8_f32 v137, v187, v191 op_sel:[0,0,1]
	v_cvt_pk_fp8_f32 v141, v180, v184
	v_cvt_pk_fp8_f32 v141, v188, v192 op_sel:[0,0,1]
	v_cvt_pk_fp8_f32 v145, v181, v185
	v_cvt_pk_fp8_f32 v145, v189, v193 op_sel:[0,0,1]
	global_store_dwordx4 v250, v[130:133], s[42:43] nt
	global_store_dwordx4 v250, v[134:137], s[42:43] offset:2048 nt
	global_store_dwordx4 v251, v[138:141], s[42:43] nt
	global_store_dwordx4 v251, v[142:145], s[42:43] offset:2048 nt
	s_add_u32 s42, s42, 0x800000
	s_addc_u32 s43, s43, 0
	global_load_dwordx4 v[130:133], v246, s[4:5] nt
	global_load_dwordx4 v[134:137], v247, s[4:5] nt
	global_load_dwordx4 v[138:141], v248, s[4:5] nt
	global_load_dwordx4 v[142:145], v249, s[4:5] nt
	global_load_dwordx4 v[146:149], v246, s[6:7] nt
	global_load_dwordx4 v[150:153], v247, s[6:7] nt
	global_load_dwordx4 v[154:157], v248, s[6:7] nt
	global_load_dwordx4 v[158:161], v249, s[6:7] nt
	global_load_dwordx4 v[162:165], v246, s[8:9] nt
	global_load_dwordx4 v[166:169], v247, s[8:9] nt
	global_load_dwordx4 v[170:173], v248, s[8:9] nt
	global_load_dwordx4 v[174:177], v249, s[8:9] nt
	global_load_dwordx4 v[178:181], v246, s[38:39] nt
	global_load_dwordx4 v[182:185], v247, s[38:39] nt
	global_load_dwordx4 v[186:189], v248, s[38:39] nt
	global_load_dwordx4 v[190:193], v249, s[38:39] nt
	s_add_u32 s4, s4, 0x2000000
	s_addc_u32 s5, s5, 0
	s_add_u32 s6, s6, 0x2000000
	s_addc_u32 s7, s7, 0
	s_add_u32 s8, s8, 0x2000000
	s_addc_u32 s9, s9, 0
	s_add_u32 s38, s38, 0x2000000
	s_addc_u32 s39, s39, 0
	s_waitcnt vmcnt(40)
; #define GAS __attribute__((address_space(1)))
; template <bool GAIN, bool NT = false> __device__ __forceinline__ void titem8_load(const TItem& d, int lane, f32x4 (&r)[16], f32x4 (&g)[4]) {
;     const int q = lane & 7, kg = lane >> 3; const unsigned lo = (unsigned)((16 * kg) * d.N + 4 * q) * 4u;
;     const GAS char* base = (const GAS char*)d.src;
; #pragma unroll
;     for (int j = 0; j < 16; ++j) { const GAS f32x4* p = (const GAS f32x4*)(base + (size_t)j * (size_t)d.N * 4 + lo); r[j] = NT ? __builtin_nontemporal_load(p) : *p; }
;     if constexpr (GAIN) { const GAS char* gb = (const GAS char*)d.gain; const unsigned go = (unsigned)(16 * kg) * 4u;
; #pragma unroll
;         for (int j4 = 0; j4 < 4; ++j4) g[j4] = *(const GAS f32x4*)(gb + 16 * j4 + go); }
;     asm volatile("" ::: "memory"); __builtin_amdgcn_sched_barrier(0);
; }
; template <bool GAIN, bool NT = false> __device__ __forceinline__ void titem8_store(const TItem& d, int lane, const f32x4 (&r)[16], const f32x4 (&g)[4]) {
;     const int q = lane & 7, kg = lane >> 3; const unsigned lo = (unsigned)((4 * q) * d.ldk + 16 * kg);
;     GAS char* base = (GAS char*)d.dst;
;     f32x4 s[16];
; #pragma unroll
;     for (int j = 0; j < 16; ++j) s[j] = r[j] * ((GAIN ? g[j >> 2][j & 3] : 1.0f) * W8_SCALE);
; #pragma unroll
;     for (int i = 0; i < 4; ++i) { v4u w;
;         w.x = pk4_fp8w(s[0][i], s[1][i], s[2][i], s[3][i]); w.y = pk4_fp8w(s[4][i], s[5][i], s[6][i], s[7][i]);
;         w.z = pk4_fp8w(s[8][i], s[9][i], s[10][i], s[11][i]); w.w = pk4_fp8w(s[12][i], s[13][i], s[14][i], s[15][i]);
;         GAS v4u* p = (GAS v4u*)(base + (size_t)i * (size_t)d.ldk + lo);
;         if (NT) __builtin_nontemporal_store(w, p); else *p = w; }
; }
	v_pk_mul_f32 v[0:1], v[0:1], s[30:31] op_sel_hi:[1,0]
	v_pk_mul_f32 v[2:3], v[2:3], s[30:31] op_sel_hi:[1,0]
	v_pk_mul_f32 v[4:5], v[4:5], s[30:31] op_sel_hi:[1,0]
	v_pk_mul_f32 v[6:7], v[6:7], s[30:31] op_sel_hi:[1,0]
	v_pk_mul_f32 v[8:9], v[8:9], s[30:31] op_sel_hi:[1,0]
	v_pk_mul_f32 v[10:11], v[10:11], s[30:31] op_sel_hi:[1,0]
	v_pk_mul_f32 v[12:13], v[12:13], s[30:31] op_sel_hi:[1,0]
	v_pk_mul_f32 v[14:15], v[14:15], s[30:31] op_sel_hi:[1,0]
	v_pk_mul_f32 v[16:17], v[16:17], s[30:31] op_sel_hi:[1,0]
	v_pk_mul_f32 v[18:19], v[18:19], s[30:31] op_sel_hi:[1,0]
	v_pk_mul_f32 v[20:21], v[20:21], s[30:31] op_sel_hi:[1,0]
	v_pk_mul_f32 v[22:23], v[22:23], s[30:31] op_sel_hi:[1,0]
	v_pk_mul_f32 v[24:25], v[24:25], s[30:31] op_sel_hi:[1,0]
	v_pk_mul_f32 v[26:27], v[26:27], s[30:31] op_sel_hi:[1,0]
	v_pk_mul_f32 v[28:29], v[28:29], s[30:31] op_sel_hi:[1,0]
	v_pk_mul_f32 v[30:31], v[30:31], s[30:31] op_sel_hi:[1,0]
	v_pk_mul_f32 v[32:33], v[32:33], s[30:31] op_sel_hi:[1,0]
	v_pk_mul_f32 v[34:35], v[34:35], s[30:31] op_sel_hi:[1,0]
	v_pk_mul_f32 v[36:37], v[36:37], s[30:31] op_sel_hi:[1,0]
	v_pk_mul_f32 v[38:39], v[38:39], s[30:31] op_sel_hi:[1,0]
	v_pk_mul_f32 v[40:41], v[40:41], s[30:31] op_sel_hi:[1,0]
	v_pk_mul_f32 v[42:43], v[42:43], s[30:31] op_sel_hi:[1,0]
	v_pk_mul_f32 v[44:45], v[44:45], s[30:31] op_sel_hi:[1,0]
	v_pk_mul_f32 v[46:47], v[46:47], s[30:31] op_sel_hi:[1,0]
	v_pk_mul_f32 v[48:49], v[48:49], s[30:31] op_sel_hi:[1,0]
	v_pk_mul_f32 v[50:51], v[50:51], s[30:31] op_sel_hi:[1,0]
	v_pk_mul_f32 v[52:53], v[52:53], s[30:31] op_sel_hi:[1,0]
	v_pk_mul_f32 v[54:55], v[54:55], s[30:31] op_sel_hi:[1,0]
	v_pk_mul_f32 v[56:57], v[56:57], s[30:31] op_sel_hi:[1,0]
	v_pk_mul_f32 v[58:59], v[58:59], s[30:31] op_sel_hi:[1,0]
	v_pk_mul_f32 v[60:61], v[60:61], s[30:31] op_sel_hi:[1,0]
	v_pk_mul_f32 v[62:63], v[62:63], s[30:31] op_sel_hi:[1,0]
	v_med3_f32 v0, v0, s24, v237
	v_med3_f32 v1, v1, s24, v237
	v_med3_f32 v2, v2, s24, v237
	v_med3_f32 v3, v3, s24, v237
	v_med3_f32 v4, v4, s24, v237
	v_med3_f32 v5, v5, s24, v237
	v_med3_f32 v6, v6, s24, v237
	v_med3_f32 v7, v7, s24, v237
	v_med3_f32 v8, v8, s24, v237
	v_med3_f32 v9, v9, s24, v237
	v_med3_f32 v10, v10, s24, v237
	v_med3_f32 v11, v11, s24, v237
	v_med3_f32 v12, v12, s24, v237
	v_med3_f32 v13, v13, s24, v237
	v_med3_f32 v14, v14, s24, v237
	v_med3_f32 v15, v15, s24, v237
	v_med3_f32 v16, v16, s24, v237
	v_med3_f32 v17, v17, s24, v237
	v_med3_f32 v18, v18, s24, v237
	v_med3_f32 v19, v19, s24, v237
	v_med3_f32 v20, v20, s24, v237
	v_med3_f32 v21, v21, s24, v237
	v_med3_f32 v22, v22, s24, v237
	v_med3_f32 v23, v23, s24, v237
	v_med3_f32 v24, v24, s24, v237
	v_med3_f32 v25, v25, s24, v237
	v_med3_f32 v26, v26, s24, v237
	v_med3_f32 v27, v27, s24, v237
	v_med3_f32 v28, v28, s24, v237
	v_med3_f32 v29, v29, s24, v237
	v_med3_f32 v30, v30, s24, v237
	v_med3_f32 v31, v31, s24, v237
	v_med3_f32 v32, v32, s24, v237
	v_med3_f32 v33, v33, s24, v237
	v_med3_f32 v34, v34, s24, v237
	v_med3_f32 v35, v35, s24, v237
	v_med3_f32 v36, v36, s24, v237
	v_med3_f32 v37, v37, s24, v237
	v_med3_f32 v38, v38, s24, v237
	v_med3_f32 v39, v39, s24, v237
	v_med3_f32 v40, v40, s24, v237
	v_med3_f32 v41, v41, s24, v237
	v_med3_f32 v42, v42, s24, v237
	v_med3_f32 v43, v43, s24, v237
	v_med3_f32 v44, v44, s24, v237
	v_med3_f32 v45, v45, s24, v237
	v_med3_f32 v46, v46, s24, v237
	v_med3_f32 v47, v47, s24, v237
	v_med3_f32 v48, v48, s24, v237
	v_med3_f32 v49, v49, s24, v237
	v_med3_f32 v50, v50, s24, v237
	v_med3_f32 v51, v51, s24, v237
	v_med3_f32 v52, v52, s24, v237
	v_med3_f32 v53, v53, s24, v237
	v_med3_f32 v54, v54, s24, v237
	v_med3_f32 v55, v55, s24, v237
	v_med3_f32 v56, v56, s24, v237
	v_med3_f32 v57, v57, s24, v237
	v_med3_f32 v58, v58, s24, v237
	v_med3_f32 v59, v59, s24, v237
	v_med3_f32 v60, v60, s24, v237
	v_med3_f32 v61, v61, s24, v237
	v_med3_f32 v62, v62, s24, v237
	v_med3_f32 v63, v63, s24, v237
	v_cvt_pk_fp8_f32 v0, v0, v4
	v_cvt_pk_fp8_f32 v0, v8, v12 op_sel:[0,0,1]
	v_cvt_pk_fp8_f32 v4, v1, v5
	v_cvt_pk_fp8_f32 v4, v9, v13 op_sel:[0,0,1]
	v_cvt_pk_fp8_f32 v8, v2, v6
	v_cvt_pk_fp8_f32 v8, v10, v14 op_sel:[0,0,1]
	v_cvt_pk_fp8_f32 v12, v3, v7
	v_cvt_pk_fp8_f32 v12, v11, v15 op_sel:[0,0,1]
	v_cvt_pk_fp8_f32 v1, v16, v20
	v_cvt_pk_fp8_f32 v1, v24, v28 op_sel:[0,0,1]
	v_cvt_pk_fp8_f32 v5, v17, v21
	v_cvt_pk_fp8_f32 v5, v25, v29 op_sel:[0,0,1]
	v_cvt_pk_fp8_f32 v9, v18, v22
	v_cvt_pk_fp8_f32 v9, v26, v30 op_sel:[0,0,1]
	v_cvt_pk_fp8_f32 v13, v19, v23
	v_cvt_pk_fp8_f32 v13, v27, v31 op_sel:[0,0,1]
	v_cvt_pk_fp8_f32 v2, v32, v36
	v_cvt_pk_fp8_f32 v2, v40, v44 op_sel:[0,0,1]
	v_cvt_pk_fp8_f32 v6, v33, v37
	v_cvt_pk_fp8_f32 v6, v41, v45 op_sel:[0,0,1]
	v_cvt_pk_fp8_f32 v10, v34, v38
	v_cvt_pk_fp8_f32 v10, v42, v46 op_sel:[0,0,1]
	v_cvt_pk_fp8_f32 v14, v35, v39
	v_cvt_pk_fp8_f32 v14, v43, v47 op_sel:[0,0,1]
	v_cvt_pk_fp8_f32 v3, v48, v52
	v_cvt_pk_fp8_f32 v3, v56, v60 op_sel:[0,0,1]
	v_cvt_pk_fp8_f32 v7, v49, v53
	v_cvt_pk_fp8_f32 v7, v57, v61 op_sel:[0,0,1]
	v_cvt_pk_fp8_f32 v11, v50, v54
	v_cvt_pk_fp8_f32 v11, v58, v62 op_sel:[0,0,1]
	v_cvt_pk_fp8_f32 v15, v51, v55
	v_cvt_pk_fp8_f32 v15, v59, v63 op_sel:[0,0,1]
	global_store_dwordx4 v250, v[0:3], s[42:43] nt
	global_store_dwordx4 v250, v[4:7], s[42:43] offset:2048 nt
	global_store_dwordx4 v251, v[8:11], s[42:43] nt
	global_store_dwordx4 v251, v[12:15], s[42:43] offset:2048 nt
	s_add_u32 s42, s42, 0x800000
	s_addc_u32 s43, s43, 0
	global_load_dwordx4 v[0:3], v246, s[4:5] nt
	global_load_dwordx4 v[4:7], v247, s[4:5] nt
	global_load_dwordx4 v[8:11], v248, s[4:5] nt
	global_load_dwordx4 v[12:15], v249, s[4:5] nt
	global_load_dwordx4 v[16:19], v246, s[6:7] nt
	global_load_dwordx4 v[20:23], v247, s[6:7] nt
	global_load_dwordx4 v[24:27], v248, s[6:7] nt
	global_load_dwordx4 v[28:31], v249, s[6:7] nt
	global_load_dwordx4 v[32:35], v246, s[8:9] nt
	global_load_dwordx4 v[36:39], v247, s[8:9] nt
	global_load_dwordx4 v[40:43], v248, s[8:9] nt
	global_load_dwordx4 v[44:47], v249, s[8:9] nt
	global_load_dwordx4 v[48:51], v246, s[38:39] nt
	global_load_dwordx4 v[52:55], v247, s[38:39] nt
	global_load_dwordx4 v[56:59], v248, s[38:39] nt
	global_load_dwordx4 v[60:63], v249, s[38:39] nt
	s_add_u32 s4, s4, 0x2000000
	s_addc_u32 s5, s5, 0
	s_add_u32 s6, s6, 0x2000000
	s_addc_u32 s7, s7, 0
	s_add_u32 s8, s8, 0x2000000
	s_addc_u32 s9, s9, 0
	s_add_u32 s38, s38, 0x2000000
	s_addc_u32 s39, s39, 0
	s_waitcnt vmcnt(40)
; #define GAS __attribute__((address_space(1)))
; template <bool GAIN, bool NT = false> __device__ __forceinline__ void titem8_load(const TItem& d, int lane, f32x4 (&r)[16], f32x4 (&g)[4]) {
;     const int q = lane & 7, kg = lane >> 3; const unsigned lo = (unsigned)((16 * kg) * d.N + 4 * q) * 4u;
;     const GAS char* base = (const GAS char*)d.src;
; #pragma unroll
;     for (int j = 0; j < 16; ++j) { const GAS f32x4* p = (const GAS f32x4*)(base + (size_t)j * (size_t)d.N * 4 + lo); r[j] = NT ? __builtin_nontemporal_load(p) : *p; }
;     if constexpr (GAIN) { const GAS char* gb = (const GAS char*)d.gain; const unsigned go = (unsigned)(16 * kg) * 4u;
; #pragma unroll
;         for (int j4 = 0; j4 < 4; ++j4) g[j4] = *(const GAS f32x4*)(gb + 16 * j4 + go); }
;     asm volatile("" ::: "memory"); __builtin_amdgcn_sched_barrier(0);
; }
; template <bool GAIN, bool NT = false> __device__ __forceinline__ void titem8_store(const TItem& d, int lane, const f32x4 (&r)[16], const f32x4 (&g)[4]) {
;     const int q = lane & 7, kg = lane >> 3; const unsigned lo = (unsigned)((4 * q) * d.ldk + 16 * kg);
;     GAS char* base = (GAS char*)d.dst;
;     f32x4 s[16];
; #pragma unroll
;     for (int j = 0; j < 16; ++j) s[j] = r[j] * ((GAIN ? g[j >> 2][j & 3] : 1.0f) * W8_SCALE);
; #pragma unroll
;     for (int i = 0; i < 4; ++i) { v4u w;
;         w.x = pk4_fp8w(s[0][i], s[1][i], s[2][i], s[3][i]); w.y = pk4_fp8w(s[4][i], s[5][i], s[6][i], s[7][i]);
;         w.z = pk4_fp8w(s[8][i], s[9][i], s[10][i], s[11][i]); w.w = pk4_fp8w(s[12][i], s[13][i], s[14][i], s[15][i]);
;         GAS v4u* p = (GAS v4u*)(base + (size_t)i * (size_t)d.ldk + lo);
;         if (NT) __builtin_nontemporal_store(w, p); else *p = w; }
; }
	v_pk_mul_f32 v[66:67], v[66:67], s[30:31] op_sel_hi:[1,0]
	v_pk_mul_f32 v[68:69], v[68:69], s[30:31] op_sel_hi:[1,0]
	v_pk_mul_f32 v[70:71], v[70:71], s[30:31] op_sel_hi:[1,0]
	v_pk_mul_f32 v[72:73], v[72:73], s[30:31] op_sel_hi:[1,0]
	v_pk_mul_f32 v[74:75], v[74:75], s[30:31] op_sel_hi:[1,0]
	v_pk_mul_f32 v[76:77], v[76:77], s[30:31] op_sel_hi:[1,0]
	v_pk_mul_f32 v[78:79], v[78:79], s[30:31] op_sel_hi:[1,0]
	v_pk_mul_f32 v[80:81], v[80:81], s[30:31] op_sel_hi:[1,0]
	v_pk_mul_f32 v[82:83], v[82:83], s[30:31] op_sel_hi:[1,0]
	v_pk_mul_f32 v[84:85], v[84:85], s[30:31] op_sel_hi:[1,0]
	v_pk_mul_f32 v[86:87], v[86:87], s[30:31] op_sel_hi:[1,0]
	v_pk_mul_f32 v[88:89], v[88:89], s[30:31] op_sel_hi:[1,0]
	v_pk_mul_f32 v[90:91], v[90:91], s[30:31] op_sel_hi:[1,0]
	v_pk_mul_f32 v[92:93], v[92:93], s[30:31] op_sel_hi:[1,0]
	v_pk_mul_f32 v[94:95], v[94:95], s[30:31] op_sel_hi:[1,0]
	v_pk_mul_f32 v[96:97], v[96:97], s[30:31] op_sel_hi:[1,0]
	v_pk_mul_f32 v[98:99], v[98:99], s[30:31] op_sel_hi:[1,0]
	v_pk_mul_f32 v[100:101], v[100:101], s[30:31] op_sel_hi:[1,0]
	v_pk_mul_f32 v[102:103], v[102:103], s[30:31] op_sel_hi:[1,0]
	v_pk_mul_f32 v[104:105], v[104:105], s[30:31] op_sel_hi:[1,0]
	v_pk_mul_f32 v[106:107], v[106:107], s[30:31] op_sel_hi:[1,0]
	v_pk_mul_f32 v[108:109], v[108:109], s[30:31] op_sel_hi:[1,0]
	v_pk_mul_f32 v[110:111], v[110:111], s[30:31] op_sel_hi:[1,0]
	v_pk_mul_f32 v[112:113], v[112:113], s[30:31] op_sel_hi:[1,0]
	v_pk_mul_f32 v[114:115], v[114:115], s[30:31] op_sel_hi:[1,0]
	v_pk_mul_f32 v[116:117], v[116:117], s[30:31] op_sel_hi:[1,0]
	v_pk_mul_f32 v[118:119], v[118:119], s[30:31] op_sel_hi:[1,0]
	v_pk_mul_f32 v[120:121], v[120:121], s[30:31] op_sel_hi:[1,0]
	v_pk_mul_f32 v[122:123], v[122:123], s[30:31] op_sel_hi:[1,0]
	v_pk_mul_f32 v[124:125], v[124:125], s[30:31] op_sel_hi:[1,0]
	v_pk_mul_f32 v[126:127], v[126:127], s[30:31] op_sel_hi:[1,0]
	v_pk_mul_f32 v[128:129], v[128:129], s[30:31] op_sel_hi:[1,0]
	v_med3_f32 v66, v66, s24, v237
	v_med3_f32 v67, v67, s24, v237
	v_med3_f32 v68, v68, s24, v237
	v_med3_f32 v69, v69, s24, v237
	v_med3_f32 v70, v70, s24, v237
	v_med3_f32 v71, v71, s24, v237
	v_med3_f32 v72, v72, s24, v237
	v_med3_f32 v73, v73, s24, v237
	v_med3_f32 v74, v74, s24, v237
	v_med3_f32 v75, v75, s24, v237
	v_med3_f32 v76, v76, s24, v237
	v_med3_f32 v77, v77, s24, v237
	v_med3_f32 v78, v78, s24, v237
	v_med3_f32 v79, v79, s24, v237
	v_med3_f32 v80, v80, s24, v237
	v_med3_f32 v81, v81, s24, v237
	v_med3_f32 v82, v82, s24, v237
	v_med3_f32 v83, v83, s24, v237
	v_med3_f32 v84, v84, s24, v237
	v_med3_f32 v85, v85, s24, v237
	v_med3_f32 v86, v86, s24, v237
	v_med3_f32 v87, v87, s24, v237
	v_med3_f32 v88, v88, s24, v237
	v_med3_f32 v89, v89, s24, v237
	v_med3_f32 v90, v90, s24, v237
	v_med3_f32 v91, v91, s24, v237
	v_med3_f32 v92, v92, s24, v237
	v_med3_f32 v93, v93, s24, v237
	v_med3_f32 v94, v94, s24, v237
	v_med3_f32 v95, v95, s24, v237
	v_med3_f32 v96, v96, s24, v237
	v_med3_f32 v97, v97, s24, v237
	v_med3_f32 v98, v98, s24, v237
	v_med3_f32 v99, v99, s24, v237
	v_med3_f32 v100, v100, s24, v237
	v_med3_f32 v101, v101, s24, v237
	v_med3_f32 v102, v102, s24, v237
	v_med3_f32 v103, v103, s24, v237
	v_med3_f32 v104, v104, s24, v237
	v_med3_f32 v105, v105, s24, v237
	v_med3_f32 v106, v106, s24, v237
	v_med3_f32 v107, v107, s24, v237
	v_med3_f32 v108, v108, s24, v237
	v_med3_f32 v109, v109, s24, v237
	v_med3_f32 v110, v110, s24, v237
	v_med3_f32 v111, v111, s24, v237
	v_med3_f32 v112, v112, s24, v237
	v_med3_f32 v113, v113, s24, v237
	v_med3_f32 v114, v114, s24, v237
	v_med3_f32 v115, v115, s24, v237
	v_med3_f32 v116, v116, s24, v237
	v_med3_f32 v117, v117, s24, v237
	v_med3_f32 v118, v118, s24, v237
	v_med3_f32 v119, v119, s24, v237
	v_med3_f32 v120, v120, s24, v237
	v_med3_f32 v121, v121, s24, v237
	v_med3_f32 v122, v122, s24, v237
	v_med3_f32 v123, v123, s24, v237
	v_med3_f32 v124, v124, s24, v237
	v_med3_f32 v125, v125, s24, v237
	v_med3_f32 v126, v126, s24, v237
	v_med3_f32 v127, v127, s24, v237
	v_med3_f32 v128, v128, s24, v237
	v_med3_f32 v129, v129, s24, v237
	v_cvt_pk_fp8_f32 v66, v66, v70
	v_cvt_pk_fp8_f32 v66, v74, v78 op_sel:[0,0,1]
	v_cvt_pk_fp8_f32 v70, v67, v71
	v_cvt_pk_fp8_f32 v70, v75, v79 op_sel:[0,0,1]
	v_cvt_pk_fp8_f32 v74, v68, v72
	v_cvt_pk_fp8_f32 v74, v76, v80 op_sel:[0,0,1]
	v_cvt_pk_fp8_f32 v78, v69, v73
	v_cvt_pk_fp8_f32 v78, v77, v81 op_sel:[0,0,1]
	v_cvt_pk_fp8_f32 v67, v82, v86
	v_cvt_pk_fp8_f32 v67, v90, v94 op_sel:[0,0,1]
	v_cvt_pk_fp8_f32 v71, v83, v87
	v_cvt_pk_fp8_f32 v71, v91, v95 op_sel:[0,0,1]
	v_cvt_pk_fp8_f32 v75, v84, v88
	v_cvt_pk_fp8_f32 v75, v92, v96 op_sel:[0,0,1]
	v_cvt_pk_fp8_f32 v79, v85, v89
	v_cvt_pk_fp8_f32 v79, v93, v97 op_sel:[0,0,1]
	v_cvt_pk_fp8_f32 v68, v98, v102
	v_cvt_pk_fp8_f32 v68, v106, v110 op_sel:[0,0,1]
	v_cvt_pk_fp8_f32 v72, v99, v103
	v_cvt_pk_fp8_f32 v72, v107, v111 op_sel:[0,0,1]
	v_cvt_pk_fp8_f32 v76, v100, v104
	v_cvt_pk_fp8_f32 v76, v108, v112 op_sel:[0,0,1]
	v_cvt_pk_fp8_f32 v80, v101, v105
	v_cvt_pk_fp8_f32 v80, v109, v113 op_sel:[0,0,1]
	v_cvt_pk_fp8_f32 v69, v114, v118
	v_cvt_pk_fp8_f32 v69, v122, v126 op_sel:[0,0,1]
	v_cvt_pk_fp8_f32 v73, v115, v119
	v_cvt_pk_fp8_f32 v73, v123, v127 op_sel:[0,0,1]
	v_cvt_pk_fp8_f32 v77, v116, v120
	v_cvt_pk_fp8_f32 v77, v124, v128 op_sel:[0,0,1]
	v_cvt_pk_fp8_f32 v81, v117, v121
	v_cvt_pk_fp8_f32 v81, v125, v129 op_sel:[0,0,1]
	global_store_dwordx4 v250, v[66:69], s[42:43] nt
	global_store_dwordx4 v250, v[70:73], s[42:43] offset:2048 nt
	global_store_dwordx4 v251, v[74:77], s[42:43] nt
	global_store_dwordx4 v251, v[78:81], s[42:43] offset:2048 nt
	s_add_u32 s42, s42, 0x800000
	s_addc_u32 s43, s43, 0
	global_load_dwordx4 v[66:69], v246, s[4:5] nt
	global_load_dwordx4 v[70:73], v247, s[4:5] nt
	global_load_dwordx4 v[74:77], v248, s[4:5] nt
	global_load_dwordx4 v[78:81], v249, s[4:5] nt
	global_load_dwordx4 v[82:85], v246, s[6:7] nt
	global_load_dwordx4 v[86:89], v247, s[6:7] nt
	global_load_dwordx4 v[90:93], v248, s[6:7] nt
	global_load_dwordx4 v[94:97], v249, s[6:7] nt
	global_load_dwordx4 v[98:101], v246, s[8:9] nt
	global_load_dwordx4 v[102:105], v247, s[8:9] nt
	global_load_dwordx4 v[106:109], v248, s[8:9] nt
	global_load_dwordx4 v[110:113], v249, s[8:9] nt
	global_load_dwordx4 v[114:117], v246, s[38:39] nt
	global_load_dwordx4 v[118:121], v247, s[38:39] nt
	global_load_dwordx4 v[122:125], v248, s[38:39] nt
	global_load_dwordx4 v[126:129], v249, s[38:39] nt
	s_add_u32 s4, s4, 0x2000000
	s_addc_u32 s5, s5, 0
	s_add_u32 s6, s6, 0x2000000
	s_addc_u32 s7, s7, 0
	s_add_u32 s8, s8, 0x2000000
	s_addc_u32 s9, s9, 0
	s_add_u32 s38, s38, 0x2000000
	s_addc_u32 s39, s39, 0
	s_waitcnt vmcnt(40)
; #define GAS __attribute__((address_space(1)))
; template <bool GAIN, bool NT = false> __device__ __forceinline__ void titem8_load(const TItem& d, int lane, f32x4 (&r)[16], f32x4 (&g)[4]) {
;     const int q = lane & 7, kg = lane >> 3; const unsigned lo = (unsigned)((16 * kg) * d.N + 4 * q) * 4u;
;     const GAS char* base = (const GAS char*)d.src;
; #pragma unroll
;     for (int j = 0; j < 16; ++j) { const GAS f32x4* p = (const GAS f32x4*)(base + (size_t)j * (size_t)d.N * 4 + lo); r[j] = NT ? __builtin_nontemporal_load(p) : *p; }
;     if constexpr (GAIN) { const GAS char* gb = (const GAS char*)d.gain; const unsigned go = (unsigned)(16 * kg) * 4u;
; #pragma unroll
;         for (int j4 = 0; j4 < 4; ++j4) g[j4] = *(const GAS f32x4*)(gb + 16 * j4 + go); }
;     asm volatile("" ::: "memory"); __builtin_amdgcn_sched_barrier(0);
; }
; template <bool GAIN, bool NT = false> __device__ __forceinline__ void titem8_store(const TItem& d, int lane, const f32x4 (&r)[16], const f32x4 (&g)[4]) {
;     const int q = lane & 7, kg = lane >> 3; const unsigned lo = (unsigned)((4 * q) * d.ldk + 16 * kg);
;     GAS char* base = (GAS char*)d.dst;
;     f32x4 s[16];
; #pragma unroll
;     for (int j = 0; j < 16; ++j) s[j] = r[j] * ((GAIN ? g[j >> 2][j & 3] : 1.0f) * W8_SCALE);
; #pragma unroll
;     for (int i = 0; i < 4; ++i) { v4u w;
;         w.x = pk4_fp8w(s[0][i], s[1][i], s[2][i], s[3][i]); w.y = pk4_fp8w(s[4][i], s[5][i], s[6][i], s[7][i]);
;         w.z = pk4_fp8w(s[8][i], s[9][i], s[10][i], s[11][i]); w.w = pk4_fp8w(s[12][i], s[13][i], s[14][i], s[15][i]);
;         GAS v4u* p = (GAS v4u*)(base + (size_t)i * (size_t)d.ldk + lo);
;         if (NT) __builtin_nontemporal_store(w, p); else *p = w; }
; }
	v_pk_mul_f32 v[130:131], v[130:131], s[30:31] op_sel_hi:[1,0]
	v_pk_mul_f32 v[132:133], v[132:133], s[30:31] op_sel_hi:[1,0]
	v_pk_mul_f32 v[134:135], v[134:135], s[30:31] op_sel_hi:[1,0]
	v_pk_mul_f32 v[136:137], v[136:137], s[30:31] op_sel_hi:[1,0]
	v_pk_mul_f32 v[138:139], v[138:139], s[30:31] op_sel_hi:[1,0]
	v_pk_mul_f32 v[140:141], v[140:141], s[30:31] op_sel_hi:[1,0]
	v_pk_mul_f32 v[142:143], v[142:143], s[30:31] op_sel_hi:[1,0]
	v_pk_mul_f32 v[144:145], v[144:145], s[30:31] op_sel_hi:[1,0]
	v_pk_mul_f32 v[146:147], v[146:147], s[30:31] op_sel_hi:[1,0]
	v_pk_mul_f32 v[148:149], v[148:149], s[30:31] op_sel_hi:[1,0]
	v_pk_mul_f32 v[150:151], v[150:151], s[30:31] op_sel_hi:[1,0]
	v_pk_mul_f32 v[152:153], v[152:153], s[30:31] op_sel_hi:[1,0]
	v_pk_mul_f32 v[154:155], v[154:155], s[30:31] op_sel_hi:[1,0]
	v_pk_mul_f32 v[156:157], v[156:157], s[30:31] op_sel_hi:[1,0]
	v_pk_mul_f32 v[158:159], v[158:159], s[30:31] op_sel_hi:[1,0]
	v_pk_mul_f32 v[160:161], v[160:161], s[30:31] op_sel_hi:[1,0]
	v_pk_mul_f32 v[162:163], v[162:163], s[30:31] op_sel_hi:[1,0]
	v_pk_mul_f32 v[164:165], v[164:165], s[30:31] op_sel_hi:[1,0]
	v_pk_mul_f32 v[166:167], v[166:167], s[30:31] op_sel_hi:[1,0]
	v_pk_mul_f32 v[168:169], v[168:169], s[30:31] op_sel_hi:[1,0]
	v_pk_mul_f32 v[170:171], v[170:171], s[30:31] op_sel_hi:[1,0]
	v_pk_mul_f32 v[172:173], v[172:173], s[30:31] op_sel_hi:[1,0]
	v_pk_mul_f32 v[174:175], v[174:175], s[30:31] op_sel_hi:[1,0]
	v_pk_mul_f32 v[176:177], v[176:177], s[30:31] op_sel_hi:[1,0]
	v_pk_mul_f32 v[178:179], v[178:179], s[30:31] op_sel_hi:[1,0]
	v_pk_mul_f32 v[180:181], v[180:181], s[30:31] op_sel_hi:[1,0]
	v_pk_mul_f32 v[182:183], v[182:183], s[30:31] op_sel_hi:[1,0]
	v_pk_mul_f32 v[184:185], v[184:185], s[30:31] op_sel_hi:[1,0]
	v_pk_mul_f32 v[186:187], v[186:187], s[30:31] op_sel_hi:[1,0]
	v_pk_mul_f32 v[188:189], v[188:189], s[30:31] op_sel_hi:[1,0]
	v_pk_mul_f32 v[190:191], v[190:191], s[30:31] op_sel_hi:[1,0]
	v_pk_mul_f32 v[192:193], v[192:193], s[30:31] op_sel_hi:[1,0]
	v_med3_f32 v130, v130, s24, v237
	v_med3_f32 v131, v131, s24, v237
	v_med3_f32 v132, v132, s24, v237
	v_med3_f32 v133, v133, s24, v237
	v_med3_f32 v134, v134, s24, v237
	v_med3_f32 v135, v135, s24, v237
	v_med3_f32 v136, v136, s24, v237
	v_med3_f32 v137, v137, s24, v237
	v_med3_f32 v138, v138, s24, v237
	v_med3_f32 v139, v139, s24, v237
	v_med3_f32 v140, v140, s24, v237
	v_med3_f32 v141, v141, s24, v237
	v_med3_f32 v142, v142, s24, v237
	v_med3_f32 v143, v143, s24, v237
	v_med3_f32 v144, v144, s24, v237
	v_med3_f32 v145, v145, s24, v237
	v_med3_f32 v146, v146, s24, v237
	v_med3_f32 v147, v147, s24, v237
	v_med3_f32 v148, v148, s24, v237
	v_med3_f32 v149, v149, s24, v237
	v_med3_f32 v150, v150, s24, v237
	v_med3_f32 v151, v151, s24, v237
	v_med3_f32 v152, v152, s24, v237
	v_med3_f32 v153, v153, s24, v237
	v_med3_f32 v154, v154, s24, v237
	v_med3_f32 v155, v155, s24, v237
	v_med3_f32 v156, v156, s24, v237
	v_med3_f32 v157, v157, s24, v237
	v_med3_f32 v158, v158, s24, v237
	v_med3_f32 v159, v159, s24, v237
	v_med3_f32 v160, v160, s24, v237
	v_med3_f32 v161, v161, s24, v237
	v_med3_f32 v162, v162, s24, v237
	v_med3_f32 v163, v163, s24, v237
	v_med3_f32 v164, v164, s24, v237
	v_med3_f32 v165, v165, s24, v237
	v_med3_f32 v166, v166, s24, v237
	v_med3_f32 v167, v167, s24, v237
	v_med3_f32 v168, v168, s24, v237
	v_med3_f32 v169, v169, s24, v237
	v_med3_f32 v170, v170, s24, v237
	v_med3_f32 v171, v171, s24, v237
	v_med3_f32 v172, v172, s24, v237
	v_med3_f32 v173, v173, s24, v237
	v_med3_f32 v174, v174, s24, v237
	v_med3_f32 v175, v175, s24, v237
	v_med3_f32 v176, v176, s24, v237
	v_med3_f32 v177, v177, s24, v237
	v_med3_f32 v178, v178, s24, v237
	v_med3_f32 v179, v179, s24, v237
	v_med3_f32 v180, v180, s24, v237
	v_med3_f32 v181, v181, s24, v237
	v_med3_f32 v182, v182, s24, v237
	v_med3_f32 v183, v183, s24, v237
	v_med3_f32 v184, v184, s24, v237
	v_med3_f32 v185, v185, s24, v237
	v_med3_f32 v186, v186, s24, v237
	v_med3_f32 v187, v187, s24, v237
	v_med3_f32 v188, v188, s24, v237
	v_med3_f32 v189, v189, s24, v237
	v_med3_f32 v190, v190, s24, v237
	v_med3_f32 v191, v191, s24, v237
	v_med3_f32 v192, v192, s24, v237
	v_med3_f32 v193, v193, s24, v237
	v_cvt_pk_fp8_f32 v130, v130, v134
	v_cvt_pk_fp8_f32 v130, v138, v142 op_sel:[0,0,1]
	v_cvt_pk_fp8_f32 v134, v131, v135
	v_cvt_pk_fp8_f32 v134, v139, v143 op_sel:[0,0,1]
	v_cvt_pk_fp8_f32 v138, v132, v136
	v_cvt_pk_fp8_f32 v138, v140, v144 op_sel:[0,0,1]
	v_cvt_pk_fp8_f32 v142, v133, v137
	v_cvt_pk_fp8_f32 v142, v141, v145 op_sel:[0,0,1]
	v_cvt_pk_fp8_f32 v131, v146, v150
	v_cvt_pk_fp8_f32 v131, v154, v158 op_sel:[0,0,1]
	v_cvt_pk_fp8_f32 v135, v147, v151
	v_cvt_pk_fp8_f32 v135, v155, v159 op_sel:[0,0,1]
	v_cvt_pk_fp8_f32 v139, v148, v152
	v_cvt_pk_fp8_f32 v139, v156, v160 op_sel:[0,0,1]
	v_cvt_pk_fp8_f32 v143, v149, v153
	v_cvt_pk_fp8_f32 v143, v157, v161 op_sel:[0,0,1]
	v_cvt_pk_fp8_f32 v132, v162, v166
	v_cvt_pk_fp8_f32 v132, v170, v174 op_sel:[0,0,1]
	v_cvt_pk_fp8_f32 v136, v163, v167
	v_cvt_pk_fp8_f32 v136, v171, v175 op_sel:[0,0,1]
	v_cvt_pk_fp8_f32 v140, v164, v168
	v_cvt_pk_fp8_f32 v140, v172, v176 op_sel:[0,0,1]
	v_cvt_pk_fp8_f32 v144, v165, v169
	v_cvt_pk_fp8_f32 v144, v173, v177 op_sel:[0,0,1]
	v_cvt_pk_fp8_f32 v133, v178, v182
	v_cvt_pk_fp8_f32 v133, v186, v190 op_sel:[0,0,1]
	v_cvt_pk_fp8_f32 v137, v179, v183
	v_cvt_pk_fp8_f32 v137, v187, v191 op_sel:[0,0,1]
	v_cvt_pk_fp8_f32 v141, v180, v184
	v_cvt_pk_fp8_f32 v141, v188, v192 op_sel:[0,0,1]
	v_cvt_pk_fp8_f32 v145, v181, v185
	v_cvt_pk_fp8_f32 v145, v189, v193 op_sel:[0,0,1]
	global_store_dwordx4 v250, v[130:133], s[42:43] nt
	global_store_dwordx4 v250, v[134:137], s[42:43] offset:2048 nt
	global_store_dwordx4 v251, v[138:141], s[42:43] nt
	global_store_dwordx4 v251, v[142:145], s[42:43] offset:2048 nt
	s_add_u32 s42, s42, 0x800000
	s_addc_u32 s43, s43, 0
	global_load_dwordx4 v[130:133], v246, s[4:5] nt
	global_load_dwordx4 v[134:137], v247, s[4:5] nt
	global_load_dwordx4 v[138:141], v248, s[4:5] nt
	global_load_dwordx4 v[142:145], v249, s[4:5] nt
	global_load_dwordx4 v[146:149], v246, s[6:7] nt
	global_load_dwordx4 v[150:153], v247, s[6:7] nt
	global_load_dwordx4 v[154:157], v248, s[6:7] nt
	global_load_dwordx4 v[158:161], v249, s[6:7] nt
	global_load_dwordx4 v[162:165], v246, s[8:9] nt
	global_load_dwordx4 v[166:169], v247, s[8:9] nt
	global_load_dwordx4 v[170:173], v248, s[8:9] nt
	global_load_dwordx4 v[174:177], v249, s[8:9] nt
	global_load_dwordx4 v[178:181], v246, s[38:39] nt
	global_load_dwordx4 v[182:185], v247, s[38:39] nt
	global_load_dwordx4 v[186:189], v248, s[38:39] nt
	global_load_dwordx4 v[190:193], v249, s[38:39] nt
	s_add_u32 s4, s4, 0x2000000
	s_addc_u32 s5, s5, 0
	s_add_u32 s6, s6, 0x2000000
	s_addc_u32 s7, s7, 0
	s_add_u32 s8, s8, 0x2000000
	s_addc_u32 s9, s9, 0
	s_add_u32 s38, s38, 0x2000000
	s_addc_u32 s39, s39, 0
	s_waitcnt vmcnt(40)
; #define GAS __attribute__((address_space(1)))
; template <bool GAIN, bool NT = false> __device__ __forceinline__ void titem8_load(const TItem& d, int lane, f32x4 (&r)[16], f32x4 (&g)[4]) {
;     const int q = lane & 7, kg = lane >> 3; const unsigned lo = (unsigned)((16 * kg) * d.N + 4 * q) * 4u;
;     const GAS char* base = (const GAS char*)d.src;
; #pragma unroll
;     for (int j = 0; j < 16; ++j) { const GAS f32x4* p = (const GAS f32x4*)(base + (size_t)j * (size_t)d.N * 4 + lo); r[j] = NT ? __builtin_nontemporal_load(p) : *p; }
;     if constexpr (GAIN) { const GAS char* gb = (const GAS char*)d.gain; const unsigned go = (unsigned)(16 * kg) * 4u;
; #pragma unroll
;         for (int j4 = 0; j4 < 4; ++j4) g[j4] = *(const GAS f32x4*)(gb + 16 * j4 + go); }
;     asm volatile("" ::: "memory"); __builtin_amdgcn_sched_barrier(0);
; }
; template <bool GAIN, bool NT = false> __device__ __forceinline__ void titem8_store(const TItem& d, int lane, const f32x4 (&r)[16], const f32x4 (&g)[4]) {
;     const int q = lane & 7, kg = lane >> 3; const unsigned lo = (unsigned)((4 * q) * d.ldk + 16 * kg);
;     GAS char* base = (GAS char*)d.dst;
;     f32x4 s[16];
; #pragma unroll
;     for (int j = 0; j < 16; ++j) s[j] = r[j] * ((GAIN ? g[j >> 2][j & 3] : 1.0f) * W8_SCALE);
; #pragma unroll
;     for (int i = 0; i < 4; ++i) { v4u w;
;         w.x = pk4_fp8w(s[0][i], s[1][i], s[2][i], s[3][i]); w.y = pk4_fp8w(s[4][i], s[5][i], s[6][i], s[7][i]);
;         w.z = pk4_fp8w(s[8][i], s[9][i], s[10][i], s[11][i]); w.w = pk4_fp8w(s[12][i], s[13][i], s[14][i], s[15][i]);
;         GAS v4u* p = (GAS v4u*)(base + (size_t)i * (size_t)d.ldk + lo);
;         if (NT) __builtin_nontemporal_store(w, p); else *p = w; }
; }
	v_pk_mul_f32 v[0:1], v[0:1], s[30:31] op_sel_hi:[1,0]
	v_pk_mul_f32 v[2:3], v[2:3], s[30:31] op_sel_hi:[1,0]
	v_pk_mul_f32 v[4:5], v[4:5], s[30:31] op_sel_hi:[1,0]
	v_pk_mul_f32 v[6:7], v[6:7], s[30:31] op_sel_hi:[1,0]
	v_pk_mul_f32 v[8:9], v[8:9], s[30:31] op_sel_hi:[1,0]
	v_pk_mul_f32 v[10:11], v[10:11], s[30:31] op_sel_hi:[1,0]
	v_pk_mul_f32 v[12:13], v[12:13], s[30:31] op_sel_hi:[1,0]
	v_pk_mul_f32 v[14:15], v[14:15], s[30:31] op_sel_hi:[1,0]
	v_pk_mul_f32 v[16:17], v[16:17], s[30:31] op_sel_hi:[1,0]
	v_pk_mul_f32 v[18:19], v[18:19], s[30:31] op_sel_hi:[1,0]
	v_pk_mul_f32 v[20:21], v[20:21], s[30:31] op_sel_hi:[1,0]
	v_pk_mul_f32 v[22:23], v[22:23], s[30:31] op_sel_hi:[1,0]
	v_pk_mul_f32 v[24:25], v[24:25], s[30:31] op_sel_hi:[1,0]
	v_pk_mul_f32 v[26:27], v[26:27], s[30:31] op_sel_hi:[1,0]
	v_pk_mul_f32 v[28:29], v[28:29], s[30:31] op_sel_hi:[1,0]
	v_pk_mul_f32 v[30:31], v[30:31], s[30:31] op_sel_hi:[1,0]
	v_pk_mul_f32 v[32:33], v[32:33], s[30:31] op_sel_hi:[1,0]
	v_pk_mul_f32 v[34:35], v[34:35], s[30:31] op_sel_hi:[1,0]
	v_pk_mul_f32 v[36:37], v[36:37], s[30:31] op_sel_hi:[1,0]
	v_pk_mul_f32 v[38:39], v[38:39], s[30:31] op_sel_hi:[1,0]
	v_pk_mul_f32 v[40:41], v[40:41], s[30:31] op_sel_hi:[1,0]
	v_pk_mul_f32 v[42:43], v[42:43], s[30:31] op_sel_hi:[1,0]
	v_pk_mul_f32 v[44:45], v[44:45], s[30:31] op_sel_hi:[1,0]
	v_pk_mul_f32 v[46:47], v[46:47], s[30:31] op_sel_hi:[1,0]
	v_pk_mul_f32 v[48:49], v[48:49], s[30:31] op_sel_hi:[1,0]
	v_pk_mul_f32 v[50:51], v[50:51], s[30:31] op_sel_hi:[1,0]
	v_pk_mul_f32 v[52:53], v[52:53], s[30:31] op_sel_hi:[1,0]
	v_pk_mul_f32 v[54:55], v[54:55], s[30:31] op_sel_hi:[1,0]
	v_pk_mul_f32 v[56:57], v[56:57], s[30:31] op_sel_hi:[1,0]
	v_pk_mul_f32 v[58:59], v[58:59], s[30:31] op_sel_hi:[1,0]
	v_pk_mul_f32 v[60:61], v[60:61], s[30:31] op_sel_hi:[1,0]
	v_pk_mul_f32 v[62:63], v[62:63], s[30:31] op_sel_hi:[1,0]
	v_med3_f32 v0, v0, s24, v237
	v_med3_f32 v1, v1, s24, v237
	v_med3_f32 v2, v2, s24, v237
	v_med3_f32 v3, v3, s24, v237
	v_med3_f32 v4, v4, s24, v237
	v_med3_f32 v5, v5, s24, v237
	v_med3_f32 v6, v6, s24, v237
	v_med3_f32 v7, v7, s24, v237
	v_med3_f32 v8, v8, s24, v237
	v_med3_f32 v9, v9, s24, v237
	v_med3_f32 v10, v10, s24, v237
	v_med3_f32 v11, v11, s24, v237
	v_med3_f32 v12, v12, s24, v237
	v_med3_f32 v13, v13, s24, v237
	v_med3_f32 v14, v14, s24, v237
	v_med3_f32 v15, v15, s24, v237
	v_med3_f32 v16, v16, s24, v237
	v_med3_f32 v17, v17, s24, v237
	v_med3_f32 v18, v18, s24, v237
	v_med3_f32 v19, v19, s24, v237
	v_med3_f32 v20, v20, s24, v237
	v_med3_f32 v21, v21, s24, v237
	v_med3_f32 v22, v22, s24, v237
	v_med3_f32 v23, v23, s24, v237
	v_med3_f32 v24, v24, s24, v237
	v_med3_f32 v25, v25, s24, v237
	v_med3_f32 v26, v26, s24, v237
	v_med3_f32 v27, v27, s24, v237
	v_med3_f32 v28, v28, s24, v237
	v_med3_f32 v29, v29, s24, v237
	v_med3_f32 v30, v30, s24, v237
	v_med3_f32 v31, v31, s24, v237
	v_med3_f32 v32, v32, s24, v237
	v_med3_f32 v33, v33, s24, v237
	v_med3_f32 v34, v34, s24, v237
	v_med3_f32 v35, v35, s24, v237
	v_med3_f32 v36, v36, s24, v237
	v_med3_f32 v37, v37, s24, v237
	v_med3_f32 v38, v38, s24, v237
	v_med3_f32 v39, v39, s24, v237
	v_med3_f32 v40, v40, s24, v237
	v_med3_f32 v41, v41, s24, v237
	v_med3_f32 v42, v42, s24, v237
	v_med3_f32 v43, v43, s24, v237
	v_med3_f32 v44, v44, s24, v237
	v_med3_f32 v45, v45, s24, v237
	v_med3_f32 v46, v46, s24, v237
	v_med3_f32 v47, v47, s24, v237
	v_med3_f32 v48, v48, s24, v237
	v_med3_f32 v49, v49, s24, v237
	v_med3_f32 v50, v50, s24, v237
	v_med3_f32 v51, v51, s24, v237
	v_med3_f32 v52, v52, s24, v237
	v_med3_f32 v53, v53, s24, v237
	v_med3_f32 v54, v54, s24, v237
	v_med3_f32 v55, v55, s24, v237
	v_med3_f32 v56, v56, s24, v237
	v_med3_f32 v57, v57, s24, v237
	v_med3_f32 v58, v58, s24, v237
	v_med3_f32 v59, v59, s24, v237
	v_med3_f32 v60, v60, s24, v237
	v_med3_f32 v61, v61, s24, v237
	v_med3_f32 v62, v62, s24, v237
	v_med3_f32 v63, v63, s24, v237
	v_cvt_pk_fp8_f32 v0, v0, v4
	v_cvt_pk_fp8_f32 v0, v8, v12 op_sel:[0,0,1]
	v_cvt_pk_fp8_f32 v4, v1, v5
	v_cvt_pk_fp8_f32 v4, v9, v13 op_sel:[0,0,1]
	v_cvt_pk_fp8_f32 v8, v2, v6
	v_cvt_pk_fp8_f32 v8, v10, v14 op_sel:[0,0,1]
	v_cvt_pk_fp8_f32 v12, v3, v7
	v_cvt_pk_fp8_f32 v12, v11, v15 op_sel:[0,0,1]
	v_cvt_pk_fp8_f32 v1, v16, v20
	v_cvt_pk_fp8_f32 v1, v24, v28 op_sel:[0,0,1]
	v_cvt_pk_fp8_f32 v5, v17, v21
	v_cvt_pk_fp8_f32 v5, v25, v29 op_sel:[0,0,1]
	v_cvt_pk_fp8_f32 v9, v18, v22
	v_cvt_pk_fp8_f32 v9, v26, v30 op_sel:[0,0,1]
	v_cvt_pk_fp8_f32 v13, v19, v23
	v_cvt_pk_fp8_f32 v13, v27, v31 op_sel:[0,0,1]
	v_cvt_pk_fp8_f32 v2, v32, v36
	v_cvt_pk_fp8_f32 v2, v40, v44 op_sel:[0,0,1]
	v_cvt_pk_fp8_f32 v6, v33, v37
	v_cvt_pk_fp8_f32 v6, v41, v45 op_sel:[0,0,1]
	v_cvt_pk_fp8_f32 v10, v34, v38
	v_cvt_pk_fp8_f32 v10, v42, v46 op_sel:[0,0,1]
	v_cvt_pk_fp8_f32 v14, v35, v39
	v_cvt_pk_fp8_f32 v14, v43, v47 op_sel:[0,0,1]
	v_cvt_pk_fp8_f32 v3, v48, v52
	v_cvt_pk_fp8_f32 v3, v56, v60 op_sel:[0,0,1]
	v_cvt_pk_fp8_f32 v7, v49, v53
	v_cvt_pk_fp8_f32 v7, v57, v61 op_sel:[0,0,1]
	v_cvt_pk_fp8_f32 v11, v50, v54
	v_cvt_pk_fp8_f32 v11, v58, v62 op_sel:[0,0,1]
	v_cvt_pk_fp8_f32 v15, v51, v55
	v_cvt_pk_fp8_f32 v15, v59, v63 op_sel:[0,0,1]
	global_store_dwordx4 v250, v[0:3], s[42:43] nt
	global_store_dwordx4 v250, v[4:7], s[42:43] offset:2048 nt
	global_store_dwordx4 v251, v[8:11], s[42:43] nt
	global_store_dwordx4 v251, v[12:15], s[42:43] offset:2048 nt
	s_add_u32 s42, s42, 0x800000
	s_addc_u32 s43, s43, 0
	global_load_dwordx4 v[0:3], v246, s[4:5] nt
	global_load_dwordx4 v[4:7], v247, s[4:5] nt
	global_load_dwordx4 v[8:11], v248, s[4:5] nt
	global_load_dwordx4 v[12:15], v249, s[4:5] nt
	global_load_dwordx4 v[16:19], v246, s[6:7] nt
	global_load_dwordx4 v[20:23], v247, s[6:7] nt
	global_load_dwordx4 v[24:27], v248, s[6:7] nt
	global_load_dwordx4 v[28:31], v249, s[6:7] nt
	global_load_dwordx4 v[32:35], v246, s[8:9] nt
	global_load_dwordx4 v[36:39], v247, s[8:9] nt
	global_load_dwordx4 v[40:43], v248, s[8:9] nt
	global_load_dwordx4 v[44:47], v249, s[8:9] nt
	global_load_dwordx4 v[48:51], v246, s[38:39] nt
	global_load_dwordx4 v[52:55], v247, s[38:39] nt
	global_load_dwordx4 v[56:59], v248, s[38:39] nt
	global_load_dwordx4 v[60:63], v249, s[38:39] nt
	s_add_u32 s4, s4, 0x2000000
	s_addc_u32 s5, s5, 0
	s_add_u32 s6, s6, 0x2000000
	s_addc_u32 s7, s7, 0
	s_add_u32 s8, s8, 0x2000000
	s_addc_u32 s9, s9, 0
	s_add_u32 s38, s38, 0x2000000
	s_addc_u32 s39, s39, 0
	s_waitcnt vmcnt(40)
; #define GAS __attribute__((address_space(1)))
; template <bool GAIN, bool NT = false> __device__ __forceinline__ void titem8_load(const TItem& d, int lane, f32x4 (&r)[16], f32x4 (&g)[4]) {
;     const int q = lane & 7, kg = lane >> 3; const unsigned lo = (unsigned)((16 * kg) * d.N + 4 * q) * 4u;
;     const GAS char* base = (const GAS char*)d.src;
; #pragma unroll
;     for (int j = 0; j < 16; ++j) { const GAS f32x4* p = (const GAS f32x4*)(base + (size_t)j * (size_t)d.N * 4 + lo); r[j] = NT ? __builtin_nontemporal_load(p) : *p; }
;     if constexpr (GAIN) { const GAS char* gb = (const GAS char*)d.gain; const unsigned go = (unsigned)(16 * kg) * 4u;
; #pragma unroll
;         for (int j4 = 0; j4 < 4; ++j4) g[j4] = *(const GAS f32x4*)(gb + 16 * j4 + go); }
;     asm volatile("" ::: "memory"); __builtin_amdgcn_sched_barrier(0);
; }
; template <bool GAIN, bool NT = false> __device__ __forceinline__ void titem8_store(const TItem& d, int lane, const f32x4 (&r)[16], const f32x4 (&g)[4]) {
;     const int q = lane & 7, kg = lane >> 3; const unsigned lo = (unsigned)((4 * q) * d.ldk + 16 * kg);
;     GAS char* base = (GAS char*)d.dst;
;     f32x4 s[16];
; #pragma unroll
;     for (int j = 0; j < 16; ++j) s[j] = r[j] * ((GAIN ? g[j >> 2][j & 3] : 1.0f) * W8_SCALE);
; #pragma unroll
;     for (int i = 0; i < 4; ++i) { v4u w;
;         w.x = pk4_fp8w(s[0][i], s[1][i], s[2][i], s[3][i]); w.y = pk4_fp8w(s[4][i], s[5][i], s[6][i], s[7][i]);
;         w.z = pk4_fp8w(s[8][i], s[9][i], s[10][i], s[11][i]); w.w = pk4_fp8w(s[12][i], s[13][i], s[14][i], s[15][i]);
;         GAS v4u* p = (GAS v4u*)(base + (size_t)i * (size_t)d.ldk + lo);
;         if (NT) __builtin_nontemporal_store(w, p); else *p = w; }
; }
	v_pk_mul_f32 v[66:67], v[66:67], s[30:31] op_sel_hi:[1,0]
	v_pk_mul_f32 v[68:69], v[68:69], s[30:31] op_sel_hi:[1,0]
	v_pk_mul_f32 v[70:71], v[70:71], s[30:31] op_sel_hi:[1,0]
	v_pk_mul_f32 v[72:73], v[72:73], s[30:31] op_sel_hi:[1,0]
	v_pk_mul_f32 v[74:75], v[74:75], s[30:31] op_sel_hi:[1,0]
	v_pk_mul_f32 v[76:77], v[76:77], s[30:31] op_sel_hi:[1,0]
	v_pk_mul_f32 v[78:79], v[78:79], s[30:31] op_sel_hi:[1,0]
	v_pk_mul_f32 v[80:81], v[80:81], s[30:31] op_sel_hi:[1,0]
	v_pk_mul_f32 v[82:83], v[82:83], s[30:31] op_sel_hi:[1,0]
	v_pk_mul_f32 v[84:85], v[84:85], s[30:31] op_sel_hi:[1,0]
	v_pk_mul_f32 v[86:87], v[86:87], s[30:31] op_sel_hi:[1,0]
	v_pk_mul_f32 v[88:89], v[88:89], s[30:31] op_sel_hi:[1,0]
	v_pk_mul_f32 v[90:91], v[90:91], s[30:31] op_sel_hi:[1,0]
	v_pk_mul_f32 v[92:93], v[92:93], s[30:31] op_sel_hi:[1,0]
	v_pk_mul_f32 v[94:95], v[94:95], s[30:31] op_sel_hi:[1,0]
	v_pk_mul_f32 v[96:97], v[96:97], s[30:31] op_sel_hi:[1,0]
	v_pk_mul_f32 v[98:99], v[98:99], s[30:31] op_sel_hi:[1,0]
	v_pk_mul_f32 v[100:101], v[100:101], s[30:31] op_sel_hi:[1,0]
	v_pk_mul_f32 v[102:103], v[102:103], s[30:31] op_sel_hi:[1,0]
	v_pk_mul_f32 v[104:105], v[104:105], s[30:31] op_sel_hi:[1,0]
	v_pk_mul_f32 v[106:107], v[106:107], s[30:31] op_sel_hi:[1,0]
	v_pk_mul_f32 v[108:109], v[108:109], s[30:31] op_sel_hi:[1,0]
	v_pk_mul_f32 v[110:111], v[110:111], s[30:31] op_sel_hi:[1,0]
	v_pk_mul_f32 v[112:113], v[112:113], s[30:31] op_sel_hi:[1,0]
	v_pk_mul_f32 v[114:115], v[114:115], s[30:31] op_sel_hi:[1,0]
	v_pk_mul_f32 v[116:117], v[116:117], s[30:31] op_sel_hi:[1,0]
	v_pk_mul_f32 v[118:119], v[118:119], s[30:31] op_sel_hi:[1,0]
	v_pk_mul_f32 v[120:121], v[120:121], s[30:31] op_sel_hi:[1,0]
	v_pk_mul_f32 v[122:123], v[122:123], s[30:31] op_sel_hi:[1,0]
	v_pk_mul_f32 v[124:125], v[124:125], s[30:31] op_sel_hi:[1,0]
	v_pk_mul_f32 v[126:127], v[126:127], s[30:31] op_sel_hi:[1,0]
	v_pk_mul_f32 v[128:129], v[128:129], s[30:31] op_sel_hi:[1,0]
	v_med3_f32 v66, v66, s24, v237
	v_med3_f32 v67, v67, s24, v237
	v_med3_f32 v68, v68, s24, v237
	v_med3_f32 v69, v69, s24, v237
	v_med3_f32 v70, v70, s24, v237
	v_med3_f32 v71, v71, s24, v237
	v_med3_f32 v72, v72, s24, v237
	v_med3_f32 v73, v73, s24, v237
	v_med3_f32 v74, v74, s24, v237
	v_med3_f32 v75, v75, s24, v237
	v_med3_f32 v76, v76, s24, v237
	v_med3_f32 v77, v77, s24, v237
	v_med3_f32 v78, v78, s24, v237
	v_med3_f32 v79, v79, s24, v237
	v_med3_f32 v80, v80, s24, v237
	v_med3_f32 v81, v81, s24, v237
	v_med3_f32 v82, v82, s24, v237
	v_med3_f32 v83, v83, s24, v237
	v_med3_f32 v84, v84, s24, v237
	v_med3_f32 v85, v85, s24, v237
	v_med3_f32 v86, v86, s24, v237
	v_med3_f32 v87, v87, s24, v237
	v_med3_f32 v88, v88, s24, v237
	v_med3_f32 v89, v89, s24, v237
	v_med3_f32 v90, v90, s24, v237
	v_med3_f32 v91, v91, s24, v237
	v_med3_f32 v92, v92, s24, v237
	v_med3_f32 v93, v93, s24, v237
	v_med3_f32 v94, v94, s24, v237
	v_med3_f32 v95, v95, s24, v237
	v_med3_f32 v96, v96, s24, v237
	v_med3_f32 v97, v97, s24, v237
	v_med3_f32 v98, v98, s24, v237
	v_med3_f32 v99, v99, s24, v237
	v_med3_f32 v100, v100, s24, v237
	v_med3_f32 v101, v101, s24, v237
	v_med3_f32 v102, v102, s24, v237
	v_med3_f32 v103, v103, s24, v237
	v_med3_f32 v104, v104, s24, v237
	v_med3_f32 v105, v105, s24, v237
	v_med3_f32 v106, v106, s24, v237
	v_med3_f32 v107, v107, s24, v237
	v_med3_f32 v108, v108, s24, v237
	v_med3_f32 v109, v109, s24, v237
	v_med3_f32 v110, v110, s24, v237
	v_med3_f32 v111, v111, s24, v237
	v_med3_f32 v112, v112, s24, v237
	v_med3_f32 v113, v113, s24, v237
	v_med3_f32 v114, v114, s24, v237
	v_med3_f32 v115, v115, s24, v237
	v_med3_f32 v116, v116, s24, v237
	v_med3_f32 v117, v117, s24, v237
	v_med3_f32 v118, v118, s24, v237
	v_med3_f32 v119, v119, s24, v237
	v_med3_f32 v120, v120, s24, v237
	v_med3_f32 v121, v121, s24, v237
	v_med3_f32 v122, v122, s24, v237
	v_med3_f32 v123, v123, s24, v237
	v_med3_f32 v124, v124, s24, v237
	v_med3_f32 v125, v125, s24, v237
	v_med3_f32 v126, v126, s24, v237
	v_med3_f32 v127, v127, s24, v237
	v_med3_f32 v128, v128, s24, v237
	v_med3_f32 v129, v129, s24, v237
	v_cvt_pk_fp8_f32 v66, v66, v70
	v_cvt_pk_fp8_f32 v66, v74, v78 op_sel:[0,0,1]
	v_cvt_pk_fp8_f32 v70, v67, v71
	v_cvt_pk_fp8_f32 v70, v75, v79 op_sel:[0,0,1]
	v_cvt_pk_fp8_f32 v74, v68, v72
	v_cvt_pk_fp8_f32 v74, v76, v80 op_sel:[0,0,1]
	v_cvt_pk_fp8_f32 v78, v69, v73
	v_cvt_pk_fp8_f32 v78, v77, v81 op_sel:[0,0,1]
	v_cvt_pk_fp8_f32 v67, v82, v86
	v_cvt_pk_fp8_f32 v67, v90, v94 op_sel:[0,0,1]
	v_cvt_pk_fp8_f32 v71, v83, v87
	v_cvt_pk_fp8_f32 v71, v91, v95 op_sel:[0,0,1]
	v_cvt_pk_fp8_f32 v75, v84, v88
	v_cvt_pk_fp8_f32 v75, v92, v96 op_sel:[0,0,1]
	v_cvt_pk_fp8_f32 v79, v85, v89
	v_cvt_pk_fp8_f32 v79, v93, v97 op_sel:[0,0,1]
	v_cvt_pk_fp8_f32 v68, v98, v102
	v_cvt_pk_fp8_f32 v68, v106, v110 op_sel:[0,0,1]
	v_cvt_pk_fp8_f32 v72, v99, v103
	v_cvt_pk_fp8_f32 v72, v107, v111 op_sel:[0,0,1]
	v_cvt_pk_fp8_f32 v76, v100, v104
	v_cvt_pk_fp8_f32 v76, v108, v112 op_sel:[0,0,1]
	v_cvt_pk_fp8_f32 v80, v101, v105
	v_cvt_pk_fp8_f32 v80, v109, v113 op_sel:[0,0,1]
	v_cvt_pk_fp8_f32 v69, v114, v118
	v_cvt_pk_fp8_f32 v69, v122, v126 op_sel:[0,0,1]
	v_cvt_pk_fp8_f32 v73, v115, v119
	v_cvt_pk_fp8_f32 v73, v123, v127 op_sel:[0,0,1]
	v_cvt_pk_fp8_f32 v77, v116, v120
	v_cvt_pk_fp8_f32 v77, v124, v128 op_sel:[0,0,1]
	v_cvt_pk_fp8_f32 v81, v117, v121
	v_cvt_pk_fp8_f32 v81, v125, v129 op_sel:[0,0,1]
	global_store_dwordx4 v250, v[66:69], s[42:43] nt
	global_store_dwordx4 v250, v[70:73], s[42:43] offset:2048 nt
	global_store_dwordx4 v251, v[74:77], s[42:43] nt
	global_store_dwordx4 v251, v[78:81], s[42:43] offset:2048 nt
	s_add_u32 s42, s42, 0x800000
	s_addc_u32 s43, s43, 0
	global_load_dwordx4 v[66:69], v246, s[4:5] nt
	global_load_dwordx4 v[70:73], v247, s[4:5] nt
	global_load_dwordx4 v[74:77], v248, s[4:5] nt
	global_load_dwordx4 v[78:81], v249, s[4:5] nt
	global_load_dwordx4 v[82:85], v246, s[6:7] nt
	global_load_dwordx4 v[86:89], v247, s[6:7] nt
	global_load_dwordx4 v[90:93], v248, s[6:7] nt
	global_load_dwordx4 v[94:97], v249, s[6:7] nt
	global_load_dwordx4 v[98:101], v246, s[8:9] nt
	global_load_dwordx4 v[102:105], v247, s[8:9] nt
	global_load_dwordx4 v[106:109], v248, s[8:9] nt
	global_load_dwordx4 v[110:113], v249, s[8:9] nt
	global_load_dwordx4 v[114:117], v246, s[38:39] nt
	global_load_dwordx4 v[118:121], v247, s[38:39] nt
	global_load_dwordx4 v[122:125], v248, s[38:39] nt
	global_load_dwordx4 v[126:129], v249, s[38:39] nt
	s_add_u32 s4, s4, 0x2000000
	s_addc_u32 s5, s5, 0
	s_add_u32 s6, s6, 0x2000000
	s_addc_u32 s7, s7, 0
	s_add_u32 s8, s8, 0x2000000
	s_addc_u32 s9, s9, 0
	s_add_u32 s38, s38, 0x2000000
	s_addc_u32 s39, s39, 0
	s_waitcnt vmcnt(40)
; #define GAS __attribute__((address_space(1)))
; template <bool GAIN, bool NT = false> __device__ __forceinline__ void titem8_load(const TItem& d, int lane, f32x4 (&r)[16], f32x4 (&g)[4]) {
;     const int q = lane & 7, kg = lane >> 3; const unsigned lo = (unsigned)((16 * kg) * d.N + 4 * q) * 4u;
;     const GAS char* base = (const GAS char*)d.src;
; #pragma unroll
;     for (int j = 0; j < 16; ++j) { const GAS f32x4* p = (const GAS f32x4*)(base + (size_t)j * (size_t)d.N * 4 + lo); r[j] = NT ? __builtin_nontemporal_load(p) : *p; }
;     if constexpr (GAIN) { const GAS char* gb = (const GAS char*)d.gain; const unsigned go = (unsigned)(16 * kg) * 4u;
; #pragma unroll
;         for (int j4 = 0; j4 < 4; ++j4) g[j4] = *(const GAS f32x4*)(gb + 16 * j4 + go); }
;     asm volatile("" ::: "memory"); __builtin_amdgcn_sched_barrier(0);
; }
; template <bool GAIN, bool NT = false> __device__ __forceinline__ void titem8_store(const TItem& d, int lane, const f32x4 (&r)[16], const f32x4 (&g)[4]) {
;     const int q = lane & 7, kg = lane >> 3; const unsigned lo = (unsigned)((4 * q) * d.ldk + 16 * kg);
;     GAS char* base = (GAS char*)d.dst;
;     f32x4 s[16];
; #pragma unroll
;     for (int j = 0; j < 16; ++j) s[j] = r[j] * ((GAIN ? g[j >> 2][j & 3] : 1.0f) * W8_SCALE);
; #pragma unroll
;     for (int i = 0; i < 4; ++i) { v4u w;
;         w.x = pk4_fp8w(s[0][i], s[1][i], s[2][i], s[3][i]); w.y = pk4_fp8w(s[4][i], s[5][i], s[6][i], s[7][i]);
;         w.z = pk4_fp8w(s[8][i], s[9][i], s[10][i], s[11][i]); w.w = pk4_fp8w(s[12][i], s[13][i], s[14][i], s[15][i]);
;         GAS v4u* p = (GAS v4u*)(base + (size_t)i * (size_t)d.ldk + lo);
;         if (NT) __builtin_nontemporal_store(w, p); else *p = w; }
; }
	v_pk_mul_f32 v[130:131], v[130:131], s[30:31] op_sel_hi:[1,0]
	v_pk_mul_f32 v[132:133], v[132:133], s[30:31] op_sel_hi:[1,0]
	v_pk_mul_f32 v[134:135], v[134:135], s[30:31] op_sel_hi:[1,0]
	v_pk_mul_f32 v[136:137], v[136:137], s[30:31] op_sel_hi:[1,0]
	v_pk_mul_f32 v[138:139], v[138:139], s[30:31] op_sel_hi:[1,0]
	v_pk_mul_f32 v[140:141], v[140:141], s[30:31] op_sel_hi:[1,0]
	v_pk_mul_f32 v[142:143], v[142:143], s[30:31] op_sel_hi:[1,0]
	v_pk_mul_f32 v[144:145], v[144:145], s[30:31] op_sel_hi:[1,0]
	v_pk_mul_f32 v[146:147], v[146:147], s[30:31] op_sel_hi:[1,0]
	v_pk_mul_f32 v[148:149], v[148:149], s[30:31] op_sel_hi:[1,0]
	v_pk_mul_f32 v[150:151], v[150:151], s[30:31] op_sel_hi:[1,0]
	v_pk_mul_f32 v[152:153], v[152:153], s[30:31] op_sel_hi:[1,0]
	v_pk_mul_f32 v[154:155], v[154:155], s[30:31] op_sel_hi:[1,0]
	v_pk_mul_f32 v[156:157], v[156:157], s[30:31] op_sel_hi:[1,0]
	v_pk_mul_f32 v[158:159], v[158:159], s[30:31] op_sel_hi:[1,0]
	v_pk_mul_f32 v[160:161], v[160:161], s[30:31] op_sel_hi:[1,0]
	v_pk_mul_f32 v[162:163], v[162:163], s[30:31] op_sel_hi:[1,0]
	v_pk_mul_f32 v[164:165], v[164:165], s[30:31] op_sel_hi:[1,0]
	v_pk_mul_f32 v[166:167], v[166:167], s[30:31] op_sel_hi:[1,0]
	v_pk_mul_f32 v[168:169], v[168:169], s[30:31] op_sel_hi:[1,0]
	v_pk_mul_f32 v[170:171], v[170:171], s[30:31] op_sel_hi:[1,0]
	v_pk_mul_f32 v[172:173], v[172:173], s[30:31] op_sel_hi:[1,0]
	v_pk_mul_f32 v[174:175], v[174:175], s[30:31] op_sel_hi:[1,0]
	v_pk_mul_f32 v[176:177], v[176:177], s[30:31] op_sel_hi:[1,0]
	v_pk_mul_f32 v[178:179], v[178:179], s[30:31] op_sel_hi:[1,0]
	v_pk_mul_f32 v[180:181], v[180:181], s[30:31] op_sel_hi:[1,0]
	v_pk_mul_f32 v[182:183], v[182:183], s[30:31] op_sel_hi:[1,0]
	v_pk_mul_f32 v[184:185], v[184:185], s[30:31] op_sel_hi:[1,0]
	v_pk_mul_f32 v[186:187], v[186:187], s[30:31] op_sel_hi:[1,0]
	v_pk_mul_f32 v[188:189], v[188:189], s[30:31] op_sel_hi:[1,0]
	v_pk_mul_f32 v[190:191], v[190:191], s[30:31] op_sel_hi:[1,0]
	v_pk_mul_f32 v[192:193], v[192:193], s[30:31] op_sel_hi:[1,0]
	v_med3_f32 v130, v130, s24, v237
	v_med3_f32 v131, v131, s24, v237
	v_med3_f32 v132, v132, s24, v237
	v_med3_f32 v133, v133, s24, v237
	v_med3_f32 v134, v134, s24, v237
	v_med3_f32 v135, v135, s24, v237
	v_med3_f32 v136, v136, s24, v237
	v_med3_f32 v137, v137, s24, v237
	v_med3_f32 v138, v138, s24, v237
	v_med3_f32 v139, v139, s24, v237
	v_med3_f32 v140, v140, s24, v237
	v_med3_f32 v141, v141, s24, v237
	v_med3_f32 v142, v142, s24, v237
	v_med3_f32 v143, v143, s24, v237
	v_med3_f32 v144, v144, s24, v237
	v_med3_f32 v145, v145, s24, v237
	v_med3_f32 v146, v146, s24, v237
	v_med3_f32 v147, v147, s24, v237
	v_med3_f32 v148, v148, s24, v237
	v_med3_f32 v149, v149, s24, v237
	v_med3_f32 v150, v150, s24, v237
	v_med3_f32 v151, v151, s24, v237
	v_med3_f32 v152, v152, s24, v237
	v_med3_f32 v153, v153, s24, v237
	v_med3_f32 v154, v154, s24, v237
	v_med3_f32 v155, v155, s24, v237
	v_med3_f32 v156, v156, s24, v237
	v_med3_f32 v157, v157, s24, v237
	v_med3_f32 v158, v158, s24, v237
	v_med3_f32 v159, v159, s24, v237
	v_med3_f32 v160, v160, s24, v237
	v_med3_f32 v161, v161, s24, v237
	v_med3_f32 v162, v162, s24, v237
	v_med3_f32 v163, v163, s24, v237
	v_med3_f32 v164, v164, s24, v237
	v_med3_f32 v165, v165, s24, v237
	v_med3_f32 v166, v166, s24, v237
	v_med3_f32 v167, v167, s24, v237
	v_med3_f32 v168, v168, s24, v237
	v_med3_f32 v169, v169, s24, v237
	v_med3_f32 v170, v170, s24, v237
	v_med3_f32 v171, v171, s24, v237
	v_med3_f32 v172, v172, s24, v237
	v_med3_f32 v173, v173, s24, v237
	v_med3_f32 v174, v174, s24, v237
	v_med3_f32 v175, v175, s24, v237
	v_med3_f32 v176, v176, s24, v237
	v_med3_f32 v177, v177, s24, v237
	v_med3_f32 v178, v178, s24, v237
	v_med3_f32 v179, v179, s24, v237
	v_med3_f32 v180, v180, s24, v237
	v_med3_f32 v181, v181, s24, v237
	v_med3_f32 v182, v182, s24, v237
	v_med3_f32 v183, v183, s24, v237
	v_med3_f32 v184, v184, s24, v237
	v_med3_f32 v185, v185, s24, v237
	v_med3_f32 v186, v186, s24, v237
	v_med3_f32 v187, v187, s24, v237
	v_med3_f32 v188, v188, s24, v237
	v_med3_f32 v189, v189, s24, v237
	v_med3_f32 v190, v190, s24, v237
	v_med3_f32 v191, v191, s24, v237
	v_med3_f32 v192, v192, s24, v237
	v_med3_f32 v193, v193, s24, v237
	v_cvt_pk_fp8_f32 v130, v130, v134
	v_cvt_pk_fp8_f32 v130, v138, v142 op_sel:[0,0,1]
	v_cvt_pk_fp8_f32 v134, v131, v135
	v_cvt_pk_fp8_f32 v134, v139, v143 op_sel:[0,0,1]
	v_cvt_pk_fp8_f32 v138, v132, v136
	v_cvt_pk_fp8_f32 v138, v140, v144 op_sel:[0,0,1]
	v_cvt_pk_fp8_f32 v142, v133, v137
	v_cvt_pk_fp8_f32 v142, v141, v145 op_sel:[0,0,1]
	v_cvt_pk_fp8_f32 v131, v146, v150
	v_cvt_pk_fp8_f32 v131, v154, v158 op_sel:[0,0,1]
	v_cvt_pk_fp8_f32 v135, v147, v151
	v_cvt_pk_fp8_f32 v135, v155, v159 op_sel:[0,0,1]
	v_cvt_pk_fp8_f32 v139, v148, v152
	v_cvt_pk_fp8_f32 v139, v156, v160 op_sel:[0,0,1]
	v_cvt_pk_fp8_f32 v143, v149, v153
	v_cvt_pk_fp8_f32 v143, v157, v161 op_sel:[0,0,1]
	v_cvt_pk_fp8_f32 v132, v162, v166
	v_cvt_pk_fp8_f32 v132, v170, v174 op_sel:[0,0,1]
	v_cvt_pk_fp8_f32 v136, v163, v167
	v_cvt_pk_fp8_f32 v136, v171, v175 op_sel:[0,0,1]
	v_cvt_pk_fp8_f32 v140, v164, v168
	v_cvt_pk_fp8_f32 v140, v172, v176 op_sel:[0,0,1]
	v_cvt_pk_fp8_f32 v144, v165, v169
	v_cvt_pk_fp8_f32 v144, v173, v177 op_sel:[0,0,1]
	v_cvt_pk_fp8_f32 v133, v178, v182
	v_cvt_pk_fp8_f32 v133, v186, v190 op_sel:[0,0,1]
	v_cvt_pk_fp8_f32 v137, v179, v183
	v_cvt_pk_fp8_f32 v137, v187, v191 op_sel:[0,0,1]
	v_cvt_pk_fp8_f32 v141, v180, v184
	v_cvt_pk_fp8_f32 v141, v188, v192 op_sel:[0,0,1]
	v_cvt_pk_fp8_f32 v145, v181, v185
	v_cvt_pk_fp8_f32 v145, v189, v193 op_sel:[0,0,1]
	global_store_dwordx4 v250, v[130:133], s[42:43] nt
	global_store_dwordx4 v250, v[134:137], s[42:43] offset:2048 nt
	global_store_dwordx4 v251, v[138:141], s[42:43] nt
	global_store_dwordx4 v251, v[142:145], s[42:43] offset:2048 nt
	s_add_u32 s42, s42, 0x800000
	s_addc_u32 s43, s43, 0
	global_load_dwordx4 v[130:133], v246, s[4:5] nt
	global_load_dwordx4 v[134:137], v247, s[4:5] nt
	global_load_dwordx4 v[138:141], v248, s[4:5] nt
	global_load_dwordx4 v[142:145], v249, s[4:5] nt
	global_load_dwordx4 v[146:149], v246, s[6:7] nt
	global_load_dwordx4 v[150:153], v247, s[6:7] nt
	global_load_dwordx4 v[154:157], v248, s[6:7] nt
	global_load_dwordx4 v[158:161], v249, s[6:7] nt
	global_load_dwordx4 v[162:165], v246, s[8:9] nt
	global_load_dwordx4 v[166:169], v247, s[8:9] nt
	global_load_dwordx4 v[170:173], v248, s[8:9] nt
	global_load_dwordx4 v[174:177], v249, s[8:9] nt
	global_load_dwordx4 v[178:181], v246, s[38:39] nt
	global_load_dwordx4 v[182:185], v247, s[38:39] nt
	global_load_dwordx4 v[186:189], v248, s[38:39] nt
	global_load_dwordx4 v[190:193], v249, s[38:39] nt
	s_add_u32 s4, s4, 0x2000000
	s_addc_u32 s5, s5, 0
	s_add_u32 s6, s6, 0x2000000
	s_addc_u32 s7, s7, 0
	s_add_u32 s8, s8, 0x2000000
	s_addc_u32 s9, s9, 0
	s_add_u32 s38, s38, 0x2000000
	s_addc_u32 s39, s39, 0
	s_waitcnt vmcnt(40)
; #define GAS __attribute__((address_space(1)))
; template <bool GAIN, bool NT = false> __device__ __forceinline__ void titem8_load(const TItem& d, int lane, f32x4 (&r)[16], f32x4 (&g)[4]) {
;     const int q = lane & 7, kg = lane >> 3; const unsigned lo = (unsigned)((16 * kg) * d.N + 4 * q) * 4u;
;     const GAS char* base = (const GAS char*)d.src;
; #pragma unroll
;     for (int j = 0; j < 16; ++j) { const GAS f32x4* p = (const GAS f32x4*)(base + (size_t)j * (size_t)d.N * 4 + lo); r[j] = NT ? __builtin_nontemporal_load(p) : *p; }
;     if constexpr (GAIN) { const GAS char* gb = (const GAS char*)d.gain; const unsigned go = (unsigned)(16 * kg) * 4u;
; #pragma unroll
;         for (int j4 = 0; j4 < 4; ++j4) g[j4] = *(const GAS f32x4*)(gb + 16 * j4 + go); }
;     asm volatile("" ::: "memory"); __builtin_amdgcn_sched_barrier(0);
; }
; template <bool GAIN, bool NT = false> __device__ __forceinline__ void titem8_store(const TItem& d, int lane, const f32x4 (&r)[16], const f32x4 (&g)[4]) {
;     const int q = lane & 7, kg = lane >> 3; const unsigned lo = (unsigned)((4 * q) * d.ldk + 16 * kg);
;     GAS char* base = (GAS char*)d.dst;
;     f32x4 s[16];
; #pragma unroll
;     for (int j = 0; j < 16; ++j) s[j] = r[j] * ((GAIN ? g[j >> 2][j & 3] : 1.0f) * W8_SCALE);
; #pragma unroll
;     for (int i = 0; i < 4; ++i) { v4u w;
;         w.x = pk4_fp8w(s[0][i], s[1][i], s[2][i], s[3][i]); w.y = pk4_fp8w(s[4][i], s[5][i], s[6][i], s[7][i]);
;         w.z = pk4_fp8w(s[8][i], s[9][i], s[10][i], s[11][i]); w.w = pk4_fp8w(s[12][i], s[13][i], s[14][i], s[15][i]);
;         GAS v4u* p = (GAS v4u*)(base + (size_t)i * (size_t)d.ldk + lo);
;         if (NT) __builtin_nontemporal_store(w, p); else *p = w; }
; }
	v_pk_mul_f32 v[0:1], v[0:1], s[30:31] op_sel_hi:[1,0]
	v_pk_mul_f32 v[2:3], v[2:3], s[30:31] op_sel_hi:[1,0]
	v_pk_mul_f32 v[4:5], v[4:5], s[30:31] op_sel_hi:[1,0]
	v_pk_mul_f32 v[6:7], v[6:7], s[30:31] op_sel_hi:[1,0]
	v_pk_mul_f32 v[8:9], v[8:9], s[30:31] op_sel_hi:[1,0]
	v_pk_mul_f32 v[10:11], v[10:11], s[30:31] op_sel_hi:[1,0]
	v_pk_mul_f32 v[12:13], v[12:13], s[30:31] op_sel_hi:[1,0]
	v_pk_mul_f32 v[14:15], v[14:15], s[30:31] op_sel_hi:[1,0]
	v_pk_mul_f32 v[16:17], v[16:17], s[30:31] op_sel_hi:[1,0]
	v_pk_mul_f32 v[18:19], v[18:19], s[30:31] op_sel_hi:[1,0]
	v_pk_mul_f32 v[20:21], v[20:21], s[30:31] op_sel_hi:[1,0]
	v_pk_mul_f32 v[22:23], v[22:23], s[30:31] op_sel_hi:[1,0]
	v_pk_mul_f32 v[24:25], v[24:25], s[30:31] op_sel_hi:[1,0]
	v_pk_mul_f32 v[26:27], v[26:27], s[30:31] op_sel_hi:[1,0]
	v_pk_mul_f32 v[28:29], v[28:29], s[30:31] op_sel_hi:[1,0]
	v_pk_mul_f32 v[30:31], v[30:31], s[30:31] op_sel_hi:[1,0]
	v_pk_mul_f32 v[32:33], v[32:33], s[30:31] op_sel_hi:[1,0]
	v_pk_mul_f32 v[34:35], v[34:35], s[30:31] op_sel_hi:[1,0]
	v_pk_mul_f32 v[36:37], v[36:37], s[30:31] op_sel_hi:[1,0]
	v_pk_mul_f32 v[38:39], v[38:39], s[30:31] op_sel_hi:[1,0]
	v_pk_mul_f32 v[40:41], v[40:41], s[30:31] op_sel_hi:[1,0]
	v_pk_mul_f32 v[42:43], v[42:43], s[30:31] op_sel_hi:[1,0]
	v_pk_mul_f32 v[44:45], v[44:45], s[30:31] op_sel_hi:[1,0]
	v_pk_mul_f32 v[46:47], v[46:47], s[30:31] op_sel_hi:[1,0]
	v_pk_mul_f32 v[48:49], v[48:49], s[30:31] op_sel_hi:[1,0]
	v_pk_mul_f32 v[50:51], v[50:51], s[30:31] op_sel_hi:[1,0]
	v_pk_mul_f32 v[52:53], v[52:53], s[30:31] op_sel_hi:[1,0]
	v_pk_mul_f32 v[54:55], v[54:55], s[30:31] op_sel_hi:[1,0]
	v_pk_mul_f32 v[56:57], v[56:57], s[30:31] op_sel_hi:[1,0]
	v_pk_mul_f32 v[58:59], v[58:59], s[30:31] op_sel_hi:[1,0]
	v_pk_mul_f32 v[60:61], v[60:61], s[30:31] op_sel_hi:[1,0]
	v_pk_mul_f32 v[62:63], v[62:63], s[30:31] op_sel_hi:[1,0]
	v_med3_f32 v0, v0, s24, v237
	v_med3_f32 v1, v1, s24, v237
	v_med3_f32 v2, v2, s24, v237
	v_med3_f32 v3, v3, s24, v237
	v_med3_f32 v4, v4, s24, v237
	v_med3_f32 v5, v5, s24, v237
	v_med3_f32 v6, v6, s24, v237
	v_med3_f32 v7, v7, s24, v237
	v_med3_f32 v8, v8, s24, v237
	v_med3_f32 v9, v9, s24, v237
	v_med3_f32 v10, v10, s24, v237
	v_med3_f32 v11, v11, s24, v237
	v_med3_f32 v12, v12, s24, v237
	v_med3_f32 v13, v13, s24, v237
	v_med3_f32 v14, v14, s24, v237
	v_med3_f32 v15, v15, s24, v237
	v_med3_f32 v16, v16, s24, v237
	v_med3_f32 v17, v17, s24, v237
	v_med3_f32 v18, v18, s24, v237
	v_med3_f32 v19, v19, s24, v237
	v_med3_f32 v20, v20, s24, v237
	v_med3_f32 v21, v21, s24, v237
	v_med3_f32 v22, v22, s24, v237
	v_med3_f32 v23, v23, s24, v237
	v_med3_f32 v24, v24, s24, v237
	v_med3_f32 v25, v25, s24, v237
	v_med3_f32 v26, v26, s24, v237
	v_med3_f32 v27, v27, s24, v237
	v_med3_f32 v28, v28, s24, v237
	v_med3_f32 v29, v29, s24, v237
	v_med3_f32 v30, v30, s24, v237
	v_med3_f32 v31, v31, s24, v237
	v_med3_f32 v32, v32, s24, v237
	v_med3_f32 v33, v33, s24, v237
	v_med3_f32 v34, v34, s24, v237
	v_med3_f32 v35, v35, s24, v237
	v_med3_f32 v36, v36, s24, v237
	v_med3_f32 v37, v37, s24, v237
	v_med3_f32 v38, v38, s24, v237
	v_med3_f32 v39, v39, s24, v237
	v_med3_f32 v40, v40, s24, v237
	v_med3_f32 v41, v41, s24, v237
	v_med3_f32 v42, v42, s24, v237
	v_med3_f32 v43, v43, s24, v237
	v_med3_f32 v44, v44, s24, v237
	v_med3_f32 v45, v45, s24, v237
	v_med3_f32 v46, v46, s24, v237
	v_med3_f32 v47, v47, s24, v237
	v_med3_f32 v48, v48, s24, v237
	v_med3_f32 v49, v49, s24, v237
	v_med3_f32 v50, v50, s24, v237
	v_med3_f32 v51, v51, s24, v237
	v_med3_f32 v52, v52, s24, v237
	v_med3_f32 v53, v53, s24, v237
	v_med3_f32 v54, v54, s24, v237
	v_med3_f32 v55, v55, s24, v237
	v_med3_f32 v56, v56, s24, v237
	v_med3_f32 v57, v57, s24, v237
	v_med3_f32 v58, v58, s24, v237
	v_med3_f32 v59, v59, s24, v237
	v_med3_f32 v60, v60, s24, v237
	v_med3_f32 v61, v61, s24, v237
	v_med3_f32 v62, v62, s24, v237
	v_med3_f32 v63, v63, s24, v237
	v_cvt_pk_fp8_f32 v0, v0, v4
	v_cvt_pk_fp8_f32 v0, v8, v12 op_sel:[0,0,1]
	v_cvt_pk_fp8_f32 v4, v1, v5
	v_cvt_pk_fp8_f32 v4, v9, v13 op_sel:[0,0,1]
	v_cvt_pk_fp8_f32 v8, v2, v6
	v_cvt_pk_fp8_f32 v8, v10, v14 op_sel:[0,0,1]
	v_cvt_pk_fp8_f32 v12, v3, v7
	v_cvt_pk_fp8_f32 v12, v11, v15 op_sel:[0,0,1]
	v_cvt_pk_fp8_f32 v1, v16, v20
	v_cvt_pk_fp8_f32 v1, v24, v28 op_sel:[0,0,1]
	v_cvt_pk_fp8_f32 v5, v17, v21
	v_cvt_pk_fp8_f32 v5, v25, v29 op_sel:[0,0,1]
	v_cvt_pk_fp8_f32 v9, v18, v22
	v_cvt_pk_fp8_f32 v9, v26, v30 op_sel:[0,0,1]
	v_cvt_pk_fp8_f32 v13, v19, v23
	v_cvt_pk_fp8_f32 v13, v27, v31 op_sel:[0,0,1]
	v_cvt_pk_fp8_f32 v2, v32, v36
	v_cvt_pk_fp8_f32 v2, v40, v44 op_sel:[0,0,1]
	v_cvt_pk_fp8_f32 v6, v33, v37
	v_cvt_pk_fp8_f32 v6, v41, v45 op_sel:[0,0,1]
	v_cvt_pk_fp8_f32 v10, v34, v38
	v_cvt_pk_fp8_f32 v10, v42, v46 op_sel:[0,0,1]
	v_cvt_pk_fp8_f32 v14, v35, v39
	v_cvt_pk_fp8_f32 v14, v43, v47 op_sel:[0,0,1]
	v_cvt_pk_fp8_f32 v3, v48, v52
	v_cvt_pk_fp8_f32 v3, v56, v60 op_sel:[0,0,1]
	v_cvt_pk_fp8_f32 v7, v49, v53
	v_cvt_pk_fp8_f32 v7, v57, v61 op_sel:[0,0,1]
	v_cvt_pk_fp8_f32 v11, v50, v54
	v_cvt_pk_fp8_f32 v11, v58, v62 op_sel:[0,0,1]
	v_cvt_pk_fp8_f32 v15, v51, v55
	v_cvt_pk_fp8_f32 v15, v59, v63 op_sel:[0,0,1]
	global_store_dwordx4 v250, v[0:3], s[42:43] nt
	global_store_dwordx4 v250, v[4:7], s[42:43] offset:2048 nt
	global_store_dwordx4 v251, v[8:11], s[42:43] nt
	global_store_dwordx4 v251, v[12:15], s[42:43] offset:2048 nt
	s_add_u32 s42, s42, 0x800000
	s_addc_u32 s43, s43, 0
	global_load_dwordx4 v[0:3], v246, s[4:5] nt
	global_load_dwordx4 v[4:7], v247, s[4:5] nt
	global_load_dwordx4 v[8:11], v248, s[4:5] nt
	global_load_dwordx4 v[12:15], v249, s[4:5] nt
	global_load_dwordx4 v[16:19], v246, s[6:7] nt
	global_load_dwordx4 v[20:23], v247, s[6:7] nt
	global_load_dwordx4 v[24:27], v248, s[6:7] nt
	global_load_dwordx4 v[28:31], v249, s[6:7] nt
	global_load_dwordx4 v[32:35], v246, s[8:9] nt
	global_load_dwordx4 v[36:39], v247, s[8:9] nt
	global_load_dwordx4 v[40:43], v248, s[8:9] nt
	global_load_dwordx4 v[44:47], v249, s[8:9] nt
	global_load_dwordx4 v[48:51], v246, s[38:39] nt
	global_load_dwordx4 v[52:55], v247, s[38:39] nt
	global_load_dwordx4 v[56:59], v248, s[38:39] nt
	global_load_dwordx4 v[60:63], v249, s[38:39] nt
	s_add_u32 s4, s4, 0x2000000
	s_addc_u32 s5, s5, 0
	s_add_u32 s6, s6, 0x2000000
	s_addc_u32 s7, s7, 0
	s_add_u32 s8, s8, 0x2000000
	s_addc_u32 s9, s9, 0
	s_add_u32 s38, s38, 0x2000000
	s_addc_u32 s39, s39, 0
	s_waitcnt vmcnt(40)
; #define GAS __attribute__((address_space(1)))
; template <bool GAIN, bool NT = false> __device__ __forceinline__ void titem8_load(const TItem& d, int lane, f32x4 (&r)[16], f32x4 (&g)[4]) {
;     const int q = lane & 7, kg = lane >> 3; const unsigned lo = (unsigned)((16 * kg) * d.N + 4 * q) * 4u;
;     const GAS char* base = (const GAS char*)d.src;
; #pragma unroll
;     for (int j = 0; j < 16; ++j) { const GAS f32x4* p = (const GAS f32x4*)(base + (size_t)j * (size_t)d.N * 4 + lo); r[j] = NT ? __builtin_nontemporal_load(p) : *p; }
;     if constexpr (GAIN) { const GAS char* gb = (const GAS char*)d.gain; const unsigned go = (unsigned)(16 * kg) * 4u;
; #pragma unroll
;         for (int j4 = 0; j4 < 4; ++j4) g[j4] = *(const GAS f32x4*)(gb + 16 * j4 + go); }
;     asm volatile("" ::: "memory"); __builtin_amdgcn_sched_barrier(0);
; }
; template <bool GAIN, bool NT = false> __device__ __forceinline__ void titem8_store(const TItem& d, int lane, const f32x4 (&r)[16], const f32x4 (&g)[4]) {
;     const int q = lane & 7, kg = lane >> 3; const unsigned lo = (unsigned)((4 * q) * d.ldk + 16 * kg);
;     GAS char* base = (GAS char*)d.dst;
;     f32x4 s[16];
; #pragma unroll
;     for (int j = 0; j < 16; ++j) s[j] = r[j] * ((GAIN ? g[j >> 2][j & 3] : 1.0f) * W8_SCALE);
; #pragma unroll
;     for (int i = 0; i < 4; ++i) { v4u w;
;         w.x = pk4_fp8w(s[0][i], s[1][i], s[2][i], s[3][i]); w.y = pk4_fp8w(s[4][i], s[5][i], s[6][i], s[7][i]);
;         w.z = pk4_fp8w(s[8][i], s[9][i], s[10][i], s[11][i]); w.w = pk4_fp8w(s[12][i], s[13][i], s[14][i], s[15][i]);
;         GAS v4u* p = (GAS v4u*)(base + (size_t)i * (size_t)d.ldk + lo);
;         if (NT) __builtin_nontemporal_store(w, p); else *p = w; }
; }
	v_pk_mul_f32 v[66:67], v[66:67], s[30:31] op_sel_hi:[1,0]
	v_pk_mul_f32 v[68:69], v[68:69], s[30:31] op_sel_hi:[1,0]
	v_pk_mul_f32 v[70:71], v[70:71], s[30:31] op_sel_hi:[1,0]
	v_pk_mul_f32 v[72:73], v[72:73], s[30:31] op_sel_hi:[1,0]
	v_pk_mul_f32 v[74:75], v[74:75], s[30:31] op_sel_hi:[1,0]
	v_pk_mul_f32 v[76:77], v[76:77], s[30:31] op_sel_hi:[1,0]
	v_pk_mul_f32 v[78:79], v[78:79], s[30:31] op_sel_hi:[1,0]
	v_pk_mul_f32 v[80:81], v[80:81], s[30:31] op_sel_hi:[1,0]
	v_pk_mul_f32 v[82:83], v[82:83], s[30:31] op_sel_hi:[1,0]
	v_pk_mul_f32 v[84:85], v[84:85], s[30:31] op_sel_hi:[1,0]
	v_pk_mul_f32 v[86:87], v[86:87], s[30:31] op_sel_hi:[1,0]
	v_pk_mul_f32 v[88:89], v[88:89], s[30:31] op_sel_hi:[1,0]
	v_pk_mul_f32 v[90:91], v[90:91], s[30:31] op_sel_hi:[1,0]
	v_pk_mul_f32 v[92:93], v[92:93], s[30:31] op_sel_hi:[1,0]
	v_pk_mul_f32 v[94:95], v[94:95], s[30:31] op_sel_hi:[1,0]
	v_pk_mul_f32 v[96:97], v[96:97], s[30:31] op_sel_hi:[1,0]
	v_pk_mul_f32 v[98:99], v[98:99], s[30:31] op_sel_hi:[1,0]
	v_pk_mul_f32 v[100:101], v[100:101], s[30:31] op_sel_hi:[1,0]
	v_pk_mul_f32 v[102:103], v[102:103], s[30:31] op_sel_hi:[1,0]
	v_pk_mul_f32 v[104:105], v[104:105], s[30:31] op_sel_hi:[1,0]
	v_pk_mul_f32 v[106:107], v[106:107], s[30:31] op_sel_hi:[1,0]
	v_pk_mul_f32 v[108:109], v[108:109], s[30:31] op_sel_hi:[1,0]
	v_pk_mul_f32 v[110:111], v[110:111], s[30:31] op_sel_hi:[1,0]
	v_pk_mul_f32 v[112:113], v[112:113], s[30:31] op_sel_hi:[1,0]
	v_pk_mul_f32 v[114:115], v[114:115], s[30:31] op_sel_hi:[1,0]
	v_pk_mul_f32 v[116:117], v[116:117], s[30:31] op_sel_hi:[1,0]
	v_pk_mul_f32 v[118:119], v[118:119], s[30:31] op_sel_hi:[1,0]
	v_pk_mul_f32 v[120:121], v[120:121], s[30:31] op_sel_hi:[1,0]
	v_pk_mul_f32 v[122:123], v[122:123], s[30:31] op_sel_hi:[1,0]
	v_pk_mul_f32 v[124:125], v[124:125], s[30:31] op_sel_hi:[1,0]
	v_pk_mul_f32 v[126:127], v[126:127], s[30:31] op_sel_hi:[1,0]
	v_pk_mul_f32 v[128:129], v[128:129], s[30:31] op_sel_hi:[1,0]
	v_med3_f32 v66, v66, s24, v237
	v_med3_f32 v67, v67, s24, v237
	v_med3_f32 v68, v68, s24, v237
	v_med3_f32 v69, v69, s24, v237
	v_med3_f32 v70, v70, s24, v237
	v_med3_f32 v71, v71, s24, v237
	v_med3_f32 v72, v72, s24, v237
	v_med3_f32 v73, v73, s24, v237
	v_med3_f32 v74, v74, s24, v237
	v_med3_f32 v75, v75, s24, v237
	v_med3_f32 v76, v76, s24, v237
	v_med3_f32 v77, v77, s24, v237
	v_med3_f32 v78, v78, s24, v237
	v_med3_f32 v79, v79, s24, v237
	v_med3_f32 v80, v80, s24, v237
	v_med3_f32 v81, v81, s24, v237
	v_med3_f32 v82, v82, s24, v237
	v_med3_f32 v83, v83, s24, v237
	v_med3_f32 v84, v84, s24, v237
	v_med3_f32 v85, v85, s24, v237
	v_med3_f32 v86, v86, s24, v237
	v_med3_f32 v87, v87, s24, v237
	v_med3_f32 v88, v88, s24, v237
	v_med3_f32 v89, v89, s24, v237
	v_med3_f32 v90, v90, s24, v237
	v_med3_f32 v91, v91, s24, v237
	v_med3_f32 v92, v92, s24, v237
	v_med3_f32 v93, v93, s24, v237
	v_med3_f32 v94, v94, s24, v237
	v_med3_f32 v95, v95, s24, v237
	v_med3_f32 v96, v96, s24, v237
	v_med3_f32 v97, v97, s24, v237
	v_med3_f32 v98, v98, s24, v237
	v_med3_f32 v99, v99, s24, v237
	v_med3_f32 v100, v100, s24, v237
	v_med3_f32 v101, v101, s24, v237
	v_med3_f32 v102, v102, s24, v237
	v_med3_f32 v103, v103, s24, v237
	v_med3_f32 v104, v104, s24, v237
	v_med3_f32 v105, v105, s24, v237
	v_med3_f32 v106, v106, s24, v237
	v_med3_f32 v107, v107, s24, v237
	v_med3_f32 v108, v108, s24, v237
	v_med3_f32 v109, v109, s24, v237
	v_med3_f32 v110, v110, s24, v237
	v_med3_f32 v111, v111, s24, v237
	v_med3_f32 v112, v112, s24, v237
	v_med3_f32 v113, v113, s24, v237
	v_med3_f32 v114, v114, s24, v237
	v_med3_f32 v115, v115, s24, v237
	v_med3_f32 v116, v116, s24, v237
	v_med3_f32 v117, v117, s24, v237
	v_med3_f32 v118, v118, s24, v237
	v_med3_f32 v119, v119, s24, v237
	v_med3_f32 v120, v120, s24, v237
	v_med3_f32 v121, v121, s24, v237
	v_med3_f32 v122, v122, s24, v237
	v_med3_f32 v123, v123, s24, v237
	v_med3_f32 v124, v124, s24, v237
	v_med3_f32 v125, v125, s24, v237
	v_med3_f32 v126, v126, s24, v237
	v_med3_f32 v127, v127, s24, v237
	v_med3_f32 v128, v128, s24, v237
	v_med3_f32 v129, v129, s24, v237
	v_cvt_pk_fp8_f32 v66, v66, v70
	v_cvt_pk_fp8_f32 v66, v74, v78 op_sel:[0,0,1]
	v_cvt_pk_fp8_f32 v70, v67, v71
	v_cvt_pk_fp8_f32 v70, v75, v79 op_sel:[0,0,1]
	v_cvt_pk_fp8_f32 v74, v68, v72
	v_cvt_pk_fp8_f32 v74, v76, v80 op_sel:[0,0,1]
	v_cvt_pk_fp8_f32 v78, v69, v73
	v_cvt_pk_fp8_f32 v78, v77, v81 op_sel:[0,0,1]
	v_cvt_pk_fp8_f32 v67, v82, v86
	v_cvt_pk_fp8_f32 v67, v90, v94 op_sel:[0,0,1]
	v_cvt_pk_fp8_f32 v71, v83, v87
	v_cvt_pk_fp8_f32 v71, v91, v95 op_sel:[0,0,1]
	v_cvt_pk_fp8_f32 v75, v84, v88
	v_cvt_pk_fp8_f32 v75, v92, v96 op_sel:[0,0,1]
	v_cvt_pk_fp8_f32 v79, v85, v89
	v_cvt_pk_fp8_f32 v79, v93, v97 op_sel:[0,0,1]
	v_cvt_pk_fp8_f32 v68, v98, v102
	v_cvt_pk_fp8_f32 v68, v106, v110 op_sel:[0,0,1]
	v_cvt_pk_fp8_f32 v72, v99, v103
	v_cvt_pk_fp8_f32 v72, v107, v111 op_sel:[0,0,1]
	v_cvt_pk_fp8_f32 v76, v100, v104
	v_cvt_pk_fp8_f32 v76, v108, v112 op_sel:[0,0,1]
	v_cvt_pk_fp8_f32 v80, v101, v105
	v_cvt_pk_fp8_f32 v80, v109, v113 op_sel:[0,0,1]
	v_cvt_pk_fp8_f32 v69, v114, v118
	v_cvt_pk_fp8_f32 v69, v122, v126 op_sel:[0,0,1]
	v_cvt_pk_fp8_f32 v73, v115, v119
	v_cvt_pk_fp8_f32 v73, v123, v127 op_sel:[0,0,1]
	v_cvt_pk_fp8_f32 v77, v116, v120
	v_cvt_pk_fp8_f32 v77, v124, v128 op_sel:[0,0,1]
	v_cvt_pk_fp8_f32 v81, v117, v121
	v_cvt_pk_fp8_f32 v81, v125, v129 op_sel:[0,0,1]
	global_store_dwordx4 v250, v[66:69], s[42:43] nt
	global_store_dwordx4 v250, v[70:73], s[42:43] offset:2048 nt
	global_store_dwordx4 v251, v[74:77], s[42:43] nt
	global_store_dwordx4 v251, v[78:81], s[42:43] offset:2048 nt
	s_add_u32 s42, s42, 0x800000
	s_addc_u32 s43, s43, 0
	global_load_dwordx4 v[66:69], v246, s[4:5] nt
	global_load_dwordx4 v[70:73], v247, s[4:5] nt
	global_load_dwordx4 v[74:77], v248, s[4:5] nt
	global_load_dwordx4 v[78:81], v249, s[4:5] nt
	global_load_dwordx4 v[82:85], v246, s[6:7] nt
	global_load_dwordx4 v[86:89], v247, s[6:7] nt
	global_load_dwordx4 v[90:93], v248, s[6:7] nt
	global_load_dwordx4 v[94:97], v249, s[6:7] nt
	global_load_dwordx4 v[98:101], v246, s[8:9] nt
	global_load_dwordx4 v[102:105], v247, s[8:9] nt
	global_load_dwordx4 v[106:109], v248, s[8:9] nt
	global_load_dwordx4 v[110:113], v249, s[8:9] nt
	global_load_dwordx4 v[114:117], v246, s[38:39] nt
	global_load_dwordx4 v[118:121], v247, s[38:39] nt
	global_load_dwordx4 v[122:125], v248, s[38:39] nt
	global_load_dwordx4 v[126:129], v249, s[38:39] nt
	s_add_u32 s4, s4, 0x2000000
	s_addc_u32 s5, s5, 0
	s_add_u32 s6, s6, 0x2000000
	s_addc_u32 s7, s7, 0
	s_add_u32 s8, s8, 0x2000000
	s_addc_u32 s9, s9, 0
	s_add_u32 s38, s38, 0x2000000
	s_addc_u32 s39, s39, 0
	s_waitcnt vmcnt(40)
; #define GAS __attribute__((address_space(1)))
; template <bool GAIN, bool NT = false> __device__ __forceinline__ void titem8_load(const TItem& d, int lane, f32x4 (&r)[16], f32x4 (&g)[4]) {
;     const int q = lane & 7, kg = lane >> 3; const unsigned lo = (unsigned)((16 * kg) * d.N + 4 * q) * 4u;
;     const GAS char* base = (const GAS char*)d.src;
; #pragma unroll
;     for (int j = 0; j < 16; ++j) { const GAS f32x4* p = (const GAS f32x4*)(base + (size_t)j * (size_t)d.N * 4 + lo); r[j] = NT ? __builtin_nontemporal_load(p) : *p; }
; template <bool GAIN, bool NT = false> __device__ __forceinline__ void titem8_store(const TItem& d, int lane, const f32x4 (&r)[16], const f32x4 (&g)[4]) {
;     const int q = lane & 7, kg = lane >> 3; const unsigned lo = (unsigned)((4 * q) * d.ldk + 16 * kg);
;     GAS char* base = (GAS char*)d.dst;
;     f32x4 s[16];
; #pragma unroll
;     for (int j = 0; j < 16; ++j) s[j] = r[j] * ((GAIN ? g[j >> 2][j & 3] : 1.0f) * W8_SCALE);
; #pragma unroll
;     for (int i = 0; i < 4; ++i) { v4u w;
;         w.x = pk4_fp8w(s[0][i], s[1][i], s[2][i], s[3][i]); w.y = pk4_fp8w(s[4][i], s[5][i], s[6][i], s[7][i]);
;         w.z = pk4_fp8w(s[8][i], s[9][i], s[10][i], s[11][i]); w.w = pk4_fp8w(s[12][i], s[13][i], s[14][i], s[15][i]);
;         GAS v4u* p = (GAS v4u*)(base + (size_t)i * (size_t)d.ldk + lo);
;         if (NT) __builtin_nontemporal_store(w, p); else *p = w; }
; }
	v_pk_mul_f32 v[130:131], v[130:131], s[30:31] op_sel_hi:[1,0]
	v_pk_mul_f32 v[132:133], v[132:133], s[30:31] op_sel_hi:[1,0]
	v_pk_mul_f32 v[134:135], v[134:135], s[30:31] op_sel_hi:[1,0]
	v_pk_mul_f32 v[136:137], v[136:137], s[30:31] op_sel_hi:[1,0]
	v_pk_mul_f32 v[138:139], v[138:139], s[30:31] op_sel_hi:[1,0]
	v_pk_mul_f32 v[140:141], v[140:141], s[30:31] op_sel_hi:[1,0]
	v_pk_mul_f32 v[142:143], v[142:143], s[30:31] op_sel_hi:[1,0]
	v_pk_mul_f32 v[144:145], v[144:145], s[30:31] op_sel_hi:[1,0]
	v_pk_mul_f32 v[146:147], v[146:147], s[30:31] op_sel_hi:[1,0]
	v_pk_mul_f32 v[148:149], v[148:149], s[30:31] op_sel_hi:[1,0]
	v_pk_mul_f32 v[150:151], v[150:151], s[30:31] op_sel_hi:[1,0]
	v_pk_mul_f32 v[152:153], v[152:153], s[30:31] op_sel_hi:[1,0]
	v_pk_mul_f32 v[154:155], v[154:155], s[30:31] op_sel_hi:[1,0]
	v_pk_mul_f32 v[156:157], v[156:157], s[30:31] op_sel_hi:[1,0]
	v_pk_mul_f32 v[158:159], v[158:159], s[30:31] op_sel_hi:[1,0]
	v_pk_mul_f32 v[160:161], v[160:161], s[30:31] op_sel_hi:[1,0]
	v_pk_mul_f32 v[162:163], v[162:163], s[30:31] op_sel_hi:[1,0]
	v_pk_mul_f32 v[164:165], v[164:165], s[30:31] op_sel_hi:[1,0]
	v_pk_mul_f32 v[166:167], v[166:167], s[30:31] op_sel_hi:[1,0]
	v_pk_mul_f32 v[168:169], v[168:169], s[30:31] op_sel_hi:[1,0]
	v_pk_mul_f32 v[170:171], v[170:171], s[30:31] op_sel_hi:[1,0]
	v_pk_mul_f32 v[172:173], v[172:173], s[30:31] op_sel_hi:[1,0]
	v_pk_mul_f32 v[174:175], v[174:175], s[30:31] op_sel_hi:[1,0]
	v_pk_mul_f32 v[176:177], v[176:177], s[30:31] op_sel_hi:[1,0]
	v_pk_mul_f32 v[178:179], v[178:179], s[30:31] op_sel_hi:[1,0]
	v_pk_mul_f32 v[180:181], v[180:181], s[30:31] op_sel_hi:[1,0]
	v_pk_mul_f32 v[182:183], v[182:183], s[30:31] op_sel_hi:[1,0]
	v_pk_mul_f32 v[184:185], v[184:185], s[30:31] op_sel_hi:[1,0]
	v_pk_mul_f32 v[186:187], v[186:187], s[30:31] op_sel_hi:[1,0]
	v_pk_mul_f32 v[188:189], v[188:189], s[30:31] op_sel_hi:[1,0]
	v_pk_mul_f32 v[190:191], v[190:191], s[30:31] op_sel_hi:[1,0]
	v_pk_mul_f32 v[192:193], v[192:193], s[30:31] op_sel_hi:[1,0]
	v_med3_f32 v130, v130, s24, v237
	v_med3_f32 v131, v131, s24, v237
	v_med3_f32 v132, v132, s24, v237
	v_med3_f32 v133, v133, s24, v237
	v_med3_f32 v134, v134, s24, v237
	v_med3_f32 v135, v135, s24, v237
	v_med3_f32 v136, v136, s24, v237
	v_med3_f32 v137, v137, s24, v237
	v_med3_f32 v138, v138, s24, v237
	v_med3_f32 v139, v139, s24, v237
	v_med3_f32 v140, v140, s24, v237
	v_med3_f32 v141, v141, s24, v237
	v_med3_f32 v142, v142, s24, v237
	v_med3_f32 v143, v143, s24, v237
	v_med3_f32 v144, v144, s24, v237
	v_med3_f32 v145, v145, s24, v237
	v_med3_f32 v146, v146, s24, v237
	v_med3_f32 v147, v147, s24, v237
	v_med3_f32 v148, v148, s24, v237
	v_med3_f32 v149, v149, s24, v237
	v_med3_f32 v150, v150, s24, v237
	v_med3_f32 v151, v151, s24, v237
	v_med3_f32 v152, v152, s24, v237
	v_med3_f32 v153, v153, s24, v237
	v_med3_f32 v154, v154, s24, v237
	v_med3_f32 v155, v155, s24, v237
	v_med3_f32 v156, v156, s24, v237
	v_med3_f32 v157, v157, s24, v237
	v_med3_f32 v158, v158, s24, v237
	v_med3_f32 v159, v159, s24, v237
	v_med3_f32 v160, v160, s24, v237
	v_med3_f32 v161, v161, s24, v237
	v_med3_f32 v162, v162, s24, v237
	v_med3_f32 v163, v163, s24, v237
	v_med3_f32 v164, v164, s24, v237
	v_med3_f32 v165, v165, s24, v237
	v_med3_f32 v166, v166, s24, v237
	v_med3_f32 v167, v167, s24, v237
	v_med3_f32 v168, v168, s24, v237
	v_med3_f32 v169, v169, s24, v237
	v_med3_f32 v170, v170, s24, v237
	v_med3_f32 v171, v171, s24, v237
	v_med3_f32 v172, v172, s24, v237
	v_med3_f32 v173, v173, s24, v237
	v_med3_f32 v174, v174, s24, v237
	v_med3_f32 v175, v175, s24, v237
	v_med3_f32 v176, v176, s24, v237
	v_med3_f32 v177, v177, s24, v237
	v_med3_f32 v178, v178, s24, v237
	v_med3_f32 v179, v179, s24, v237
	v_med3_f32 v180, v180, s24, v237
	v_med3_f32 v181, v181, s24, v237
	v_med3_f32 v182, v182, s24, v237
	v_med3_f32 v183, v183, s24, v237
	v_med3_f32 v184, v184, s24, v237
	v_med3_f32 v185, v185, s24, v237
	v_med3_f32 v186, v186, s24, v237
	v_med3_f32 v187, v187, s24, v237
	v_med3_f32 v188, v188, s24, v237
	v_med3_f32 v189, v189, s24, v237
	v_med3_f32 v190, v190, s24, v237
	v_med3_f32 v191, v191, s24, v237
	v_med3_f32 v192, v192, s24, v237
	v_med3_f32 v193, v193, s24, v237
	v_cvt_pk_fp8_f32 v130, v130, v134
	v_cvt_pk_fp8_f32 v130, v138, v142 op_sel:[0,0,1]
	v_cvt_pk_fp8_f32 v134, v131, v135
	v_cvt_pk_fp8_f32 v134, v139, v143 op_sel:[0,0,1]
	v_cvt_pk_fp8_f32 v138, v132, v136
	v_cvt_pk_fp8_f32 v138, v140, v144 op_sel:[0,0,1]
	v_cvt_pk_fp8_f32 v142, v133, v137
	v_cvt_pk_fp8_f32 v142, v141, v145 op_sel:[0,0,1]
	v_cvt_pk_fp8_f32 v131, v146, v150
	v_cvt_pk_fp8_f32 v131, v154, v158 op_sel:[0,0,1]
	v_cvt_pk_fp8_f32 v135, v147, v151
	v_cvt_pk_fp8_f32 v135, v155, v159 op_sel:[0,0,1]
	v_cvt_pk_fp8_f32 v139, v148, v152
	v_cvt_pk_fp8_f32 v139, v156, v160 op_sel:[0,0,1]
	v_cvt_pk_fp8_f32 v143, v149, v153
	v_cvt_pk_fp8_f32 v143, v157, v161 op_sel:[0,0,1]
	v_cvt_pk_fp8_f32 v132, v162, v166
	v_cvt_pk_fp8_f32 v132, v170, v174 op_sel:[0,0,1]
	v_cvt_pk_fp8_f32 v136, v163, v167
	v_cvt_pk_fp8_f32 v136, v171, v175 op_sel:[0,0,1]
	v_cvt_pk_fp8_f32 v140, v164, v168
	v_cvt_pk_fp8_f32 v140, v172, v176 op_sel:[0,0,1]
	v_cvt_pk_fp8_f32 v144, v165, v169
	v_cvt_pk_fp8_f32 v144, v173, v177 op_sel:[0,0,1]
	v_cvt_pk_fp8_f32 v133, v178, v182
	v_cvt_pk_fp8_f32 v133, v186, v190 op_sel:[0,0,1]
	v_cvt_pk_fp8_f32 v137, v179, v183
	v_cvt_pk_fp8_f32 v137, v187, v191 op_sel:[0,0,1]
	v_cvt_pk_fp8_f32 v141, v180, v184
	v_cvt_pk_fp8_f32 v141, v188, v192 op_sel:[0,0,1]
	v_cvt_pk_fp8_f32 v145, v181, v185
	v_cvt_pk_fp8_f32 v145, v189, v193 op_sel:[0,0,1]
	global_store_dwordx4 v250, v[130:133], s[42:43] nt
	global_store_dwordx4 v250, v[134:137], s[42:43] offset:2048 nt
	global_store_dwordx4 v251, v[138:141], s[42:43] nt
	global_store_dwordx4 v251, v[142:145], s[42:43] offset:2048 nt
	s_add_u32 s42, s42, 0x800000
	s_addc_u32 s43, s43, 0
	global_load_dwordx4 v[130:133], v246, s[4:5] nt
	global_load_dwordx4 v[134:137], v247, s[4:5] nt
	global_load_dwordx4 v[138:141], v248, s[4:5] nt
	global_load_dwordx4 v[142:145], v249, s[4:5] nt
	global_load_dwordx4 v[146:149], v246, s[6:7] nt
	global_load_dwordx4 v[150:153], v247, s[6:7] nt
	global_load_dwordx4 v[154:157], v248, s[6:7] nt
	global_load_dwordx4 v[158:161], v249, s[6:7] nt
	global_load_dwordx4 v[162:165], v246, s[8:9] nt
	global_load_dwordx4 v[166:169], v247, s[8:9] nt
	global_load_dwordx4 v[170:173], v248, s[8:9] nt
	global_load_dwordx4 v[174:177], v249, s[8:9] nt
	global_load_dwordx4 v[178:181], v246, s[38:39] nt
	global_load_dwordx4 v[182:185], v247, s[38:39] nt
	global_load_dwordx4 v[186:189], v248, s[38:39] nt
	global_load_dwordx4 v[190:193], v249, s[38:39] nt
	s_add_u32 s4, s4, 0x2000000
	s_addc_u32 s5, s5, 0
	s_add_u32 s6, s6, 0x2000000
	s_addc_u32 s7, s7, 0
	s_add_u32 s8, s8, 0x2000000
	s_addc_u32 s9, s9, 0
	s_add_u32 s38, s38, 0x2000000
	s_addc_u32 s39, s39, 0
	s_waitcnt vmcnt(40)
; #define GAS __attribute__((address_space(1)))
; template <bool GAIN, bool NT = false> __device__ __forceinline__ void titem8_load(const TItem& d, int lane, f32x4 (&r)[16], f32x4 (&g)[4]) {
;     const int q = lane & 7, kg = lane >> 3; const unsigned lo = (unsigned)((16 * kg) * d.N + 4 * q) * 4u;
;     const GAS char* base = (const GAS char*)d.src;
; #pragma unroll
;     for (int j = 0; j < 16; ++j) { const GAS f32x4* p = (const GAS f32x4*)(base + (size_t)j * (size_t)d.N * 4 + lo); r[j] = NT ? __builtin_nontemporal_load(p) : *p; }
; template <bool GAIN, bool NT = false> __device__ __forceinline__ void titem8_store(const TItem& d, int lane, const f32x4 (&r)[16], const f32x4 (&g)[4]) {
;     const int q = lane & 7, kg = lane >> 3; const unsigned lo = (unsigned)((4 * q) * d.ldk + 16 * kg);
;     GAS char* base = (GAS char*)d.dst;
;     f32x4 s[16];
; #pragma unroll
;     for (int j = 0; j < 16; ++j) s[j] = r[j] * ((GAIN ? g[j >> 2][j & 3] : 1.0f) * W8_SCALE);
; #pragma unroll
;     for (int i = 0; i < 4; ++i) { v4u w;
;         w.x = pk4_fp8w(s[0][i], s[1][i], s[2][i], s[3][i]); w.y = pk4_fp8w(s[4][i], s[5][i], s[6][i], s[7][i]);
;         w.z = pk4_fp8w(s[8][i], s[9][i], s[10][i], s[11][i]); w.w = pk4_fp8w(s[12][i], s[13][i], s[14][i], s[15][i]);
;         GAS v4u* p = (GAS v4u*)(base + (size_t)i * (size_t)d.ldk + lo);
;         if (NT) __builtin_nontemporal_store(w, p); else *p = w; }
; }
	v_pk_mul_f32 v[0:1], v[0:1], s[30:31] op_sel_hi:[1,0]
	v_pk_mul_f32 v[2:3], v[2:3], s[30:31] op_sel_hi:[1,0]
	v_pk_mul_f32 v[4:5], v[4:5], s[30:31] op_sel_hi:[1,0]
	v_pk_mul_f32 v[6:7], v[6:7], s[30:31] op_sel_hi:[1,0]
	v_pk_mul_f32 v[8:9], v[8:9], s[30:31] op_sel_hi:[1,0]
	v_pk_mul_f32 v[10:11], v[10:11], s[30:31] op_sel_hi:[1,0]
	v_pk_mul_f32 v[12:13], v[12:13], s[30:31] op_sel_hi:[1,0]
	v_pk_mul_f32 v[14:15], v[14:15], s[30:31] op_sel_hi:[1,0]
	v_pk_mul_f32 v[16:17], v[16:17], s[30:31] op_sel_hi:[1,0]
	v_pk_mul_f32 v[18:19], v[18:19], s[30:31] op_sel_hi:[1,0]
	v_pk_mul_f32 v[20:21], v[20:21], s[30:31] op_sel_hi:[1,0]
	v_pk_mul_f32 v[22:23], v[22:23], s[30:31] op_sel_hi:[1,0]
	v_pk_mul_f32 v[24:25], v[24:25], s[30:31] op_sel_hi:[1,0]
	v_pk_mul_f32 v[26:27], v[26:27], s[30:31] op_sel_hi:[1,0]
	v_pk_mul_f32 v[28:29], v[28:29], s[30:31] op_sel_hi:[1,0]
	v_pk_mul_f32 v[30:31], v[30:31], s[30:31] op_sel_hi:[1,0]
	v_pk_mul_f32 v[32:33], v[32:33], s[30:31] op_sel_hi:[1,0]
	v_pk_mul_f32 v[34:35], v[34:35], s[30:31] op_sel_hi:[1,0]
	v_pk_mul_f32 v[36:37], v[36:37], s[30:31] op_sel_hi:[1,0]
	v_pk_mul_f32 v[38:39], v[38:39], s[30:31] op_sel_hi:[1,0]
	v_pk_mul_f32 v[40:41], v[40:41], s[30:31] op_sel_hi:[1,0]
	v_pk_mul_f32 v[42:43], v[42:43], s[30:31] op_sel_hi:[1,0]
	v_pk_mul_f32 v[44:45], v[44:45], s[30:31] op_sel_hi:[1,0]
	v_pk_mul_f32 v[46:47], v[46:47], s[30:31] op_sel_hi:[1,0]
	v_pk_mul_f32 v[48:49], v[48:49], s[30:31] op_sel_hi:[1,0]
	v_pk_mul_f32 v[50:51], v[50:51], s[30:31] op_sel_hi:[1,0]
	v_pk_mul_f32 v[52:53], v[52:53], s[30:31] op_sel_hi:[1,0]
	v_pk_mul_f32 v[54:55], v[54:55], s[30:31] op_sel_hi:[1,0]
	v_pk_mul_f32 v[56:57], v[56:57], s[30:31] op_sel_hi:[1,0]
	v_pk_mul_f32 v[58:59], v[58:59], s[30:31] op_sel_hi:[1,0]
	v_pk_mul_f32 v[60:61], v[60:61], s[30:31] op_sel_hi:[1,0]
	v_pk_mul_f32 v[62:63], v[62:63], s[30:31] op_sel_hi:[1,0]
	v_med3_f32 v0, v0, s24, v237
	v_med3_f32 v1, v1, s24, v237
	v_med3_f32 v2, v2, s24, v237
	v_med3_f32 v3, v3, s24, v237
	v_med3_f32 v4, v4, s24, v237
	v_med3_f32 v5, v5, s24, v237
	v_med3_f32 v6, v6, s24, v237
	v_med3_f32 v7, v7, s24, v237
	v_med3_f32 v8, v8, s24, v237
	v_med3_f32 v9, v9, s24, v237
	v_med3_f32 v10, v10, s24, v237
	v_med3_f32 v11, v11, s24, v237
	v_med3_f32 v12, v12, s24, v237
	v_med3_f32 v13, v13, s24, v237
	v_med3_f32 v14, v14, s24, v237
	v_med3_f32 v15, v15, s24, v237
	v_med3_f32 v16, v16, s24, v237
	v_med3_f32 v17, v17, s24, v237
	v_med3_f32 v18, v18, s24, v237
	v_med3_f32 v19, v19, s24, v237
	v_med3_f32 v20, v20, s24, v237
	v_med3_f32 v21, v21, s24, v237
	v_med3_f32 v22, v22, s24, v237
	v_med3_f32 v23, v23, s24, v237
	v_med3_f32 v24, v24, s24, v237
	v_med3_f32 v25, v25, s24, v237
	v_med3_f32 v26, v26, s24, v237
	v_med3_f32 v27, v27, s24, v237
	v_med3_f32 v28, v28, s24, v237
	v_med3_f32 v29, v29, s24, v237
	v_med3_f32 v30, v30, s24, v237
	v_med3_f32 v31, v31, s24, v237
	v_med3_f32 v32, v32, s24, v237
	v_med3_f32 v33, v33, s24, v237
	v_med3_f32 v34, v34, s24, v237
	v_med3_f32 v35, v35, s24, v237
	v_med3_f32 v36, v36, s24, v237
	v_med3_f32 v37, v37, s24, v237
	v_med3_f32 v38, v38, s24, v237
	v_med3_f32 v39, v39, s24, v237
	v_med3_f32 v40, v40, s24, v237
	v_med3_f32 v41, v41, s24, v237
	v_med3_f32 v42, v42, s24, v237
	v_med3_f32 v43, v43, s24, v237
	v_med3_f32 v44, v44, s24, v237
	v_med3_f32 v45, v45, s24, v237
	v_med3_f32 v46, v46, s24, v237
	v_med3_f32 v47, v47, s24, v237
	v_med3_f32 v48, v48, s24, v237
	v_med3_f32 v49, v49, s24, v237
	v_med3_f32 v50, v50, s24, v237
	v_med3_f32 v51, v51, s24, v237
	v_med3_f32 v52, v52, s24, v237
	v_med3_f32 v53, v53, s24, v237
	v_med3_f32 v54, v54, s24, v237
	v_med3_f32 v55, v55, s24, v237
	v_med3_f32 v56, v56, s24, v237
	v_med3_f32 v57, v57, s24, v237
	v_med3_f32 v58, v58, s24, v237
	v_med3_f32 v59, v59, s24, v237
	v_med3_f32 v60, v60, s24, v237
	v_med3_f32 v61, v61, s24, v237
	v_med3_f32 v62, v62, s24, v237
	v_med3_f32 v63, v63, s24, v237
	v_cvt_pk_fp8_f32 v0, v0, v4
	v_cvt_pk_fp8_f32 v0, v8, v12 op_sel:[0,0,1]
	v_cvt_pk_fp8_f32 v4, v1, v5
	v_cvt_pk_fp8_f32 v4, v9, v13 op_sel:[0,0,1]
	v_cvt_pk_fp8_f32 v8, v2, v6
	v_cvt_pk_fp8_f32 v8, v10, v14 op_sel:[0,0,1]
	v_cvt_pk_fp8_f32 v12, v3, v7
	v_cvt_pk_fp8_f32 v12, v11, v15 op_sel:[0,0,1]
	v_cvt_pk_fp8_f32 v1, v16, v20
	v_cvt_pk_fp8_f32 v1, v24, v28 op_sel:[0,0,1]
	v_cvt_pk_fp8_f32 v5, v17, v21
	v_cvt_pk_fp8_f32 v5, v25, v29 op_sel:[0,0,1]
	v_cvt_pk_fp8_f32 v9, v18, v22
	v_cvt_pk_fp8_f32 v9, v26, v30 op_sel:[0,0,1]
	v_cvt_pk_fp8_f32 v13, v19, v23
	v_cvt_pk_fp8_f32 v13, v27, v31 op_sel:[0,0,1]
	v_cvt_pk_fp8_f32 v2, v32, v36
	v_cvt_pk_fp8_f32 v2, v40, v44 op_sel:[0,0,1]
	v_cvt_pk_fp8_f32 v6, v33, v37
	v_cvt_pk_fp8_f32 v6, v41, v45 op_sel:[0,0,1]
	v_cvt_pk_fp8_f32 v10, v34, v38
	v_cvt_pk_fp8_f32 v10, v42, v46 op_sel:[0,0,1]
	v_cvt_pk_fp8_f32 v14, v35, v39
	v_cvt_pk_fp8_f32 v14, v43, v47 op_sel:[0,0,1]
	v_cvt_pk_fp8_f32 v3, v48, v52
	v_cvt_pk_fp8_f32 v3, v56, v60 op_sel:[0,0,1]
	v_cvt_pk_fp8_f32 v7, v49, v53
	v_cvt_pk_fp8_f32 v7, v57, v61 op_sel:[0,0,1]
	v_cvt_pk_fp8_f32 v11, v50, v54
	v_cvt_pk_fp8_f32 v11, v58, v62 op_sel:[0,0,1]
	v_cvt_pk_fp8_f32 v15, v51, v55
	v_cvt_pk_fp8_f32 v15, v59, v63 op_sel:[0,0,1]
	global_store_dwordx4 v250, v[0:3], s[42:43] nt
	global_store_dwordx4 v250, v[4:7], s[42:43] offset:2048 nt
	global_store_dwordx4 v251, v[8:11], s[42:43] nt
	global_store_dwordx4 v251, v[12:15], s[42:43] offset:2048 nt
	s_add_u32 s42, s42, 0x800000
	s_addc_u32 s43, s43, 0
	global_load_dwordx4 v[0:3], v246, s[4:5] nt
	global_load_dwordx4 v[4:7], v247, s[4:5] nt
	global_load_dwordx4 v[8:11], v248, s[4:5] nt
	global_load_dwordx4 v[12:15], v249, s[4:5] nt
	global_load_dwordx4 v[16:19], v246, s[6:7] nt
	global_load_dwordx4 v[20:23], v247, s[6:7] nt
	global_load_dwordx4 v[24:27], v248, s[6:7] nt
	global_load_dwordx4 v[28:31], v249, s[6:7] nt
	global_load_dwordx4 v[32:35], v246, s[8:9] nt
	global_load_dwordx4 v[36:39], v247, s[8:9] nt
	global_load_dwordx4 v[40:43], v248, s[8:9] nt
	global_load_dwordx4 v[44:47], v249, s[8:9] nt
	global_load_dwordx4 v[48:51], v246, s[38:39] nt
	global_load_dwordx4 v[52:55], v247, s[38:39] nt
	global_load_dwordx4 v[56:59], v248, s[38:39] nt
	global_load_dwordx4 v[60:63], v249, s[38:39] nt
	s_add_u32 s4, s4, 0x2000000
	s_addc_u32 s5, s5, 0
	s_add_u32 s6, s6, 0x2000000
	s_addc_u32 s7, s7, 0
	s_add_u32 s8, s8, 0x2000000
	s_addc_u32 s9, s9, 0
	s_add_u32 s38, s38, 0x2000000
	s_addc_u32 s39, s39, 0
	s_waitcnt vmcnt(40)
; #define GAS __attribute__((address_space(1)))
; template <bool GAIN, bool NT = false> __device__ __forceinline__ void titem8_store(const TItem& d, int lane, const f32x4 (&r)[16], const f32x4 (&g)[4]) {
;     const int q = lane & 7, kg = lane >> 3; const unsigned lo = (unsigned)((4 * q) * d.ldk + 16 * kg);
;     GAS char* base = (GAS char*)d.dst;
;     f32x4 s[16];
; #pragma unroll
;     for (int j = 0; j < 16; ++j) s[j] = r[j] * ((GAIN ? g[j >> 2][j & 3] : 1.0f) * W8_SCALE);
; #pragma unroll
;     for (int i = 0; i < 4; ++i) { v4u w;
;         w.x = pk4_fp8w(s[0][i], s[1][i], s[2][i], s[3][i]); w.y = pk4_fp8w(s[4][i], s[5][i], s[6][i], s[7][i]);
;         w.z = pk4_fp8w(s[8][i], s[9][i], s[10][i], s[11][i]); w.w = pk4_fp8w(s[12][i], s[13][i], s[14][i], s[15][i]);
;         GAS v4u* p = (GAS v4u*)(base + (size_t)i * (size_t)d.ldk + lo);
;         if (NT) __builtin_nontemporal_store(w, p); else *p = w; }
; }
	v_pk_mul_f32 v[66:67], v[66:67], s[30:31] op_sel_hi:[1,0]
	v_pk_mul_f32 v[68:69], v[68:69], s[30:31] op_sel_hi:[1,0]
	v_pk_mul_f32 v[70:71], v[70:71], s[30:31] op_sel_hi:[1,0]
	v_pk_mul_f32 v[72:73], v[72:73], s[30:31] op_sel_hi:[1,0]
	v_pk_mul_f32 v[74:75], v[74:75], s[30:31] op_sel_hi:[1,0]
	v_pk_mul_f32 v[76:77], v[76:77], s[30:31] op_sel_hi:[1,0]
	v_pk_mul_f32 v[78:79], v[78:79], s[30:31] op_sel_hi:[1,0]
	v_pk_mul_f32 v[80:81], v[80:81], s[30:31] op_sel_hi:[1,0]
	v_pk_mul_f32 v[82:83], v[82:83], s[30:31] op_sel_hi:[1,0]
	v_pk_mul_f32 v[84:85], v[84:85], s[30:31] op_sel_hi:[1,0]
	v_pk_mul_f32 v[86:87], v[86:87], s[30:31] op_sel_hi:[1,0]
	v_pk_mul_f32 v[88:89], v[88:89], s[30:31] op_sel_hi:[1,0]
	v_pk_mul_f32 v[90:91], v[90:91], s[30:31] op_sel_hi:[1,0]
	v_pk_mul_f32 v[92:93], v[92:93], s[30:31] op_sel_hi:[1,0]
	v_pk_mul_f32 v[94:95], v[94:95], s[30:31] op_sel_hi:[1,0]
	v_pk_mul_f32 v[96:97], v[96:97], s[30:31] op_sel_hi:[1,0]
	v_pk_mul_f32 v[98:99], v[98:99], s[30:31] op_sel_hi:[1,0]
	v_pk_mul_f32 v[100:101], v[100:101], s[30:31] op_sel_hi:[1,0]
	v_pk_mul_f32 v[102:103], v[102:103], s[30:31] op_sel_hi:[1,0]
	v_pk_mul_f32 v[104:105], v[104:105], s[30:31] op_sel_hi:[1,0]
	v_pk_mul_f32 v[106:107], v[106:107], s[30:31] op_sel_hi:[1,0]
	v_pk_mul_f32 v[108:109], v[108:109], s[30:31] op_sel_hi:[1,0]
	v_pk_mul_f32 v[110:111], v[110:111], s[30:31] op_sel_hi:[1,0]
	v_pk_mul_f32 v[112:113], v[112:113], s[30:31] op_sel_hi:[1,0]
	v_pk_mul_f32 v[114:115], v[114:115], s[30:31] op_sel_hi:[1,0]
	v_pk_mul_f32 v[116:117], v[116:117], s[30:31] op_sel_hi:[1,0]
	v_pk_mul_f32 v[118:119], v[118:119], s[30:31] op_sel_hi:[1,0]
	v_pk_mul_f32 v[120:121], v[120:121], s[30:31] op_sel_hi:[1,0]
	v_pk_mul_f32 v[122:123], v[122:123], s[30:31] op_sel_hi:[1,0]
	v_pk_mul_f32 v[124:125], v[124:125], s[30:31] op_sel_hi:[1,0]
	v_pk_mul_f32 v[126:127], v[126:127], s[30:31] op_sel_hi:[1,0]
	v_pk_mul_f32 v[128:129], v[128:129], s[30:31] op_sel_hi:[1,0]
	v_med3_f32 v66, v66, s24, v237
	v_med3_f32 v67, v67, s24, v237
	v_med3_f32 v68, v68, s24, v237
	v_med3_f32 v69, v69, s24, v237
	v_med3_f32 v70, v70, s24, v237
	v_med3_f32 v71, v71, s24, v237
	v_med3_f32 v72, v72, s24, v237
	v_med3_f32 v73, v73, s24, v237
	v_med3_f32 v74, v74, s24, v237
	v_med3_f32 v75, v75, s24, v237
	v_med3_f32 v76, v76, s24, v237
	v_med3_f32 v77, v77, s24, v237
	v_med3_f32 v78, v78, s24, v237
	v_med3_f32 v79, v79, s24, v237
	v_med3_f32 v80, v80, s24, v237
	v_med3_f32 v81, v81, s24, v237
	v_med3_f32 v82, v82, s24, v237
	v_med3_f32 v83, v83, s24, v237
	v_med3_f32 v84, v84, s24, v237
	v_med3_f32 v85, v85, s24, v237
	v_med3_f32 v86, v86, s24, v237
	v_med3_f32 v87, v87, s24, v237
	v_med3_f32 v88, v88, s24, v237
	v_med3_f32 v89, v89, s24, v237
	v_med3_f32 v90, v90, s24, v237
	v_med3_f32 v91, v91, s24, v237
	v_med3_f32 v92, v92, s24, v237
	v_med3_f32 v93, v93, s24, v237
	v_med3_f32 v94, v94, s24, v237
	v_med3_f32 v95, v95, s24, v237
	v_med3_f32 v96, v96, s24, v237
	v_med3_f32 v97, v97, s24, v237
	v_med3_f32 v98, v98, s24, v237
	v_med3_f32 v99, v99, s24, v237
	v_med3_f32 v100, v100, s24, v237
	v_med3_f32 v101, v101, s24, v237
	v_med3_f32 v102, v102, s24, v237
	v_med3_f32 v103, v103, s24, v237
	v_med3_f32 v104, v104, s24, v237
	v_med3_f32 v105, v105, s24, v237
	v_med3_f32 v106, v106, s24, v237
	v_med3_f32 v107, v107, s24, v237
	v_med3_f32 v108, v108, s24, v237
	v_med3_f32 v109, v109, s24, v237
	v_med3_f32 v110, v110, s24, v237
	v_med3_f32 v111, v111, s24, v237
	v_med3_f32 v112, v112, s24, v237
	v_med3_f32 v113, v113, s24, v237
	v_med3_f32 v114, v114, s24, v237
	v_med3_f32 v115, v115, s24, v237
	v_med3_f32 v116, v116, s24, v237
	v_med3_f32 v117, v117, s24, v237
	v_med3_f32 v118, v118, s24, v237
	v_med3_f32 v119, v119, s24, v237
	v_med3_f32 v120, v120, s24, v237
	v_med3_f32 v121, v121, s24, v237
	v_med3_f32 v122, v122, s24, v237
	v_med3_f32 v123, v123, s24, v237
	v_med3_f32 v124, v124, s24, v237
	v_med3_f32 v125, v125, s24, v237
	v_med3_f32 v126, v126, s24, v237
	v_med3_f32 v127, v127, s24, v237
	v_med3_f32 v128, v128, s24, v237
	v_med3_f32 v129, v129, s24, v237
	v_cvt_pk_fp8_f32 v66, v66, v70
	v_cvt_pk_fp8_f32 v66, v74, v78 op_sel:[0,0,1]
	v_cvt_pk_fp8_f32 v70, v67, v71
	v_cvt_pk_fp8_f32 v70, v75, v79 op_sel:[0,0,1]
	v_cvt_pk_fp8_f32 v74, v68, v72
	v_cvt_pk_fp8_f32 v74, v76, v80 op_sel:[0,0,1]
	v_cvt_pk_fp8_f32 v78, v69, v73
	v_cvt_pk_fp8_f32 v78, v77, v81 op_sel:[0,0,1]
	v_cvt_pk_fp8_f32 v67, v82, v86
	v_cvt_pk_fp8_f32 v67, v90, v94 op_sel:[0,0,1]
	v_cvt_pk_fp8_f32 v71, v83, v87
	v_cvt_pk_fp8_f32 v71, v91, v95 op_sel:[0,0,1]
	v_cvt_pk_fp8_f32 v75, v84, v88
	v_cvt_pk_fp8_f32 v75, v92, v96 op_sel:[0,0,1]
	v_cvt_pk_fp8_f32 v79, v85, v89
	v_cvt_pk_fp8_f32 v79, v93, v97 op_sel:[0,0,1]
	v_cvt_pk_fp8_f32 v68, v98, v102
	v_cvt_pk_fp8_f32 v68, v106, v110 op_sel:[0,0,1]
	v_cvt_pk_fp8_f32 v72, v99, v103
	v_cvt_pk_fp8_f32 v72, v107, v111 op_sel:[0,0,1]
	v_cvt_pk_fp8_f32 v76, v100, v104
	v_cvt_pk_fp8_f32 v76, v108, v112 op_sel:[0,0,1]
	v_cvt_pk_fp8_f32 v80, v101, v105
	v_cvt_pk_fp8_f32 v80, v109, v113 op_sel:[0,0,1]
	v_cvt_pk_fp8_f32 v69, v114, v118
	v_cvt_pk_fp8_f32 v69, v122, v126 op_sel:[0,0,1]
	v_cvt_pk_fp8_f32 v73, v115, v119
	v_cvt_pk_fp8_f32 v73, v123, v127 op_sel:[0,0,1]
	v_cvt_pk_fp8_f32 v77, v116, v120
	v_cvt_pk_fp8_f32 v77, v124, v128 op_sel:[0,0,1]
	v_cvt_pk_fp8_f32 v81, v117, v121
	v_cvt_pk_fp8_f32 v81, v125, v129 op_sel:[0,0,1]
	global_store_dwordx4 v250, v[66:69], s[42:43] nt
	global_store_dwordx4 v250, v[70:73], s[42:43] offset:2048 nt
	global_store_dwordx4 v251, v[74:77], s[42:43] nt
	global_store_dwordx4 v251, v[78:81], s[42:43] offset:2048 nt
	s_add_u32 s42, s42, 0x800000
	s_addc_u32 s43, s43, 0
	s_waitcnt vmcnt(24)
; #define GAS __attribute__((address_space(1)))
; template <bool GAIN, bool NT = false> __device__ __forceinline__ void titem8_store(const TItem& d, int lane, const f32x4 (&r)[16], const f32x4 (&g)[4]) {
;     const int q = lane & 7, kg = lane >> 3; const unsigned lo = (unsigned)((4 * q) * d.ldk + 16 * kg);
;     GAS char* base = (GAS char*)d.dst;
;     f32x4 s[16];
; #pragma unroll
;     for (int j = 0; j < 16; ++j) s[j] = r[j] * ((GAIN ? g[j >> 2][j & 3] : 1.0f) * W8_SCALE);
; #pragma unroll
;     for (int i = 0; i < 4; ++i) { v4u w;
;         w.x = pk4_fp8w(s[0][i], s[1][i], s[2][i], s[3][i]); w.y = pk4_fp8w(s[4][i], s[5][i], s[6][i], s[7][i]);
;         w.z = pk4_fp8w(s[8][i], s[9][i], s[10][i], s[11][i]); w.w = pk4_fp8w(s[12][i], s[13][i], s[14][i], s[15][i]);
;         GAS v4u* p = (GAS v4u*)(base + (size_t)i * (size_t)d.ldk + lo);
;         if (NT) __builtin_nontemporal_store(w, p); else *p = w; }
; }
	v_pk_mul_f32 v[130:131], v[130:131], s[30:31] op_sel_hi:[1,0]
	v_pk_mul_f32 v[132:133], v[132:133], s[30:31] op_sel_hi:[1,0]
	v_pk_mul_f32 v[134:135], v[134:135], s[30:31] op_sel_hi:[1,0]
	v_pk_mul_f32 v[136:137], v[136:137], s[30:31] op_sel_hi:[1,0]
	v_pk_mul_f32 v[138:139], v[138:139], s[30:31] op_sel_hi:[1,0]
	v_pk_mul_f32 v[140:141], v[140:141], s[30:31] op_sel_hi:[1,0]
	v_pk_mul_f32 v[142:143], v[142:143], s[30:31] op_sel_hi:[1,0]
	v_pk_mul_f32 v[144:145], v[144:145], s[30:31] op_sel_hi:[1,0]
	v_pk_mul_f32 v[146:147], v[146:147], s[30:31] op_sel_hi:[1,0]
	v_pk_mul_f32 v[148:149], v[148:149], s[30:31] op_sel_hi:[1,0]
	v_pk_mul_f32 v[150:151], v[150:151], s[30:31] op_sel_hi:[1,0]
	v_pk_mul_f32 v[152:153], v[152:153], s[30:31] op_sel_hi:[1,0]
	v_pk_mul_f32 v[154:155], v[154:155], s[30:31] op_sel_hi:[1,0]
	v_pk_mul_f32 v[156:157], v[156:157], s[30:31] op_sel_hi:[1,0]
	v_pk_mul_f32 v[158:159], v[158:159], s[30:31] op_sel_hi:[1,0]
	v_pk_mul_f32 v[160:161], v[160:161], s[30:31] op_sel_hi:[1,0]
	v_pk_mul_f32 v[162:163], v[162:163], s[30:31] op_sel_hi:[1,0]
	v_pk_mul_f32 v[164:165], v[164:165], s[30:31] op_sel_hi:[1,0]
	v_pk_mul_f32 v[166:167], v[166:167], s[30:31] op_sel_hi:[1,0]
	v_pk_mul_f32 v[168:169], v[168:169], s[30:31] op_sel_hi:[1,0]
	v_pk_mul_f32 v[170:171], v[170:171], s[30:31] op_sel_hi:[1,0]
	v_pk_mul_f32 v[172:173], v[172:173], s[30:31] op_sel_hi:[1,0]
	v_pk_mul_f32 v[174:175], v[174:175], s[30:31] op_sel_hi:[1,0]
	v_pk_mul_f32 v[176:177], v[176:177], s[30:31] op_sel_hi:[1,0]
	v_pk_mul_f32 v[178:179], v[178:179], s[30:31] op_sel_hi:[1,0]
	v_pk_mul_f32 v[180:181], v[180:181], s[30:31] op_sel_hi:[1,0]
	v_pk_mul_f32 v[182:183], v[182:183], s[30:31] op_sel_hi:[1,0]
	v_pk_mul_f32 v[184:185], v[184:185], s[30:31] op_sel_hi:[1,0]
	v_pk_mul_f32 v[186:187], v[186:187], s[30:31] op_sel_hi:[1,0]
	v_pk_mul_f32 v[188:189], v[188:189], s[30:31] op_sel_hi:[1,0]
	v_pk_mul_f32 v[190:191], v[190:191], s[30:31] op_sel_hi:[1,0]
	v_pk_mul_f32 v[192:193], v[192:193], s[30:31] op_sel_hi:[1,0]
	v_med3_f32 v130, v130, s24, v237
	v_med3_f32 v131, v131, s24, v237
	v_med3_f32 v132, v132, s24, v237
	v_med3_f32 v133, v133, s24, v237
	v_med3_f32 v134, v134, s24, v237
	v_med3_f32 v135, v135, s24, v237
	v_med3_f32 v136, v136, s24, v237
	v_med3_f32 v137, v137, s24, v237
	v_med3_f32 v138, v138, s24, v237
	v_med3_f32 v139, v139, s24, v237
	v_med3_f32 v140, v140, s24, v237
	v_med3_f32 v141, v141, s24, v237
	v_med3_f32 v142, v142, s24, v237
	v_med3_f32 v143, v143, s24, v237
	v_med3_f32 v144, v144, s24, v237
	v_med3_f32 v145, v145, s24, v237
	v_med3_f32 v146, v146, s24, v237
	v_med3_f32 v147, v147, s24, v237
	v_med3_f32 v148, v148, s24, v237
	v_med3_f32 v149, v149, s24, v237
	v_med3_f32 v150, v150, s24, v237
	v_med3_f32 v151, v151, s24, v237
	v_med3_f32 v152, v152, s24, v237
	v_med3_f32 v153, v153, s24, v237
	v_med3_f32 v154, v154, s24, v237
	v_med3_f32 v155, v155, s24, v237
	v_med3_f32 v156, v156, s24, v237
	v_med3_f32 v157, v157, s24, v237
	v_med3_f32 v158, v158, s24, v237
	v_med3_f32 v159, v159, s24, v237
	v_med3_f32 v160, v160, s24, v237
	v_med3_f32 v161, v161, s24, v237
	v_med3_f32 v162, v162, s24, v237
	v_med3_f32 v163, v163, s24, v237
	v_med3_f32 v164, v164, s24, v237
	v_med3_f32 v165, v165, s24, v237
	v_med3_f32 v166, v166, s24, v237
	v_med3_f32 v167, v167, s24, v237
	v_med3_f32 v168, v168, s24, v237
	v_med3_f32 v169, v169, s24, v237
	v_med3_f32 v170, v170, s24, v237
	v_med3_f32 v171, v171, s24, v237
	v_med3_f32 v172, v172, s24, v237
	v_med3_f32 v173, v173, s24, v237
	v_med3_f32 v174, v174, s24, v237
	v_med3_f32 v175, v175, s24, v237
	v_med3_f32 v176, v176, s24, v237
	v_med3_f32 v177, v177, s24, v237
	v_med3_f32 v178, v178, s24, v237
	v_med3_f32 v179, v179, s24, v237
	v_med3_f32 v180, v180, s24, v237
	v_med3_f32 v181, v181, s24, v237
	v_med3_f32 v182, v182, s24, v237
	v_med3_f32 v183, v183, s24, v237
	v_med3_f32 v184, v184, s24, v237
	v_med3_f32 v185, v185, s24, v237
	v_med3_f32 v186, v186, s24, v237
	v_med3_f32 v187, v187, s24, v237
	v_med3_f32 v188, v188, s24, v237
	v_med3_f32 v189, v189, s24, v237
	v_med3_f32 v190, v190, s24, v237
	v_med3_f32 v191, v191, s24, v237
	v_med3_f32 v192, v192, s24, v237
	v_med3_f32 v193, v193, s24, v237
	v_cvt_pk_fp8_f32 v130, v130, v134
	v_cvt_pk_fp8_f32 v130, v138, v142 op_sel:[0,0,1]
	v_cvt_pk_fp8_f32 v134, v131, v135
	v_cvt_pk_fp8_f32 v134, v139, v143 op_sel:[0,0,1]
	v_cvt_pk_fp8_f32 v138, v132, v136
	v_cvt_pk_fp8_f32 v138, v140, v144 op_sel:[0,0,1]
	v_cvt_pk_fp8_f32 v142, v133, v137
	v_cvt_pk_fp8_f32 v142, v141, v145 op_sel:[0,0,1]
	v_cvt_pk_fp8_f32 v131, v146, v150
	v_cvt_pk_fp8_f32 v131, v154, v158 op_sel:[0,0,1]
	v_cvt_pk_fp8_f32 v135, v147, v151
	v_cvt_pk_fp8_f32 v135, v155, v159 op_sel:[0,0,1]
	v_cvt_pk_fp8_f32 v139, v148, v152
	v_cvt_pk_fp8_f32 v139, v156, v160 op_sel:[0,0,1]
	v_cvt_pk_fp8_f32 v143, v149, v153
	v_cvt_pk_fp8_f32 v143, v157, v161 op_sel:[0,0,1]
	v_cvt_pk_fp8_f32 v132, v162, v166
	v_cvt_pk_fp8_f32 v132, v170, v174 op_sel:[0,0,1]
	v_cvt_pk_fp8_f32 v136, v163, v167
	v_cvt_pk_fp8_f32 v136, v171, v175 op_sel:[0,0,1]
	v_cvt_pk_fp8_f32 v140, v164, v168
	v_cvt_pk_fp8_f32 v140, v172, v176 op_sel:[0,0,1]
	v_cvt_pk_fp8_f32 v144, v165, v169
	v_cvt_pk_fp8_f32 v144, v173, v177 op_sel:[0,0,1]
	v_cvt_pk_fp8_f32 v133, v178, v182
	v_cvt_pk_fp8_f32 v133, v186, v190 op_sel:[0,0,1]
	v_cvt_pk_fp8_f32 v137, v179, v183
	v_cvt_pk_fp8_f32 v137, v187, v191 op_sel:[0,0,1]
	v_cvt_pk_fp8_f32 v141, v180, v184
	v_cvt_pk_fp8_f32 v141, v188, v192 op_sel:[0,0,1]
	v_cvt_pk_fp8_f32 v145, v181, v185
	v_cvt_pk_fp8_f32 v145, v189, v193 op_sel:[0,0,1]
	global_store_dwordx4 v250, v[130:133], s[42:43] nt
	global_store_dwordx4 v250, v[134:137], s[42:43] offset:2048 nt
	global_store_dwordx4 v251, v[138:141], s[42:43] nt
	global_store_dwordx4 v251, v[142:145], s[42:43] offset:2048 nt
	s_add_u32 s42, s42, 0x800000
	s_addc_u32 s43, s43, 0
	s_waitcnt vmcnt(8)
; #define GAS __attribute__((address_space(1)))
; template <bool GAIN, bool NT = false> __device__ __forceinline__ void titem8_store(const TItem& d, int lane, const f32x4 (&r)[16], const f32x4 (&g)[4]) {
;     const int q = lane & 7, kg = lane >> 3; const unsigned lo = (unsigned)((4 * q) * d.ldk + 16 * kg);
;     GAS char* base = (GAS char*)d.dst;
;     f32x4 s[16];
; #pragma unroll
;     for (int j = 0; j < 16; ++j) s[j] = r[j] * ((GAIN ? g[j >> 2][j & 3] : 1.0f) * W8_SCALE);
; #pragma unroll
;     for (int i = 0; i < 4; ++i) { v4u w;
;         w.x = pk4_fp8w(s[0][i], s[1][i], s[2][i], s[3][i]); w.y = pk4_fp8w(s[4][i], s[5][i], s[6][i], s[7][i]);
;         w.z = pk4_fp8w(s[8][i], s[9][i], s[10][i], s[11][i]); w.w = pk4_fp8w(s[12][i], s[13][i], s[14][i], s[15][i]);
;         GAS v4u* p = (GAS v4u*)(base + (size_t)i * (size_t)d.ldk + lo);
;         if (NT) __builtin_nontemporal_store(w, p); else *p = w; }
; }
	v_pk_mul_f32 v[0:1], v[0:1], s[30:31] op_sel_hi:[1,0]
	v_pk_mul_f32 v[2:3], v[2:3], s[30:31] op_sel_hi:[1,0]
	v_pk_mul_f32 v[4:5], v[4:5], s[30:31] op_sel_hi:[1,0]
	v_pk_mul_f32 v[6:7], v[6:7], s[30:31] op_sel_hi:[1,0]
	v_pk_mul_f32 v[8:9], v[8:9], s[30:31] op_sel_hi:[1,0]
	v_pk_mul_f32 v[10:11], v[10:11], s[30:31] op_sel_hi:[1,0]
	v_pk_mul_f32 v[12:13], v[12:13], s[30:31] op_sel_hi:[1,0]
	v_pk_mul_f32 v[14:15], v[14:15], s[30:31] op_sel_hi:[1,0]
	v_pk_mul_f32 v[16:17], v[16:17], s[30:31] op_sel_hi:[1,0]
	v_pk_mul_f32 v[18:19], v[18:19], s[30:31] op_sel_hi:[1,0]
	v_pk_mul_f32 v[20:21], v[20:21], s[30:31] op_sel_hi:[1,0]
	v_pk_mul_f32 v[22:23], v[22:23], s[30:31] op_sel_hi:[1,0]
	v_pk_mul_f32 v[24:25], v[24:25], s[30:31] op_sel_hi:[1,0]
	v_pk_mul_f32 v[26:27], v[26:27], s[30:31] op_sel_hi:[1,0]
	v_pk_mul_f32 v[28:29], v[28:29], s[30:31] op_sel_hi:[1,0]
	v_pk_mul_f32 v[30:31], v[30:31], s[30:31] op_sel_hi:[1,0]
	v_pk_mul_f32 v[32:33], v[32:33], s[30:31] op_sel_hi:[1,0]
	v_pk_mul_f32 v[34:35], v[34:35], s[30:31] op_sel_hi:[1,0]
	v_pk_mul_f32 v[36:37], v[36:37], s[30:31] op_sel_hi:[1,0]
	v_pk_mul_f32 v[38:39], v[38:39], s[30:31] op_sel_hi:[1,0]
	v_pk_mul_f32 v[40:41], v[40:41], s[30:31] op_sel_hi:[1,0]
	v_pk_mul_f32 v[42:43], v[42:43], s[30:31] op_sel_hi:[1,0]
	v_pk_mul_f32 v[44:45], v[44:45], s[30:31] op_sel_hi:[1,0]
	v_pk_mul_f32 v[46:47], v[46:47], s[30:31] op_sel_hi:[1,0]
	v_pk_mul_f32 v[48:49], v[48:49], s[30:31] op_sel_hi:[1,0]
	v_pk_mul_f32 v[50:51], v[50:51], s[30:31] op_sel_hi:[1,0]
	v_pk_mul_f32 v[52:53], v[52:53], s[30:31] op_sel_hi:[1,0]
	v_pk_mul_f32 v[54:55], v[54:55], s[30:31] op_sel_hi:[1,0]
	v_pk_mul_f32 v[56:57], v[56:57], s[30:31] op_sel_hi:[1,0]
	v_pk_mul_f32 v[58:59], v[58:59], s[30:31] op_sel_hi:[1,0]
	v_pk_mul_f32 v[60:61], v[60:61], s[30:31] op_sel_hi:[1,0]
	v_pk_mul_f32 v[62:63], v[62:63], s[30:31] op_sel_hi:[1,0]
	v_med3_f32 v0, v0, s24, v237
	v_med3_f32 v1, v1, s24, v237
	v_med3_f32 v2, v2, s24, v237
	v_med3_f32 v3, v3, s24, v237
	v_med3_f32 v4, v4, s24, v237
	v_med3_f32 v5, v5, s24, v237
	v_med3_f32 v6, v6, s24, v237
	v_med3_f32 v7, v7, s24, v237
	v_med3_f32 v8, v8, s24, v237
	v_med3_f32 v9, v9, s24, v237
	v_med3_f32 v10, v10, s24, v237
	v_med3_f32 v11, v11, s24, v237
	v_med3_f32 v12, v12, s24, v237
	v_med3_f32 v13, v13, s24, v237
	v_med3_f32 v14, v14, s24, v237
	v_med3_f32 v15, v15, s24, v237
	v_med3_f32 v16, v16, s24, v237
	v_med3_f32 v17, v17, s24, v237
	v_med3_f32 v18, v18, s24, v237
	v_med3_f32 v19, v19, s24, v237
	v_med3_f32 v20, v20, s24, v237
	v_med3_f32 v21, v21, s24, v237
	v_med3_f32 v22, v22, s24, v237
	v_med3_f32 v23, v23, s24, v237
	v_med3_f32 v24, v24, s24, v237
	v_med3_f32 v25, v25, s24, v237
	v_med3_f32 v26, v26, s24, v237
	v_med3_f32 v27, v27, s24, v237
	v_med3_f32 v28, v28, s24, v237
	v_med3_f32 v29, v29, s24, v237
	v_med3_f32 v30, v30, s24, v237
	v_med3_f32 v31, v31, s24, v237
	v_med3_f32 v32, v32, s24, v237
	v_med3_f32 v33, v33, s24, v237
	v_med3_f32 v34, v34, s24, v237
	v_med3_f32 v35, v35, s24, v237
	v_med3_f32 v36, v36, s24, v237
	v_med3_f32 v37, v37, s24, v237
	v_med3_f32 v38, v38, s24, v237
	v_med3_f32 v39, v39, s24, v237
	v_med3_f32 v40, v40, s24, v237
	v_med3_f32 v41, v41, s24, v237
	v_med3_f32 v42, v42, s24, v237
	v_med3_f32 v43, v43, s24, v237
	v_med3_f32 v44, v44, s24, v237
	v_med3_f32 v45, v45, s24, v237
	v_med3_f32 v46, v46, s24, v237
	v_med3_f32 v47, v47, s24, v237
	v_med3_f32 v48, v48, s24, v237
	v_med3_f32 v49, v49, s24, v237
	v_med3_f32 v50, v50, s24, v237
	v_med3_f32 v51, v51, s24, v237
	v_med3_f32 v52, v52, s24, v237
	v_med3_f32 v53, v53, s24, v237
	v_med3_f32 v54, v54, s24, v237
	v_med3_f32 v55, v55, s24, v237
	v_med3_f32 v56, v56, s24, v237
	v_med3_f32 v57, v57, s24, v237
	v_med3_f32 v58, v58, s24, v237
	v_med3_f32 v59, v59, s24, v237
	v_med3_f32 v60, v60, s24, v237
	v_med3_f32 v61, v61, s24, v237
	v_med3_f32 v62, v62, s24, v237
	v_med3_f32 v63, v63, s24, v237
	v_cvt_pk_fp8_f32 v0, v0, v4
	v_cvt_pk_fp8_f32 v0, v8, v12 op_sel:[0,0,1]
	v_cvt_pk_fp8_f32 v4, v1, v5
	v_cvt_pk_fp8_f32 v4, v9, v13 op_sel:[0,0,1]
	v_cvt_pk_fp8_f32 v8, v2, v6
	v_cvt_pk_fp8_f32 v8, v10, v14 op_sel:[0,0,1]
	v_cvt_pk_fp8_f32 v12, v3, v7
	v_cvt_pk_fp8_f32 v12, v11, v15 op_sel:[0,0,1]
	v_cvt_pk_fp8_f32 v1, v16, v20
	v_cvt_pk_fp8_f32 v1, v24, v28 op_sel:[0,0,1]
	v_cvt_pk_fp8_f32 v5, v17, v21
	v_cvt_pk_fp8_f32 v5, v25, v29 op_sel:[0,0,1]
	v_cvt_pk_fp8_f32 v9, v18, v22
	v_cvt_pk_fp8_f32 v9, v26, v30 op_sel:[0,0,1]
	v_cvt_pk_fp8_f32 v13, v19, v23
	v_cvt_pk_fp8_f32 v13, v27, v31 op_sel:[0,0,1]
	v_cvt_pk_fp8_f32 v2, v32, v36
	v_cvt_pk_fp8_f32 v2, v40, v44 op_sel:[0,0,1]
	v_cvt_pk_fp8_f32 v6, v33, v37
	v_cvt_pk_fp8_f32 v6, v41, v45 op_sel:[0,0,1]
	v_cvt_pk_fp8_f32 v10, v34, v38
	v_cvt_pk_fp8_f32 v10, v42, v46 op_sel:[0,0,1]
	v_cvt_pk_fp8_f32 v14, v35, v39
	v_cvt_pk_fp8_f32 v14, v43, v47 op_sel:[0,0,1]
	v_cvt_pk_fp8_f32 v3, v48, v52
	v_cvt_pk_fp8_f32 v3, v56, v60 op_sel:[0,0,1]
	v_cvt_pk_fp8_f32 v7, v49, v53
	v_cvt_pk_fp8_f32 v7, v57, v61 op_sel:[0,0,1]
	v_cvt_pk_fp8_f32 v11, v50, v54
	v_cvt_pk_fp8_f32 v11, v58, v62 op_sel:[0,0,1]
	v_cvt_pk_fp8_f32 v15, v51, v55
	v_cvt_pk_fp8_f32 v15, v59, v63 op_sel:[0,0,1]
	global_store_dwordx4 v250, v[0:3], s[42:43] nt
	global_store_dwordx4 v250, v[4:7], s[42:43] offset:2048 nt
	global_store_dwordx4 v251, v[8:11], s[42:43] nt
	global_store_dwordx4 v251, v[12:15], s[42:43] offset:2048 nt
	s_add_u32 s42, s42, 0x800000
	s_addc_u32 s43, s43, 0
	v_mov_b32_e32 v65, 0
